# s24
# baseline (speedup 1.0000x reference)
.LBB1_4:
	v_readfirstlane_b32 s0, v66
	v_add_u32_e32 v67, 0x2000, v66
	v_lshl_add_u64 v[68:69], s[4:5], 0, v[194:195]
	s_add_u32 m0, s0, 0x20000
	v_readfirstlane_b32 s0, v67
	v_add_u32_e32 v67, 0x4000, v66
	global_load_lds_dwordx4 v[68:69], off
	v_lshl_add_u64 v[70:71], v[68:69], 0, s[58:59]
	s_add_u32 m0, s0, 0x20000
	v_readfirstlane_b32 s0, v67
	v_add_u32_e32 v67, 0x6000, v66
	global_load_lds_dwordx4 v[70:71], off
	v_lshl_add_u64 v[70:71], v[68:69], 0, s[60:61]
	s_add_u32 m0, s0, 0x20000
	v_readfirstlane_b32 s0, v67
	global_load_lds_dwordx4 v[70:71], off
	v_lshl_add_u64 v[68:69], v[68:69], 0, s[62:63]
	s_add_u32 m0, s0, 0x20000
	v_mov_b32_e32 v94, v66
	global_load_lds_dwordx4 v[68:69], off
	s_waitcnt vmcnt(4)
.LBB1_5:
	v_lshlrev_b32_e32 v67, 4, v1
	v_lshrrev_b32_e32 v1, 1, v1
	v_lshrrev_b32_e32 v69, 5, v132
	v_ashrrev_i32_e32 v66, 4, v132
	v_bitop3_b32 v1, v1, v69, 7 bitop3:0x78
	s_add_u32 s22, s24, s2
	v_lshlrev_b32_e32 v68, 7, v66
	v_lshlrev_b32_e32 v1, 4, v1
	v_and_b32_e32 v0, 8, v0
	s_addc_u32 s90, s25, s3
	v_lshl_or_b32 v201, v66, 12, v67
	v_or3_b32 v0, v68, v1, v0
	v_add_u32_e32 v100, 0x10000, v0
	v_cvt_pk_f16_f32 v1, v64, v65
	v_cvt_pk_f16_f32 v0, v62, v63
	v_cvt_pk_f16_f32 v61, v60, v61
	v_cvt_pk_f16_f32 v60, v58, v59
	ds_write2st64_b64 v100, v[0:1], v[60:61] offset1:8
	v_cvt_pk_f16_f32 v1, v56, v57
	v_cvt_pk_f16_f32 v0, v54, v55
	v_cvt_pk_f16_f32 v53, v52, v53
	v_cvt_pk_f16_f32 v52, v50, v51
	ds_write2st64_b64 v100, v[0:1], v[52:53] offset0:16 offset1:24
	v_cvt_pk_f16_f32 v1, v48, v49
	v_cvt_pk_f16_f32 v0, v46, v47
	v_cvt_pk_f16_f32 v45, v44, v45
	v_cvt_pk_f16_f32 v44, v42, v43
	ds_write2st64_b64 v100, v[0:1], v[44:45] offset0:32 offset1:40
	v_cvt_pk_f16_f32 v1, v40, v41
	v_cvt_pk_f16_f32 v0, v38, v39
	v_cvt_pk_f16_f32 v37, v36, v37
	v_cvt_pk_f16_f32 v36, v34, v35
	ds_write2st64_b64 v100, v[0:1], v[36:37] offset0:48 offset1:56
	s_add_u32 s0, s22, 0x200
	s_addc_u32 s1, s90, 0
	s_add_u32 s70, s0, 0x20000
	s_addc_u32 s71, s1, 0
	s_add_u32 s72, s0, 0x40000
	s_addc_u32 s73, s1, 0
	s_add_u32 s92, s0, 0x60000
	s_addc_u32 s93, s1, 0
	s_add_u32 s94, s0, 0x80000
	s_addc_u32 s95, s1, 0
	s_add_u32 s96, s0, 0xa0000
	s_addc_u32 s97, s1, 0
	s_add_u32 s98, s0, 0xc0000
	s_addc_u32 s99, s1, 0
	s_add_u32 s80, s0, 0xe0000
	s_addc_u32 s81, s1, 0
	global_load_dwordx4 v[70:73], v201, s[0:1] nt
	global_load_dwordx4 v[42:45], v201, s[70:71] nt
	global_load_dwordx4 v[46:49], v201, s[72:73] nt
	global_load_dwordx4 v[66:69], v201, s[92:93] nt
	global_load_dwordx4 v[62:65], v201, s[94:95] nt
	global_load_dwordx4 v[58:61], v201, s[96:97] nt
	global_load_dwordx4 v[54:57], v201, s[98:99] nt
	global_load_dwordx4 v[50:53], v201, s[80:81] nt
	s_waitcnt vmcnt(8)
	s_waitcnt lgkmcnt(0)
	s_barrier
	v_add_u32_e32 v250, 0x20000, v129
	v_add_u32_e32 v251, 0x20000, v130
	ds_read_b128 v[34:37], v131
	ds_read_b128 v[38:41], v131 offset:2048
	ds_read_b128 v[74:77], v131 offset:4096
	ds_read_b128 v[78:81], v131 offset:6144
	ds_read_b128 v[82:85], v250
	ds_read_b128 v[86:89], v250 offset:2048
	s_add_u32 s70, s22, 0x300
	v_add_u32_e32 v95, 0x8000, v94
	v_lshl_add_u64 v[0:1], s[26:27], 0, v[196:197]
	s_addc_u32 s71, s90, 0
	v_readfirstlane_b32 s0, v95
	s_mov_b32 m0, s0
	v_cvt_pk_f16_f32 v33, v32, v33
	global_load_lds_dwordx4 v[0:1], off
	v_cvt_pk_f16_f32 v32, v30, v31
	ds_write_b64 v100, v[32:33] offset:32768
	global_load_dwordx4 v[30:33], v201, s[70:71] nt
	s_setprio 1
	s_waitcnt lgkmcnt(1)
	v_mfma_f32_16x16x32_f16 v[90:93], v[82:85], v[34:37], 0
	v_mfma_f32_16x16x32_f16 v[102:105], v[82:85], v[38:41], 0
	v_mfma_f32_16x16x32_f16 v[106:109], v[82:85], v[74:77], 0
	v_mfma_f32_16x16x32_f16 v[82:85], v[82:85], v[78:81], 0
	v_mfma_f32_16x16x32_f16 v[110:113], v[86:89], v[34:37], 0
	v_mfma_f32_16x16x32_f16 v[114:117], v[86:89], v[38:41], 0
	v_mfma_f32_16x16x32_f16 v[118:121], v[86:89], v[74:77], 0
	v_mfma_f32_16x16x32_f16 v[86:89], v[86:89], v[78:81], 0
	s_setprio 0
	ds_read_b128 v[122:125], v250 offset:4096
	ds_read_b128 v[134:137], v250 offset:6144
	v_add_u32_e32 v96, 0xa000, v94
	v_lshl_add_u64 v[98:99], v[0:1], 0, s[58:59]
	v_readfirstlane_b32 s1, v96
	s_mov_b32 m0, s1
	v_cvt_pk_f16_f32 v29, v28, v29
	global_load_lds_dwordx4 v[98:99], off
	v_cvt_pk_f16_f32 v28, v26, v27
	ds_write_b64 v100, v[28:29] offset:36864
	s_add_u32 s70, s22, 0x20300
	s_addc_u32 s71, s90, 0
	global_load_dwordx4 v[26:29], v201, s[70:71] nt
	s_setprio 1
	s_waitcnt lgkmcnt(1)
	v_mfma_f32_16x16x32_f16 v[138:141], v[122:125], v[34:37], 0
	v_mfma_f32_16x16x32_f16 v[142:145], v[122:125], v[38:41], 0
	v_mfma_f32_16x16x32_f16 v[146:149], v[122:125], v[74:77], 0
	v_mfma_f32_16x16x32_f16 v[122:125], v[122:125], v[78:81], 0
	v_mfma_f32_16x16x32_f16 v[150:153], v[134:137], v[34:37], 0
	v_mfma_f32_16x16x32_f16 v[154:157], v[134:137], v[38:41], 0
	v_mfma_f32_16x16x32_f16 v[158:161], v[134:137], v[74:77], 0
	v_mfma_f32_16x16x32_f16 v[134:137], v[134:137], v[78:81], 0
	s_setprio 0
	ds_read_b128 v[162:165], v250 offset:8192
	ds_read_b128 v[166:169], v250 offset:10240
	v_add_u32_e32 v97, 0xc000, v94
	v_lshl_add_u64 v[98:99], v[0:1], 0, s[60:61]
	v_readfirstlane_b32 s71, v97
	s_mov_b32 m0, s71
	v_cvt_pk_f16_f32 v25, v24, v25
	global_load_lds_dwordx4 v[98:99], off
	v_cvt_pk_f16_f32 v24, v22, v23
	ds_write_b64 v100, v[24:25] offset:40960
	s_add_u32 s72, s22, 0x40300
	s_addc_u32 s73, s90, 0
	global_load_dwordx4 v[22:25], v201, s[72:73] nt
	s_setprio 1
	s_waitcnt lgkmcnt(1)
	v_mfma_f32_16x16x32_f16 v[170:173], v[162:165], v[34:37], 0
	v_mfma_f32_16x16x32_f16 v[174:177], v[162:165], v[38:41], 0
	v_mfma_f32_16x16x32_f16 v[178:181], v[162:165], v[74:77], 0
	v_mfma_f32_16x16x32_f16 v[162:165], v[162:165], v[78:81], 0
	v_mfma_f32_16x16x32_f16 v[182:185], v[166:169], v[34:37], 0
	v_mfma_f32_16x16x32_f16 v[186:189], v[166:169], v[38:41], 0
	v_mfma_f32_16x16x32_f16 v[190:193], v[166:169], v[74:77], 0
	v_mfma_f32_16x16x32_f16 v[166:169], v[166:169], v[78:81], 0
	s_setprio 0
	ds_read_b128 v[202:205], v250 offset:12288
	ds_read_b128 v[206:209], v250 offset:14336
	v_add_u32_e32 v98, 0xe000, v94
	v_lshl_add_u64 v[0:1], v[0:1], 0, s[62:63]
	v_readfirstlane_b32 s72, v98
	s_mov_b32 m0, s72
	s_nop 0
	global_load_lds_dwordx4 v[0:1], off
	v_cvt_pk_f16_f32 v1, v20, v21
	v_cvt_pk_f16_f32 v0, v18, v19
	ds_write_b64 v100, v[0:1] offset:45056
	s_add_u32 s80, s22, 0x60300
	s_addc_u32 s81, s90, 0
	global_load_dwordx4 v[18:21], v201, s[80:81] nt
	s_setprio 1
	s_waitcnt lgkmcnt(1)
	v_mfma_f32_16x16x32_f16 v[210:213], v[202:205], v[34:37], 0
	v_mfma_f32_16x16x32_f16 v[214:217], v[202:205], v[38:41], 0
	v_mfma_f32_16x16x32_f16 v[218:221], v[202:205], v[74:77], 0
	v_mfma_f32_16x16x32_f16 v[202:205], v[202:205], v[78:81], 0
	v_mfma_f32_16x16x32_f16 v[74:77], v[206:209], v[74:77], 0
	v_mfma_f32_16x16x32_f16 v[78:81], v[206:209], v[78:81], 0
	v_mfma_f32_16x16x32_f16 v[222:225], v[206:209], v[34:37], 0
	v_mfma_f32_16x16x32_f16 v[226:229], v[206:209], v[38:41], 0
	s_setprio 0
	ds_read_b128 v[206:209], v128
	ds_read_b128 v[230:233], v128 offset:2048
	ds_read_b128 v[234:237], v128 offset:4096
	ds_read_b128 v[238:241], v128 offset:6144
	ds_read_b128 v[34:37], v251
	ds_read_b128 v[38:41], v251 offset:2048
	v_cvt_pk_f16_f32 v1, v16, v17
	v_cvt_pk_f16_f32 v0, v14, v15
	ds_write_b64 v100, v[0:1] offset:49152
	s_add_u32 s80, s22, 0x80300
	s_addc_u32 s81, s90, 0
	global_load_dwordx4 v[14:17], v201, s[80:81] nt
	s_setprio 1
	s_waitcnt lgkmcnt(1)
	v_mfma_f32_16x16x32_f16 v[90:93], v[34:37], v[206:209], v[90:93]
	v_mfma_f32_16x16x32_f16 v[102:105], v[34:37], v[230:233], v[102:105]
	v_mfma_f32_16x16x32_f16 v[106:109], v[34:37], v[234:237], v[106:109]
	v_mfma_f32_16x16x32_f16 v[82:85], v[34:37], v[238:241], v[82:85]
	v_mfma_f32_16x16x32_f16 v[110:113], v[38:41], v[206:209], v[110:113]
	v_mfma_f32_16x16x32_f16 v[114:117], v[38:41], v[230:233], v[114:117]
	v_mfma_f32_16x16x32_f16 v[118:121], v[38:41], v[234:237], v[118:121]
	v_mfma_f32_16x16x32_f16 v[86:89], v[38:41], v[238:241], v[86:89]
	s_setprio 0
	ds_read_b128 v[34:37], v251 offset:4096
	ds_read_b128 v[38:41], v251 offset:6144
	v_cvt_pk_f16_f32 v1, v12, v13
	v_cvt_pk_f16_f32 v0, v10, v11
	ds_write_b64 v100, v[0:1] offset:53248
	s_add_u32 s80, s22, 0xa0300
	s_addc_u32 s81, s90, 0
	global_load_dwordx4 v[10:13], v201, s[80:81] nt
	s_setprio 1
	s_waitcnt lgkmcnt(1)
	v_mfma_f32_16x16x32_f16 v[146:149], v[34:37], v[234:237], v[146:149]
	v_mfma_f32_16x16x32_f16 v[122:125], v[34:37], v[238:241], v[122:125]
	v_mfma_f32_16x16x32_f16 v[134:137], v[38:41], v[238:241], v[134:137]
	v_mfma_f32_16x16x32_f16 v[138:141], v[34:37], v[206:209], v[138:141]
	v_mfma_f32_16x16x32_f16 v[142:145], v[34:37], v[230:233], v[142:145]
	v_mfma_f32_16x16x32_f16 v[150:153], v[38:41], v[206:209], v[150:153]
	v_mfma_f32_16x16x32_f16 v[154:157], v[38:41], v[230:233], v[154:157]
	v_mfma_f32_16x16x32_f16 v[158:161], v[38:41], v[234:237], v[158:161]
	s_setprio 0
	ds_read_b128 v[38:41], v251 offset:8192
	ds_read_b128 v[242:245], v251 offset:10240
	v_cvt_pk_f16_f32 v1, v8, v9
	v_cvt_pk_f16_f32 v0, v6, v7
	ds_write_b64 v100, v[0:1] offset:57344
	s_add_u32 s80, s22, 0xc0300
	s_addc_u32 s81, s90, 0
	global_load_dwordx4 v[34:37], v201, s[80:81] nt
	s_setprio 1
	s_waitcnt lgkmcnt(1)
	v_mfma_f32_16x16x32_f16 v[6:9], v[38:41], v[206:209], v[170:173]
	v_mfma_f32_16x16x32_f16 v[170:173], v[38:41], v[230:233], v[174:177]
	v_mfma_f32_16x16x32_f16 v[174:177], v[38:41], v[234:237], v[178:181]
	v_mfma_f32_16x16x32_f16 v[162:165], v[38:41], v[238:241], v[162:165]
	v_mfma_f32_16x16x32_f16 v[178:181], v[242:245], v[206:209], v[182:185]
	v_mfma_f32_16x16x32_f16 v[182:185], v[242:245], v[230:233], v[186:189]
	v_mfma_f32_16x16x32_f16 v[186:189], v[242:245], v[234:237], v[190:193]
	v_mfma_f32_16x16x32_f16 v[166:169], v[242:245], v[238:241], v[166:169]
	s_setprio 0
	s_nop 0
	ds_read_b128 v[190:193], v251 offset:12288
	ds_read_b128 v[242:245], v251 offset:14336
	v_cvt_pk_f16_f32 v1, v4, v5
	v_cvt_pk_f16_f32 v0, v2, v3
	ds_write_b64 v100, v[0:1] offset:61440
	s_add_u32 s80, s22, 0xe0300
	s_addc_u32 s81, s90, 0
	global_load_dwordx4 v[38:41], v201, s[80:81] nt
	s_setprio 1
	s_waitcnt lgkmcnt(1)
	v_mfma_f32_16x16x32_f16 v[78:81], v[242:245], v[238:241], v[78:81]
	v_mfma_f32_16x16x32_f16 v[210:213], v[190:193], v[206:209], v[210:213]
	v_mfma_f32_16x16x32_f16 v[214:217], v[190:193], v[230:233], v[214:217]
	v_mfma_f32_16x16x32_f16 v[218:221], v[190:193], v[234:237], v[218:221]
	v_mfma_f32_16x16x32_f16 v[190:193], v[190:193], v[238:241], v[202:205]
	v_mfma_f32_16x16x32_f16 v[202:205], v[242:245], v[206:209], v[222:225]
	v_mfma_f32_16x16x32_f16 v[206:209], v[242:245], v[230:233], v[226:229]
	v_mfma_f32_16x16x32_f16 v[222:225], v[242:245], v[234:237], v[74:77]
	s_setprio 0
	s_waitcnt vmcnt(4)
	s_waitcnt lgkmcnt(0)
	s_barrier
	ds_read_b128 v[226:229], v131 offset:32768
	ds_read_b128 v[230:233], v131 offset:34816
	ds_read_b128 v[234:237], v131 offset:36864
	ds_read_b128 v[238:241], v131 offset:38912
	ds_read_b128 v[74:77], v129 offset:32768
	ds_read_b128 v[242:245], v129 offset:34816
	s_add_u32 s80, s22, 0x400
	s_addc_u32 s81, s90, 0
	v_lshl_add_u64 v[198:199], s[28:29], 0, v[196:197]
	v_readfirstlane_b32 s70, v94
	s_mov_b32 m0, s70
	v_cvt_pk_f16_f32 v1, v72, v73
	global_load_lds_dwordx4 v[198:199], off
	v_cvt_pk_f16_f32 v0, v70, v71
	ds_write_b64 v100, v[0:1]
	global_load_dwordx4 v[0:3], v201, s[80:81] nt
	s_setprio 1
	s_waitcnt lgkmcnt(1)
	v_mfma_f32_16x16x32_f16 v[70:73], v[74:77], v[226:229], v[90:93]
	v_mfma_f32_16x16x32_f16 v[90:93], v[74:77], v[230:233], v[102:105]
	v_mfma_f32_16x16x32_f16 v[104:107], v[74:77], v[234:237], v[106:109]
	v_mfma_f32_16x16x32_f16 v[82:85], v[74:77], v[238:241], v[82:85]
	v_mfma_f32_16x16x32_f16 v[108:111], v[242:245], v[226:229], v[110:113]
	v_mfma_f32_16x16x32_f16 v[112:115], v[242:245], v[230:233], v[114:117]
	v_mfma_f32_16x16x32_f16 v[116:119], v[242:245], v[234:237], v[118:121]
	v_mfma_f32_16x16x32_f16 v[86:89], v[242:245], v[238:241], v[86:89]
	s_setprio 0
	ds_read_b128 v[74:77], v129 offset:36864
	ds_read_b128 v[242:245], v129 offset:38912
	v_add_u32_e32 v99, 0x2000, v94
	v_lshl_add_u64 v[4:5], v[198:199], 0, s[58:59]
	v_readfirstlane_b32 s73, v99
	s_mov_b32 m0, s73
	s_nop 0
	global_load_lds_dwordx4 v[4:5], off
	v_cvt_pk_f16_f32 v5, v44, v45
	v_cvt_pk_f16_f32 v4, v42, v43
	ds_write_b64 v100, v[4:5] offset:4096
	s_add_u32 s80, s22, 0x20400
	s_addc_u32 s81, s90, 0
	global_load_dwordx4 v[42:45], v201, s[80:81] nt
	s_setprio 1
	s_waitcnt lgkmcnt(1)
	v_mfma_f32_16x16x32_f16 v[146:149], v[74:77], v[234:237], v[146:149]
	v_mfma_f32_16x16x32_f16 v[120:123], v[74:77], v[238:241], v[122:125]
	v_mfma_f32_16x16x32_f16 v[124:127], v[242:245], v[226:229], v[150:153]
	v_mfma_f32_16x16x32_f16 v[134:137], v[242:245], v[238:241], v[134:137]
	v_mfma_f32_16x16x32_f16 v[138:141], v[74:77], v[226:229], v[138:141]
	v_mfma_f32_16x16x32_f16 v[142:145], v[74:77], v[230:233], v[142:145]
	v_mfma_f32_16x16x32_f16 v[150:153], v[242:245], v[230:233], v[154:157]
	v_mfma_f32_16x16x32_f16 v[154:157], v[242:245], v[234:237], v[158:161]
	s_setprio 0
	ds_read_b128 v[74:77], v129 offset:40960
	s_nop 0
	ds_read_b128 v[158:161], v129 offset:43008
	v_add_u32_e32 v101, 0x4000, v94
	v_lshl_add_u64 v[4:5], v[198:199], 0, s[60:61]
	v_readfirstlane_b32 s91, v101
	s_mov_b32 m0, s91
	s_nop 0
	global_load_lds_dwordx4 v[4:5], off
	v_cvt_pk_f16_f32 v5, v48, v49
	v_cvt_pk_f16_f32 v4, v46, v47
	ds_write_b64 v100, v[4:5] offset:8192
	s_add_u32 s80, s22, 0x40400
	s_addc_u32 s81, s90, 0
	global_load_dwordx4 v[46:49], v201, s[80:81] nt
	s_setprio 1
	s_waitcnt lgkmcnt(1)
	v_mfma_f32_16x16x32_f16 v[4:7], v[74:77], v[226:229], v[6:9]
	v_mfma_f32_16x16x32_f16 v[170:173], v[74:77], v[230:233], v[170:173]
	v_mfma_f32_16x16x32_f16 v[174:177], v[74:77], v[234:237], v[174:177]
	v_mfma_f32_16x16x32_f16 v[162:165], v[74:77], v[238:241], v[162:165]
	v_mfma_f32_16x16x32_f16 v[178:181], v[158:161], v[226:229], v[178:181]
	v_mfma_f32_16x16x32_f16 v[182:185], v[158:161], v[230:233], v[182:185]
	v_mfma_f32_16x16x32_f16 v[186:189], v[158:161], v[234:237], v[186:189]
	v_mfma_f32_16x16x32_f16 v[158:161], v[158:161], v[238:241], v[166:169]
	s_setprio 0
	s_nop 1
	ds_read_b128 v[166:169], v129 offset:45056
	ds_read_b128 v[242:245], v129 offset:47104
	v_add_u32_e32 v102, 0x6000, v94
	v_lshl_add_u64 v[8:9], v[198:199], 0, s[62:63]
	v_readfirstlane_b32 s92, v102
	s_mov_b32 m0, s92
	s_nop 0
	global_load_lds_dwordx4 v[8:9], off
	v_cvt_pk_f16_f32 v9, v68, v69
	v_cvt_pk_f16_f32 v8, v66, v67
	ds_write_b64 v100, v[8:9] offset:12288
	s_add_u32 s80, s22, 0x60400
	s_addc_u32 s81, s90, 0
	global_load_dwordx4 v[74:77], v201, s[80:81] nt
	s_setprio 1
	s_waitcnt lgkmcnt(1)
	v_mfma_f32_16x16x32_f16 v[66:69], v[166:169], v[226:229], v[210:213]
	v_mfma_f32_16x16x32_f16 v[210:213], v[166:169], v[230:233], v[214:217]
	v_mfma_f32_16x16x32_f16 v[214:217], v[166:169], v[234:237], v[218:221]
	v_mfma_f32_16x16x32_f16 v[166:169], v[166:169], v[238:241], v[190:193]
	v_mfma_f32_16x16x32_f16 v[190:193], v[242:245], v[226:229], v[202:205]
	v_mfma_f32_16x16x32_f16 v[202:205], v[242:245], v[230:233], v[206:209]
	v_mfma_f32_16x16x32_f16 v[206:209], v[242:245], v[234:237], v[222:225]
	v_mfma_f32_16x16x32_f16 v[218:221], v[242:245], v[238:241], v[78:81]
	s_setprio 0
	s_nop 0
	ds_read_b128 v[222:225], v128 offset:32768
	ds_read_b128 v[226:229], v128 offset:34816
	ds_read_b128 v[230:233], v128 offset:36864
	ds_read_b128 v[234:237], v128 offset:38912
	ds_read_b128 v[238:241], v130 offset:32768
	ds_read_b128 v[242:245], v130 offset:34816
	v_cvt_pk_f16_f32 v9, v64, v65
	v_cvt_pk_f16_f32 v8, v62, v63
	ds_write_b64 v100, v[8:9] offset:16384
	s_add_u32 s80, s22, 0x80400
	s_addc_u32 s81, s90, 0
	global_load_dwordx4 v[78:81], v201, s[80:81] nt
	s_setprio 1
	s_waitcnt lgkmcnt(1)
	v_mfma_f32_16x16x32_f16 v[62:65], v[238:241], v[222:225], v[70:73]
	v_mfma_f32_16x16x32_f16 v[70:73], v[238:241], v[226:229], v[90:93]
	v_mfma_f32_16x16x32_f16 v[104:107], v[238:241], v[230:233], v[104:107]
	v_mfma_f32_16x16x32_f16 v[108:111], v[242:245], v[222:225], v[108:111]
	v_mfma_f32_16x16x32_f16 v[112:115], v[242:245], v[226:229], v[112:115]
	v_mfma_f32_16x16x32_f16 v[116:119], v[242:245], v[230:233], v[116:119]
	v_mfma_f32_16x16x32_f16 v[238:241], v[238:241], v[234:237], v[82:85]
	v_mfma_f32_16x16x32_f16 v[242:245], v[242:245], v[234:237], v[86:89]
	s_setprio 0
	s_nop 1
	ds_read_b128 v[86:89], v130 offset:36864
	ds_read_b128 v[90:93], v130 offset:38912
	v_cvt_pk_f16_f32 v9, v60, v61
	v_cvt_pk_f16_f32 v8, v58, v59
	ds_write_b64 v100, v[8:9] offset:20480
	s_add_u32 s80, s22, 0xa0400
	s_addc_u32 s81, s90, 0
	global_load_dwordx4 v[82:85], v201, s[80:81] nt
	s_setprio 1
	s_waitcnt lgkmcnt(1)
	v_mfma_f32_16x16x32_f16 v[58:61], v[86:89], v[222:225], v[138:141]
	v_mfma_f32_16x16x32_f16 v[138:141], v[86:89], v[226:229], v[142:145]
	v_mfma_f32_16x16x32_f16 v[142:145], v[86:89], v[230:233], v[146:149]
	v_mfma_f32_16x16x32_f16 v[120:123], v[86:89], v[234:237], v[120:123]
	v_mfma_f32_16x16x32_f16 v[124:127], v[90:93], v[222:225], v[124:127]
	v_mfma_f32_16x16x32_f16 v[146:149], v[90:93], v[226:229], v[150:153]
	v_mfma_f32_16x16x32_f16 v[134:137], v[90:93], v[234:237], v[134:137]
	v_mfma_f32_16x16x32_f16 v[150:153], v[90:93], v[230:233], v[154:157]
	s_setprio 0
	ds_read_b128 v[90:93], v130 offset:40960
	s_nop 0
	ds_read_b128 v[154:157], v130 offset:43008
	v_cvt_pk_f16_f32 v9, v56, v57
	v_cvt_pk_f16_f32 v8, v54, v55
	ds_write_b64 v100, v[8:9] offset:24576
	s_add_u32 s80, s22, 0xc0400
	s_addc_u32 s81, s90, 0
	global_load_dwordx4 v[86:89], v201, s[80:81] nt
	s_setprio 1
	s_waitcnt lgkmcnt(1)
	v_mfma_f32_16x16x32_f16 v[246:249], v[90:93], v[222:225], v[4:7]
	v_mfma_f32_16x16x32_f16 v[170:173], v[90:93], v[226:229], v[170:173]
	v_mfma_f32_16x16x32_f16 v[174:177], v[90:93], v[230:233], v[174:177]
	v_mfma_f32_16x16x32_f16 v[162:165], v[90:93], v[234:237], v[162:165]
	v_mfma_f32_16x16x32_f16 v[178:181], v[154:157], v[222:225], v[178:181]
	v_mfma_f32_16x16x32_f16 v[182:185], v[154:157], v[226:229], v[182:185]
	v_mfma_f32_16x16x32_f16 v[186:189], v[154:157], v[230:233], v[186:189]
	v_mfma_f32_16x16x32_f16 v[154:157], v[154:157], v[234:237], v[158:161]
	s_setprio 0
	ds_read_b128 v[4:7], v130 offset:45056
	ds_read_b128 v[54:57], v130 offset:47104
	v_cvt_pk_f16_f32 v9, v52, v53
	v_cvt_pk_f16_f32 v8, v50, v51
	ds_write_b64 v100, v[8:9] offset:28672
	s_add_u32 s80, s22, 0xe0400
	s_addc_u32 s81, s90, 0
	global_load_dwordx4 v[90:93], v201, s[80:81] nt
	s_setprio 1
	s_waitcnt lgkmcnt(1)
	v_mfma_f32_16x16x32_f16 v[66:69], v[4:7], v[222:225], v[66:69]
	v_mfma_f32_16x16x32_f16 v[158:161], v[4:7], v[226:229], v[210:213]
	v_mfma_f32_16x16x32_f16 v[210:213], v[4:7], v[230:233], v[214:217]
	v_mfma_f32_16x16x32_f16 v[166:169], v[4:7], v[234:237], v[166:169]
	v_mfma_f32_16x16x32_f16 v[190:193], v[54:57], v[222:225], v[190:193]
	v_mfma_f32_16x16x32_f16 v[202:205], v[54:57], v[226:229], v[202:205]
	v_mfma_f32_16x16x32_f16 v[206:209], v[54:57], v[230:233], v[206:209]
	v_mfma_f32_16x16x32_f16 v[214:217], v[54:57], v[234:237], v[218:221]
	s_setprio 0
	s_waitcnt vmcnt(4)
	s_waitcnt lgkmcnt(0)
	s_barrier
	s_nop 0
	ds_read_b128 v[218:221], v131
	ds_read_b128 v[222:225], v131 offset:2048
	ds_read_b128 v[226:229], v131 offset:4096
	ds_read_b128 v[230:233], v131 offset:6144
	ds_read_b128 v[50:53], v129
	ds_read_b128 v[54:57], v129 offset:2048
	s_add_u32 s80, s22, 0x500
	v_lshl_add_u64 v[8:9], s[30:31], 0, v[196:197]
	s_addc_u32 s81, s90, 0
	s_mov_b32 m0, s0
	v_cvt_pk_f16_f32 v5, v32, v33
	global_load_lds_dwordx4 v[8:9], off
	v_cvt_pk_f16_f32 v4, v30, v31
	ds_write_b64 v100, v[4:5] offset:32768
	global_load_dwordx4 v[4:7], v201, s[80:81] nt
	s_setprio 1
	s_waitcnt lgkmcnt(1)
	v_mfma_f32_16x16x32_f16 v[30:33], v[50:53], v[218:221], v[62:65]
	v_mfma_f32_16x16x32_f16 v[70:73], v[50:53], v[222:225], v[70:73]
	v_mfma_f32_16x16x32_f16 v[104:107], v[50:53], v[226:229], v[104:107]
	v_mfma_f32_16x16x32_f16 v[108:111], v[54:57], v[218:221], v[108:111]
	v_mfma_f32_16x16x32_f16 v[112:115], v[54:57], v[222:225], v[112:115]
	v_mfma_f32_16x16x32_f16 v[116:119], v[54:57], v[226:229], v[116:119]
	v_mfma_f32_16x16x32_f16 v[234:237], v[50:53], v[230:233], v[238:241]
	v_mfma_f32_16x16x32_f16 v[238:241], v[54:57], v[230:233], v[242:245]
	s_setprio 0
	ds_read_b128 v[54:57], v129 offset:4096
	ds_read_b128 v[62:65], v129 offset:6144
	s_mov_b32 m0, s1
	v_lshl_add_u64 v[50:51], v[8:9], 0, s[58:59]
	global_load_lds_dwordx4 v[50:51], off
	v_cvt_pk_f16_f32 v29, v28, v29
	v_cvt_pk_f16_f32 v28, v26, v27
	ds_write_b64 v100, v[28:29] offset:36864
	s_add_u32 s0, s22, 0x20500
	s_addc_u32 s1, s90, 0
	global_load_dwordx4 v[50:53], v201, s[0:1] nt
	s_setprio 1
	s_waitcnt lgkmcnt(1)
	v_mfma_f32_16x16x32_f16 v[26:29], v[54:57], v[218:221], v[58:61]
	v_mfma_f32_16x16x32_f16 v[120:123], v[54:57], v[230:233], v[120:123]
	v_mfma_f32_16x16x32_f16 v[124:127], v[62:65], v[218:221], v[124:127]
	v_mfma_f32_16x16x32_f16 v[146:149], v[62:65], v[222:225], v[146:149]
	v_mfma_f32_16x16x32_f16 v[134:137], v[62:65], v[230:233], v[134:137]
	v_mfma_f32_16x16x32_f16 v[138:141], v[54:57], v[222:225], v[138:141]
	v_mfma_f32_16x16x32_f16 v[142:145], v[54:57], v[226:229], v[142:145]
	v_mfma_f32_16x16x32_f16 v[150:153], v[62:65], v[226:229], v[150:153]
	s_setprio 0
	ds_read_b128 v[58:61], v129 offset:8192
	ds_read_b128 v[62:65], v129 offset:10240
	s_mov_b32 m0, s71
	v_lshl_add_u64 v[54:55], v[8:9], 0, s[60:61]
	global_load_lds_dwordx4 v[54:55], off
	v_cvt_pk_f16_f32 v25, v24, v25
	v_cvt_pk_f16_f32 v24, v22, v23
	ds_write_b64 v100, v[24:25] offset:40960
	s_add_u32 s0, s22, 0x40500
	s_addc_u32 s1, s90, 0
	global_load_dwordx4 v[54:57], v201, s[0:1] nt
	s_setprio 1
	s_waitcnt lgkmcnt(1)
	v_mfma_f32_16x16x32_f16 v[22:25], v[58:61], v[218:221], v[246:249]
	v_mfma_f32_16x16x32_f16 v[170:173], v[58:61], v[222:225], v[170:173]
	v_mfma_f32_16x16x32_f16 v[174:177], v[58:61], v[226:229], v[174:177]
	v_mfma_f32_16x16x32_f16 v[162:165], v[58:61], v[230:233], v[162:165]
	v_mfma_f32_16x16x32_f16 v[178:181], v[62:65], v[218:221], v[178:181]
	v_mfma_f32_16x16x32_f16 v[182:185], v[62:65], v[222:225], v[182:185]
	v_mfma_f32_16x16x32_f16 v[186:189], v[62:65], v[226:229], v[186:189]
	v_mfma_f32_16x16x32_f16 v[154:157], v[62:65], v[230:233], v[154:157]
	s_setprio 0
	ds_read_b128 v[62:65], v129 offset:12288
	ds_read_b128 v[242:245], v129 offset:14336
	s_mov_b32 m0, s72
	v_lshl_add_u64 v[8:9], v[8:9], 0, s[62:63]
	global_load_lds_dwordx4 v[8:9], off
	v_cvt_pk_f16_f32 v9, v20, v21
	v_cvt_pk_f16_f32 v8, v18, v19
	ds_write_b64 v100, v[8:9] offset:45056
	s_add_u32 s0, s22, 0x60500
	s_addc_u32 s1, s90, 0
	global_load_dwordx4 v[58:61], v201, s[0:1] nt
	s_setprio 1
	s_waitcnt lgkmcnt(1)
	v_mfma_f32_16x16x32_f16 v[18:21], v[62:65], v[218:221], v[66:69]
	v_mfma_f32_16x16x32_f16 v[158:161], v[62:65], v[222:225], v[158:161]
	v_mfma_f32_16x16x32_f16 v[210:213], v[62:65], v[226:229], v[210:213]
	v_mfma_f32_16x16x32_f16 v[166:169], v[62:65], v[230:233], v[166:169]
	v_mfma_f32_16x16x32_f16 v[190:193], v[242:245], v[218:221], v[190:193]
	v_mfma_f32_16x16x32_f16 v[202:205], v[242:245], v[222:225], v[202:205]
	v_mfma_f32_16x16x32_f16 v[206:209], v[242:245], v[226:229], v[206:209]
	v_mfma_f32_16x16x32_f16 v[214:217], v[242:245], v[230:233], v[214:217]
	s_setprio 0
	ds_read_b128 v[218:221], v128
	ds_read_b128 v[222:225], v128 offset:2048
	ds_read_b128 v[226:229], v128 offset:4096
	ds_read_b128 v[230:233], v128 offset:6144
	ds_read_b128 v[66:69], v130
	ds_read_b128 v[242:245], v130 offset:2048
	v_cvt_pk_f16_f32 v9, v16, v17
	v_cvt_pk_f16_f32 v8, v14, v15
	ds_write_b64 v100, v[8:9] offset:49152
	s_add_u32 s0, s22, 0x80500
	s_addc_u32 s1, s90, 0
	global_load_dwordx4 v[62:65], v201, s[0:1] nt
	s_setprio 1
	s_waitcnt lgkmcnt(1)
	v_mfma_f32_16x16x32_f16 v[14:17], v[66:69], v[218:221], v[30:33]
	v_mfma_f32_16x16x32_f16 v[30:33], v[66:69], v[222:225], v[70:73]
	v_mfma_f32_16x16x32_f16 v[104:107], v[66:69], v[226:229], v[104:107]
	v_mfma_f32_16x16x32_f16 v[108:111], v[242:245], v[218:221], v[108:111]
	v_mfma_f32_16x16x32_f16 v[112:115], v[242:245], v[222:225], v[112:115]
	v_mfma_f32_16x16x32_f16 v[116:119], v[242:245], v[226:229], v[116:119]
	v_mfma_f32_16x16x32_f16 v[234:237], v[66:69], v[230:233], v[234:237]
	v_mfma_f32_16x16x32_f16 v[238:241], v[242:245], v[230:233], v[238:241]
	s_setprio 0
	ds_read_b128 v[70:73], v130 offset:4096
	ds_read_b128 v[242:245], v130 offset:6144
	v_cvt_pk_f16_f32 v9, v12, v13
	v_cvt_pk_f16_f32 v8, v10, v11
	ds_write_b64 v100, v[8:9] offset:53248
	s_add_u32 s0, s22, 0xa0500
	s_addc_u32 s1, s90, 0
	global_load_dwordx4 v[66:69], v201, s[0:1] nt
	s_setprio 1
	s_waitcnt lgkmcnt(1)
	v_mfma_f32_16x16x32_f16 v[26:29], v[70:73], v[218:221], v[26:29]
	v_mfma_f32_16x16x32_f16 v[120:123], v[70:73], v[230:233], v[120:123]
	v_mfma_f32_16x16x32_f16 v[124:127], v[242:245], v[218:221], v[124:127]
	v_mfma_f32_16x16x32_f16 v[146:149], v[242:245], v[222:225], v[146:149]
	v_mfma_f32_16x16x32_f16 v[134:137], v[242:245], v[230:233], v[134:137]
	v_mfma_f32_16x16x32_f16 v[138:141], v[70:73], v[222:225], v[138:141]
	v_mfma_f32_16x16x32_f16 v[142:145], v[70:73], v[226:229], v[142:145]
	v_mfma_f32_16x16x32_f16 v[150:153], v[242:245], v[226:229], v[150:153]
	s_setprio 0
	ds_read_b128 v[8:11], v130 offset:8192
	ds_read_b128 v[242:245], v130 offset:10240
	v_cvt_pk_f16_f32 v13, v36, v37
	v_cvt_pk_f16_f32 v12, v34, v35
	ds_write_b64 v100, v[12:13] offset:57344
	s_add_u32 s0, s22, 0xc0500
	s_addc_u32 s1, s90, 0
	global_load_dwordx4 v[70:73], v201, s[0:1] nt
	s_setprio 1
	s_waitcnt lgkmcnt(1)
	v_mfma_f32_16x16x32_f16 v[22:25], v[8:11], v[218:221], v[22:25]
	v_mfma_f32_16x16x32_f16 v[170:173], v[8:11], v[222:225], v[170:173]
	v_mfma_f32_16x16x32_f16 v[174:177], v[8:11], v[226:229], v[174:177]
	v_mfma_f32_16x16x32_f16 v[162:165], v[8:11], v[230:233], v[162:165]
	v_mfma_f32_16x16x32_f16 v[178:181], v[242:245], v[218:221], v[178:181]
	v_mfma_f32_16x16x32_f16 v[182:185], v[242:245], v[222:225], v[182:185]
	v_mfma_f32_16x16x32_f16 v[186:189], v[242:245], v[226:229], v[186:189]
	v_mfma_f32_16x16x32_f16 v[154:157], v[242:245], v[230:233], v[154:157]
	s_setprio 0
	ds_read_b128 v[8:11], v130 offset:12288
	ds_read_b128 v[242:245], v130 offset:14336
	v_cvt_pk_f16_f32 v13, v40, v41
	v_cvt_pk_f16_f32 v12, v38, v39
	ds_write_b64 v100, v[12:13] offset:61440
	s_add_u32 s0, s22, 0xe0500
	s_addc_u32 s1, s90, 0
	global_load_dwordx4 v[36:39], v201, s[0:1] nt
	s_setprio 1
	s_waitcnt lgkmcnt(1)
	v_mfma_f32_16x16x32_f16 v[246:249], v[8:11], v[218:221], v[18:21]
	v_mfma_f32_16x16x32_f16 v[158:161], v[8:11], v[222:225], v[158:161]
	v_mfma_f32_16x16x32_f16 v[210:213], v[8:11], v[226:229], v[210:213]
	v_mfma_f32_16x16x32_f16 v[166:169], v[8:11], v[230:233], v[166:169]
	v_mfma_f32_16x16x32_f16 v[190:193], v[242:245], v[218:221], v[190:193]
	v_mfma_f32_16x16x32_f16 v[202:205], v[242:245], v[222:225], v[202:205]
	v_mfma_f32_16x16x32_f16 v[206:209], v[242:245], v[226:229], v[206:209]
	v_mfma_f32_16x16x32_f16 v[214:217], v[242:245], v[230:233], v[214:217]
	s_setprio 0
	s_waitcnt vmcnt(4)
	s_waitcnt lgkmcnt(0)
	s_barrier
	ds_read_b128 v[218:221], v131 offset:32768
	ds_read_b128 v[222:225], v131 offset:34816
	ds_read_b128 v[226:229], v131 offset:36864
	ds_read_b128 v[230:233], v131 offset:38912
	ds_read_b128 v[8:11], v129 offset:32768
	ds_read_b128 v[18:21], v129 offset:34816
	s_add_u32 s0, s22, 0x600
	s_addc_u32 s1, s90, 0
	v_lshl_add_u64 v[34:35], s[34:35], 0, v[196:197]
	s_mov_b32 m0, s70
	v_cvt_pk_f16_f32 v3, v2, v3
	global_load_lds_dwordx4 v[34:35], off
	v_cvt_pk_f16_f32 v2, v0, v1
	ds_write_b64 v100, v[2:3]
	global_load_dwordx4 v[0:3], v201, s[0:1] nt
	s_setprio 1
	s_waitcnt lgkmcnt(1)
	v_mfma_f32_16x16x32_f16 v[30:33], v[8:11], v[222:225], v[30:33]
	v_mfma_f32_16x16x32_f16 v[104:107], v[8:11], v[226:229], v[104:107]
	v_mfma_f32_16x16x32_f16 v[108:111], v[18:21], v[218:221], v[108:111]
	v_mfma_f32_16x16x32_f16 v[112:115], v[18:21], v[222:225], v[112:115]
	v_mfma_f32_16x16x32_f16 v[116:119], v[18:21], v[226:229], v[116:119]
	v_mfma_f32_16x16x32_f16 v[242:245], v[8:11], v[218:221], v[14:17]
	v_mfma_f32_16x16x32_f16 v[234:237], v[8:11], v[230:233], v[234:237]
	v_mfma_f32_16x16x32_f16 v[238:241], v[18:21], v[230:233], v[238:241]
	s_setprio 0
	ds_read_b128 v[12:15], v129 offset:36864
	ds_read_b128 v[16:19], v129 offset:38912
	s_mov_b32 m0, s73
	v_lshl_add_u64 v[8:9], v[34:35], 0, s[58:59]
	global_load_lds_dwordx4 v[8:9], off
	v_cvt_pk_f16_f32 v9, v44, v45
	v_cvt_pk_f16_f32 v8, v42, v43
	ds_write_b64 v100, v[8:9] offset:4096
	s_add_u32 s0, s22, 0x20600
	s_addc_u32 s1, s90, 0
	global_load_dwordx4 v[8:11], v201, s[0:1] nt
	s_setprio 1
	s_waitcnt lgkmcnt(1)
	v_mfma_f32_16x16x32_f16 v[40:43], v[12:15], v[218:221], v[26:29]
	v_mfma_f32_16x16x32_f16 v[120:123], v[12:15], v[230:233], v[120:123]
	v_mfma_f32_16x16x32_f16 v[124:127], v[16:19], v[218:221], v[124:127]
	v_mfma_f32_16x16x32_f16 v[146:149], v[16:19], v[222:225], v[146:149]
	v_mfma_f32_16x16x32_f16 v[134:137], v[16:19], v[230:233], v[134:137]
	v_mfma_f32_16x16x32_f16 v[138:141], v[12:15], v[222:225], v[138:141]
	v_mfma_f32_16x16x32_f16 v[142:145], v[12:15], v[226:229], v[142:145]
	v_mfma_f32_16x16x32_f16 v[150:153], v[16:19], v[226:229], v[150:153]
	s_setprio 0
	ds_read_b128 v[16:19], v129 offset:40960
	ds_read_b128 v[26:29], v129 offset:43008
	s_mov_b32 m0, s91
	v_lshl_add_u64 v[12:13], v[34:35], 0, s[60:61]
	global_load_lds_dwordx4 v[12:13], off
	v_cvt_pk_f16_f32 v13, v48, v49
	v_cvt_pk_f16_f32 v12, v46, v47
	ds_write_b64 v100, v[12:13] offset:8192
	s_add_u32 s0, s22, 0x40600
	s_addc_u32 s1, s90, 0
	global_load_dwordx4 v[12:15], v201, s[0:1] nt
	s_setprio 1
	s_waitcnt lgkmcnt(1)
	v_mfma_f32_16x16x32_f16 v[44:47], v[16:19], v[218:221], v[22:25]
	v_mfma_f32_16x16x32_f16 v[170:173], v[16:19], v[222:225], v[170:173]
	v_mfma_f32_16x16x32_f16 v[174:177], v[16:19], v[226:229], v[174:177]
	v_mfma_f32_16x16x32_f16 v[162:165], v[16:19], v[230:233], v[162:165]
	v_mfma_f32_16x16x32_f16 v[178:181], v[26:29], v[218:221], v[178:181]
	v_mfma_f32_16x16x32_f16 v[182:185], v[26:29], v[222:225], v[182:185]
	v_mfma_f32_16x16x32_f16 v[186:189], v[26:29], v[226:229], v[186:189]
	v_mfma_f32_16x16x32_f16 v[154:157], v[26:29], v[230:233], v[154:157]
	s_setprio 0
	ds_read_b128 v[20:23], v129 offset:45056
	ds_read_b128 v[24:27], v129 offset:47104
	s_mov_b32 m0, s92
	v_lshl_add_u64 v[16:17], v[34:35], 0, s[62:63]
	global_load_lds_dwordx4 v[16:17], off
	v_cvt_pk_f16_f32 v17, v76, v77
	v_cvt_pk_f16_f32 v16, v74, v75
	ds_write_b64 v100, v[16:17] offset:12288
	s_add_u32 s0, s22, 0x60600
	s_addc_u32 s1, s90, 0
	global_load_dwordx4 v[16:19], v201, s[0:1] nt
	s_setprio 1
	s_waitcnt lgkmcnt(1)
	v_mfma_f32_16x16x32_f16 v[74:77], v[20:23], v[218:221], v[246:249]
	v_mfma_f32_16x16x32_f16 v[158:161], v[20:23], v[222:225], v[158:161]
	v_mfma_f32_16x16x32_f16 v[210:213], v[20:23], v[226:229], v[210:213]
	v_mfma_f32_16x16x32_f16 v[166:169], v[20:23], v[230:233], v[166:169]
	v_mfma_f32_16x16x32_f16 v[190:193], v[24:27], v[218:221], v[190:193]
	v_mfma_f32_16x16x32_f16 v[202:205], v[24:27], v[222:225], v[202:205]
	v_mfma_f32_16x16x32_f16 v[206:209], v[24:27], v[226:229], v[206:209]
	v_mfma_f32_16x16x32_f16 v[214:217], v[24:27], v[230:233], v[214:217]
	s_setprio 0
	ds_read_b128 v[218:221], v128 offset:32768
	ds_read_b128 v[222:225], v128 offset:34816
	ds_read_b128 v[226:229], v128 offset:36864
	ds_read_b128 v[230:233], v128 offset:38912
	ds_read_b128 v[24:27], v130 offset:32768
	ds_read_b128 v[246:249], v130 offset:34816
	v_cvt_pk_f16_f32 v21, v80, v81
	v_cvt_pk_f16_f32 v20, v78, v79
	ds_write_b64 v100, v[20:21] offset:16384
	s_add_u32 s0, s22, 0x80600
	s_addc_u32 s1, s90, 0
	global_load_dwordx4 v[20:23], v201, s[0:1] nt
	s_setprio 1
	s_waitcnt lgkmcnt(1)
	v_mfma_f32_16x16x32_f16 v[78:81], v[24:27], v[218:221], v[242:245]
	v_mfma_f32_16x16x32_f16 v[104:107], v[24:27], v[226:229], v[104:107]
	v_mfma_f32_16x16x32_f16 v[108:111], v[246:249], v[218:221], v[108:111]
	v_mfma_f32_16x16x32_f16 v[112:115], v[246:249], v[222:225], v[112:115]
	v_mfma_f32_16x16x32_f16 v[116:119], v[246:249], v[226:229], v[116:119]
	v_mfma_f32_16x16x32_f16 v[242:245], v[24:27], v[222:225], v[30:33]
	v_mfma_f32_16x16x32_f16 v[234:237], v[24:27], v[230:233], v[234:237]
	v_mfma_f32_16x16x32_f16 v[238:241], v[246:249], v[230:233], v[238:241]
	s_setprio 0
	ds_read_b128 v[28:31], v130 offset:36864
	ds_read_b128 v[32:35], v130 offset:38912
	v_cvt_pk_f16_f32 v25, v84, v85
	v_cvt_pk_f16_f32 v24, v82, v83
	ds_write_b64 v100, v[24:25] offset:20480
	s_add_u32 s0, s22, 0xa0600
	s_addc_u32 s1, s90, 0
	global_load_dwordx4 v[24:27], v201, s[0:1] nt
	s_setprio 1
	s_waitcnt lgkmcnt(1)
	v_mfma_f32_16x16x32_f16 v[82:85], v[28:31], v[218:221], v[40:43]
	v_mfma_f32_16x16x32_f16 v[120:123], v[28:31], v[230:233], v[120:123]
	v_mfma_f32_16x16x32_f16 v[124:127], v[32:35], v[218:221], v[124:127]
	v_mfma_f32_16x16x32_f16 v[146:149], v[32:35], v[222:225], v[146:149]
	v_mfma_f32_16x16x32_f16 v[134:137], v[32:35], v[230:233], v[134:137]
	v_mfma_f32_16x16x32_f16 v[138:141], v[28:31], v[222:225], v[138:141]
	v_mfma_f32_16x16x32_f16 v[142:145], v[28:31], v[226:229], v[142:145]
	v_mfma_f32_16x16x32_f16 v[150:153], v[32:35], v[226:229], v[150:153]
	s_setprio 0
	ds_read_b128 v[32:35], v130 offset:40960
	ds_read_b128 v[40:43], v130 offset:43008
	v_cvt_pk_f16_f32 v29, v88, v89
	v_cvt_pk_f16_f32 v28, v86, v87
	ds_write_b64 v100, v[28:29] offset:24576
	s_add_u32 s0, s22, 0xc0600
	s_addc_u32 s1, s90, 0
	global_load_dwordx4 v[28:31], v201, s[0:1] nt
	s_setprio 1
	s_waitcnt lgkmcnt(1)
	v_mfma_f32_16x16x32_f16 v[86:89], v[32:35], v[218:221], v[44:47]
	v_mfma_f32_16x16x32_f16 v[170:173], v[32:35], v[222:225], v[170:173]
	v_mfma_f32_16x16x32_f16 v[174:177], v[32:35], v[226:229], v[174:177]
	v_mfma_f32_16x16x32_f16 v[162:165], v[32:35], v[230:233], v[162:165]
	v_mfma_f32_16x16x32_f16 v[178:181], v[40:43], v[218:221], v[178:181]
	v_mfma_f32_16x16x32_f16 v[182:185], v[40:43], v[222:225], v[182:185]
	v_mfma_f32_16x16x32_f16 v[186:189], v[40:43], v[226:229], v[186:189]
	v_mfma_f32_16x16x32_f16 v[154:157], v[40:43], v[230:233], v[154:157]
	s_setprio 0
	ds_read_b128 v[40:43], v130 offset:45056
	ds_read_b128 v[44:47], v130 offset:47104
	v_cvt_pk_f16_f32 v33, v92, v93
	v_cvt_pk_f16_f32 v32, v90, v91
	ds_write_b64 v100, v[32:33] offset:28672
	s_add_u32 s0, s22, 0xe0600
	s_addc_u32 s1, s90, 0
	global_load_dwordx4 v[32:35], v201, s[0:1] nt
	s_setprio 1
	s_waitcnt lgkmcnt(1)
	v_mfma_f32_16x16x32_f16 v[74:77], v[40:43], v[218:221], v[74:77]
	v_mfma_f32_16x16x32_f16 v[90:93], v[40:43], v[222:225], v[158:161]
	v_mfma_f32_16x16x32_f16 v[158:161], v[40:43], v[226:229], v[210:213]
	v_mfma_f32_16x16x32_f16 v[166:169], v[40:43], v[230:233], v[166:169]
	v_mfma_f32_16x16x32_f16 v[190:193], v[44:47], v[218:221], v[190:193]
	v_mfma_f32_16x16x32_f16 v[202:205], v[44:47], v[222:225], v[202:205]
	v_mfma_f32_16x16x32_f16 v[206:209], v[44:47], v[226:229], v[206:209]
	v_mfma_f32_16x16x32_f16 v[210:213], v[44:47], v[230:233], v[214:217]
	s_setprio 0
	s_waitcnt vmcnt(4)
	s_waitcnt lgkmcnt(0)
	s_barrier
	s_nop 0
	ds_read_b128 v[214:217], v131
	ds_read_b128 v[218:221], v131 offset:2048
	ds_read_b128 v[222:225], v131 offset:4096
	ds_read_b128 v[226:229], v131 offset:6144
	ds_read_b128 v[40:43], v129
	ds_read_b128 v[44:47], v129 offset:2048
	s_add_u32 s70, s22, 0x700
	s_addc_u32 s71, s90, 0
	v_lshl_add_u64 v[198:199], s[36:37], 0, v[196:197]
	v_readfirstlane_b32 s0, v95
	s_mov_b32 m0, s0
	v_cvt_pk_f16_f32 v7, v6, v7
	global_load_lds_dwordx4 v[198:199], off
	v_cvt_pk_f16_f32 v6, v4, v5
	ds_write_b64 v100, v[6:7] offset:32768
	global_load_dwordx4 v[4:7], v201, s[70:71] nt
	s_setprio 1
	s_waitcnt lgkmcnt(1)
	v_mfma_f32_16x16x32_f16 v[78:81], v[40:43], v[214:217], v[78:81]
	v_mfma_f32_16x16x32_f16 v[104:107], v[40:43], v[222:225], v[104:107]
	v_mfma_f32_16x16x32_f16 v[108:111], v[44:47], v[214:217], v[108:111]
	v_mfma_f32_16x16x32_f16 v[112:115], v[44:47], v[218:221], v[112:115]
	v_mfma_f32_16x16x32_f16 v[116:119], v[44:47], v[222:225], v[116:119]
	v_mfma_f32_16x16x32_f16 v[230:233], v[40:43], v[218:221], v[242:245]
	v_mfma_f32_16x16x32_f16 v[234:237], v[40:43], v[226:229], v[234:237]
	v_mfma_f32_16x16x32_f16 v[238:241], v[44:47], v[226:229], v[238:241]
	s_setprio 0
	ds_read_b128 v[44:47], v129 offset:4096
	ds_read_b128 v[242:245], v129 offset:6144
	v_readfirstlane_b32 s72, v96
	v_lshl_add_u64 v[40:41], v[198:199], 0, s[58:59]
	s_mov_b32 m0, s72
	s_nop 0
	global_load_lds_dwordx4 v[40:41], off
	v_cvt_pk_f16_f32 v41, v52, v53
	v_cvt_pk_f16_f32 v40, v50, v51
	ds_write_b64 v100, v[40:41] offset:36864
	s_add_u32 s70, s22, 0x20700
	s_addc_u32 s71, s90, 0
	global_load_dwordx4 v[40:43], v201, s[70:71] nt
	s_setprio 1
	s_waitcnt lgkmcnt(1)
	v_mfma_f32_16x16x32_f16 v[82:85], v[44:47], v[214:217], v[82:85]
	v_mfma_f32_16x16x32_f16 v[120:123], v[44:47], v[226:229], v[120:123]
	v_mfma_f32_16x16x32_f16 v[124:127], v[242:245], v[214:217], v[124:127]
	v_mfma_f32_16x16x32_f16 v[146:149], v[242:245], v[218:221], v[146:149]
	v_mfma_f32_16x16x32_f16 v[134:137], v[242:245], v[226:229], v[134:137]
	v_mfma_f32_16x16x32_f16 v[138:141], v[44:47], v[218:221], v[138:141]
	v_mfma_f32_16x16x32_f16 v[142:145], v[44:47], v[222:225], v[142:145]
	v_mfma_f32_16x16x32_f16 v[150:153], v[242:245], v[222:225], v[150:153]
	s_setprio 0
	ds_read_b128 v[48:51], v129 offset:8192
	ds_read_b128 v[242:245], v129 offset:10240
	v_readfirstlane_b32 s71, v97
	v_lshl_add_u64 v[44:45], v[198:199], 0, s[60:61]
	s_mov_b32 m0, s71
	s_nop 0
	global_load_lds_dwordx4 v[44:45], off
	v_cvt_pk_f16_f32 v45, v56, v57
	v_cvt_pk_f16_f32 v44, v54, v55
	ds_write_b64 v100, v[44:45] offset:40960
	s_add_u32 s80, s22, 0x40700
	s_addc_u32 s81, s90, 0
	global_load_dwordx4 v[44:47], v201, s[80:81] nt
	s_setprio 1
	s_waitcnt lgkmcnt(1)
	v_mfma_f32_16x16x32_f16 v[86:89], v[48:51], v[214:217], v[86:89]
	v_mfma_f32_16x16x32_f16 v[170:173], v[48:51], v[218:221], v[170:173]
	v_mfma_f32_16x16x32_f16 v[174:177], v[48:51], v[222:225], v[174:177]
	v_mfma_f32_16x16x32_f16 v[162:165], v[48:51], v[226:229], v[162:165]
	v_mfma_f32_16x16x32_f16 v[178:181], v[242:245], v[214:217], v[178:181]
	v_mfma_f32_16x16x32_f16 v[182:185], v[242:245], v[218:221], v[182:185]
	v_mfma_f32_16x16x32_f16 v[186:189], v[242:245], v[222:225], v[186:189]
	v_mfma_f32_16x16x32_f16 v[154:157], v[242:245], v[226:229], v[154:157]
	s_setprio 0
	ds_read_b128 v[52:55], v129 offset:12288
	ds_read_b128 v[242:245], v129 offset:14336
	v_readfirstlane_b32 s70, v98
	v_lshl_add_u64 v[48:49], v[198:199], 0, s[62:63]
	s_mov_b32 m0, s70
	s_nop 0
	global_load_lds_dwordx4 v[48:49], off
	v_cvt_pk_f16_f32 v49, v60, v61
	v_cvt_pk_f16_f32 v48, v58, v59
	ds_write_b64 v100, v[48:49] offset:45056
	s_add_u32 s80, s22, 0x60700
	s_addc_u32 s81, s90, 0
	global_load_dwordx4 v[48:51], v201, s[80:81] nt
	s_setprio 1
	s_waitcnt lgkmcnt(1)
	v_mfma_f32_16x16x32_f16 v[74:77], v[52:55], v[214:217], v[74:77]
	v_mfma_f32_16x16x32_f16 v[90:93], v[52:55], v[218:221], v[90:93]
	v_mfma_f32_16x16x32_f16 v[158:161], v[52:55], v[222:225], v[158:161]
	v_mfma_f32_16x16x32_f16 v[166:169], v[52:55], v[226:229], v[166:169]
	v_mfma_f32_16x16x32_f16 v[190:193], v[242:245], v[214:217], v[190:193]
	v_mfma_f32_16x16x32_f16 v[202:205], v[242:245], v[218:221], v[202:205]
	v_mfma_f32_16x16x32_f16 v[206:209], v[242:245], v[222:225], v[206:209]
	v_mfma_f32_16x16x32_f16 v[210:213], v[242:245], v[226:229], v[210:213]
	s_setprio 0
	ds_read_b128 v[214:217], v128
	ds_read_b128 v[218:221], v128 offset:2048
	ds_read_b128 v[222:225], v128 offset:4096
	ds_read_b128 v[226:229], v128 offset:6144
	ds_read_b128 v[56:59], v130
	ds_read_b128 v[242:245], v130 offset:2048
	v_cvt_pk_f16_f32 v53, v64, v65
	v_cvt_pk_f16_f32 v52, v62, v63
	ds_write_b64 v100, v[52:53] offset:49152
	s_add_u32 s80, s22, 0x80700
	s_addc_u32 s81, s90, 0
	global_load_dwordx4 v[52:55], v201, s[80:81] nt
	s_setprio 1
	s_waitcnt lgkmcnt(1)
	v_mfma_f32_16x16x32_f16 v[78:81], v[56:59], v[214:217], v[78:81]
	v_mfma_f32_16x16x32_f16 v[104:107], v[56:59], v[222:225], v[104:107]
	v_mfma_f32_16x16x32_f16 v[108:111], v[242:245], v[214:217], v[108:111]
	v_mfma_f32_16x16x32_f16 v[112:115], v[242:245], v[218:221], v[112:115]
	v_mfma_f32_16x16x32_f16 v[116:119], v[242:245], v[222:225], v[116:119]
	v_mfma_f32_16x16x32_f16 v[230:233], v[56:59], v[218:221], v[230:233]
	v_mfma_f32_16x16x32_f16 v[234:237], v[56:59], v[226:229], v[234:237]
	v_mfma_f32_16x16x32_f16 v[238:241], v[242:245], v[226:229], v[238:241]
	s_setprio 0
	ds_read_b128 v[60:63], v130 offset:4096
	ds_read_b128 v[242:245], v130 offset:6144
	v_cvt_pk_f16_f32 v57, v68, v69
	v_cvt_pk_f16_f32 v56, v66, v67
	ds_write_b64 v100, v[56:57] offset:53248
	s_add_u32 s80, s22, 0xa0700
	s_addc_u32 s81, s90, 0
	global_load_dwordx4 v[56:59], v201, s[80:81] nt
	s_setprio 1
	s_waitcnt lgkmcnt(1)
	v_mfma_f32_16x16x32_f16 v[82:85], v[60:63], v[214:217], v[82:85]
	v_mfma_f32_16x16x32_f16 v[120:123], v[60:63], v[226:229], v[120:123]
	v_mfma_f32_16x16x32_f16 v[124:127], v[242:245], v[214:217], v[124:127]
	v_mfma_f32_16x16x32_f16 v[146:149], v[242:245], v[218:221], v[146:149]
	v_mfma_f32_16x16x32_f16 v[134:137], v[242:245], v[226:229], v[134:137]
	v_mfma_f32_16x16x32_f16 v[138:141], v[60:63], v[218:221], v[138:141]
	v_mfma_f32_16x16x32_f16 v[142:145], v[60:63], v[222:225], v[142:145]
	v_mfma_f32_16x16x32_f16 v[150:153], v[242:245], v[222:225], v[150:153]
	s_setprio 0
	ds_read_b128 v[64:67], v130 offset:8192
	ds_read_b128 v[242:245], v130 offset:10240
	v_cvt_pk_f16_f32 v61, v72, v73
	v_cvt_pk_f16_f32 v60, v70, v71
	ds_write_b64 v100, v[60:61] offset:57344
	s_add_u32 s80, s22, 0xc0700
	s_addc_u32 s81, s90, 0
	global_load_dwordx4 v[60:63], v201, s[80:81] nt
	s_setprio 1
	s_waitcnt lgkmcnt(1)
	v_mfma_f32_16x16x32_f16 v[86:89], v[64:67], v[214:217], v[86:89]
	v_mfma_f32_16x16x32_f16 v[170:173], v[64:67], v[218:221], v[170:173]
	v_mfma_f32_16x16x32_f16 v[174:177], v[64:67], v[222:225], v[174:177]
	v_mfma_f32_16x16x32_f16 v[162:165], v[64:67], v[226:229], v[162:165]
	v_mfma_f32_16x16x32_f16 v[178:181], v[242:245], v[214:217], v[178:181]
	v_mfma_f32_16x16x32_f16 v[182:185], v[242:245], v[218:221], v[182:185]
	v_mfma_f32_16x16x32_f16 v[186:189], v[242:245], v[222:225], v[186:189]
	v_mfma_f32_16x16x32_f16 v[154:157], v[242:245], v[226:229], v[154:157]
	s_setprio 0
	ds_read_b128 v[64:67], v130 offset:12288
	ds_read_b128 v[68:71], v130 offset:14336
	v_cvt_pk_f16_f32 v39, v38, v39
	v_cvt_pk_f16_f32 v38, v36, v37
	ds_write_b64 v100, v[38:39] offset:61440
	s_add_u32 s80, s22, 0xe0700
	s_addc_u32 s81, s90, 0
	global_load_dwordx4 v[36:39], v201, s[80:81] nt
	s_setprio 1
	s_waitcnt lgkmcnt(1)
	v_mfma_f32_16x16x32_f16 v[90:93], v[64:67], v[218:221], v[90:93]
	v_mfma_f32_16x16x32_f16 v[242:245], v[64:67], v[214:217], v[74:77]
	v_mfma_f32_16x16x32_f16 v[158:161], v[64:67], v[222:225], v[158:161]
	v_mfma_f32_16x16x32_f16 v[166:169], v[64:67], v[226:229], v[166:169]
	v_mfma_f32_16x16x32_f16 v[190:193], v[68:71], v[214:217], v[190:193]
	v_mfma_f32_16x16x32_f16 v[202:205], v[68:71], v[218:221], v[202:205]
	v_mfma_f32_16x16x32_f16 v[206:209], v[68:71], v[222:225], v[206:209]
	v_mfma_f32_16x16x32_f16 v[210:213], v[68:71], v[226:229], v[210:213]
	s_setprio 0
	s_waitcnt vmcnt(4)
	s_waitcnt lgkmcnt(0)
	s_barrier
	ds_read_b128 v[214:217], v131 offset:32768
	ds_read_b128 v[218:221], v131 offset:34816
	ds_read_b128 v[222:225], v131 offset:36864
	ds_read_b128 v[226:229], v131 offset:38912
	ds_read_b128 v[64:67], v129 offset:32768
	ds_read_b128 v[68:71], v129 offset:34816
	s_add_u32 s80, s22, 0x800
	s_addc_u32 s81, s90, 0
	v_lshl_add_u64 v[198:199], s[38:39], 0, v[196:197]
	v_readfirstlane_b32 s1, v94
	s_mov_b32 m0, s1
	v_cvt_pk_f16_f32 v3, v2, v3
	global_load_lds_dwordx4 v[198:199], off
	v_cvt_pk_f16_f32 v2, v0, v1
	ds_write_b64 v100, v[2:3]
	global_load_dwordx4 v[0:3], v201, s[80:81] nt
	s_setprio 1
	s_waitcnt lgkmcnt(1)
	v_mfma_f32_16x16x32_f16 v[104:107], v[64:67], v[222:225], v[104:107]
	v_mfma_f32_16x16x32_f16 v[108:111], v[68:71], v[214:217], v[108:111]
	v_mfma_f32_16x16x32_f16 v[112:115], v[68:71], v[218:221], v[112:115]
	v_mfma_f32_16x16x32_f16 v[116:119], v[68:71], v[222:225], v[116:119]
	v_mfma_f32_16x16x32_f16 v[246:249], v[64:67], v[214:217], v[78:81]
	v_mfma_f32_16x16x32_f16 v[230:233], v[64:67], v[218:221], v[230:233]
	v_mfma_f32_16x16x32_f16 v[234:237], v[64:67], v[226:229], v[234:237]
	v_mfma_f32_16x16x32_f16 v[238:241], v[68:71], v[226:229], v[238:241]
	s_setprio 0
	ds_read_b128 v[68:71], v129 offset:36864
	ds_read_b128 v[72:75], v129 offset:38912
	v_readfirstlane_b32 s92, v99
	v_lshl_add_u64 v[64:65], v[198:199], 0, s[58:59]
	s_mov_b32 m0, s92
	v_cvt_pk_f16_f32 v11, v10, v11
	global_load_lds_dwordx4 v[64:65], off
	v_cvt_pk_f16_f32 v10, v8, v9
	ds_write_b64 v100, v[10:11] offset:4096
	s_add_u32 s80, s22, 0x20800
	s_addc_u32 s81, s90, 0
	global_load_dwordx4 v[64:67], v201, s[80:81] nt
	s_setprio 1
	s_waitcnt lgkmcnt(1)
	v_mfma_f32_16x16x32_f16 v[8:11], v[68:71], v[214:217], v[82:85]
	v_mfma_f32_16x16x32_f16 v[120:123], v[68:71], v[226:229], v[120:123]
	v_mfma_f32_16x16x32_f16 v[124:127], v[72:75], v[214:217], v[124:127]
	v_mfma_f32_16x16x32_f16 v[146:149], v[72:75], v[218:221], v[146:149]
	v_mfma_f32_16x16x32_f16 v[134:137], v[72:75], v[226:229], v[134:137]
	v_mfma_f32_16x16x32_f16 v[138:141], v[68:71], v[218:221], v[138:141]
	v_mfma_f32_16x16x32_f16 v[142:145], v[68:71], v[222:225], v[142:145]
	v_mfma_f32_16x16x32_f16 v[150:153], v[72:75], v[222:225], v[150:153]
	s_setprio 0
	ds_read_b128 v[72:75], v129 offset:40960
	ds_read_b128 v[76:79], v129 offset:43008
	v_readfirstlane_b32 s91, v101
	v_lshl_add_u64 v[68:69], v[198:199], 0, s[60:61]
	s_mov_b32 m0, s91
	v_cvt_pk_f16_f32 v15, v14, v15
	global_load_lds_dwordx4 v[68:69], off
	v_cvt_pk_f16_f32 v14, v12, v13
	ds_write_b64 v100, v[14:15] offset:8192
	s_add_u32 s80, s22, 0x40800
	s_addc_u32 s81, s90, 0
	global_load_dwordx4 v[68:71], v201, s[80:81] nt
	s_setprio 1
	s_waitcnt lgkmcnt(1)
	v_mfma_f32_16x16x32_f16 v[12:15], v[72:75], v[214:217], v[86:89]
	v_mfma_f32_16x16x32_f16 v[170:173], v[72:75], v[218:221], v[170:173]
	v_mfma_f32_16x16x32_f16 v[174:177], v[72:75], v[222:225], v[174:177]
	v_mfma_f32_16x16x32_f16 v[162:165], v[72:75], v[226:229], v[162:165]
	v_mfma_f32_16x16x32_f16 v[178:181], v[76:79], v[214:217], v[178:181]
	v_mfma_f32_16x16x32_f16 v[182:185], v[76:79], v[218:221], v[182:185]
	v_mfma_f32_16x16x32_f16 v[186:189], v[76:79], v[222:225], v[186:189]
	v_mfma_f32_16x16x32_f16 v[154:157], v[76:79], v[226:229], v[154:157]
	s_setprio 0
	ds_read_b128 v[76:79], v129 offset:45056
	ds_read_b128 v[80:83], v129 offset:47104
	v_readfirstlane_b32 s73, v102
	v_lshl_add_u64 v[72:73], v[198:199], 0, s[62:63]
	s_mov_b32 m0, s73
	v_cvt_pk_f16_f32 v19, v18, v19
	global_load_lds_dwordx4 v[72:73], off
	v_cvt_pk_f16_f32 v18, v16, v17
	ds_write_b64 v100, v[18:19] offset:12288
	s_add_u32 s80, s22, 0x60800
	s_addc_u32 s81, s90, 0
	global_load_dwordx4 v[72:75], v201, s[80:81] nt
	s_setprio 1
	s_waitcnt lgkmcnt(1)
	v_mfma_f32_16x16x32_f16 v[16:19], v[76:79], v[214:217], v[242:245]
	v_mfma_f32_16x16x32_f16 v[242:245], v[76:79], v[218:221], v[90:93]
	v_mfma_f32_16x16x32_f16 v[158:161], v[76:79], v[222:225], v[158:161]
	v_mfma_f32_16x16x32_f16 v[166:169], v[76:79], v[226:229], v[166:169]
	v_mfma_f32_16x16x32_f16 v[190:193], v[80:83], v[214:217], v[190:193]
	v_mfma_f32_16x16x32_f16 v[202:205], v[80:83], v[218:221], v[202:205]
	v_mfma_f32_16x16x32_f16 v[206:209], v[80:83], v[222:225], v[206:209]
	v_mfma_f32_16x16x32_f16 v[210:213], v[80:83], v[226:229], v[210:213]
	s_setprio 0
	ds_read_b128 v[214:217], v128 offset:32768
	ds_read_b128 v[218:221], v128 offset:34816
	ds_read_b128 v[222:225], v128 offset:36864
	ds_read_b128 v[226:229], v128 offset:38912
	ds_read_b128 v[80:83], v130 offset:32768
	ds_read_b128 v[84:87], v130 offset:34816
	v_cvt_pk_f16_f32 v23, v22, v23
	v_cvt_pk_f16_f32 v22, v20, v21
	ds_write_b64 v100, v[22:23] offset:16384
	s_add_u32 s80, s22, 0x80800
	s_addc_u32 s81, s90, 0
	global_load_dwordx4 v[76:79], v201, s[80:81] nt
	s_setprio 1
	s_waitcnt lgkmcnt(1)
	v_mfma_f32_16x16x32_f16 v[20:23], v[80:83], v[214:217], v[246:249]
	v_mfma_f32_16x16x32_f16 v[104:107], v[80:83], v[222:225], v[104:107]
	v_mfma_f32_16x16x32_f16 v[108:111], v[84:87], v[214:217], v[108:111]
	v_mfma_f32_16x16x32_f16 v[112:115], v[84:87], v[218:221], v[112:115]
	v_mfma_f32_16x16x32_f16 v[116:119], v[84:87], v[222:225], v[116:119]
	v_mfma_f32_16x16x32_f16 v[230:233], v[80:83], v[218:221], v[230:233]
	v_mfma_f32_16x16x32_f16 v[234:237], v[80:83], v[226:229], v[234:237]
	v_mfma_f32_16x16x32_f16 v[238:241], v[84:87], v[226:229], v[238:241]
	s_setprio 0
	ds_read_b128 v[84:87], v130 offset:36864
	ds_read_b128 v[88:91], v130 offset:38912
	v_cvt_pk_f16_f32 v27, v26, v27
	v_cvt_pk_f16_f32 v26, v24, v25
	ds_write_b64 v100, v[26:27] offset:20480
	s_add_u32 s80, s22, 0xa0800
	s_addc_u32 s81, s90, 0
	global_load_dwordx4 v[80:83], v201, s[80:81] nt
	s_setprio 1
	s_waitcnt lgkmcnt(1)
	v_mfma_f32_16x16x32_f16 v[24:27], v[84:87], v[214:217], v[8:11]
	v_mfma_f32_16x16x32_f16 v[120:123], v[84:87], v[226:229], v[120:123]
	v_mfma_f32_16x16x32_f16 v[124:127], v[88:91], v[214:217], v[124:127]
	v_mfma_f32_16x16x32_f16 v[146:149], v[88:91], v[218:221], v[146:149]
	v_mfma_f32_16x16x32_f16 v[134:137], v[88:91], v[226:229], v[134:137]
	v_mfma_f32_16x16x32_f16 v[138:141], v[84:87], v[218:221], v[138:141]
	v_mfma_f32_16x16x32_f16 v[142:145], v[84:87], v[222:225], v[142:145]
	v_mfma_f32_16x16x32_f16 v[150:153], v[88:91], v[222:225], v[150:153]
	s_setprio 0
	ds_read_b128 v[8:11], v130 offset:40960
	ds_read_b128 v[88:91], v130 offset:43008
	v_cvt_pk_f16_f32 v31, v30, v31
	v_cvt_pk_f16_f32 v30, v28, v29
	ds_write_b64 v100, v[30:31] offset:24576
	s_add_u32 s80, s22, 0xc0800
	s_addc_u32 s81, s90, 0
	global_load_dwordx4 v[84:87], v201, s[80:81] nt
	s_setprio 1
	s_waitcnt lgkmcnt(1)
	v_mfma_f32_16x16x32_f16 v[12:15], v[8:11], v[214:217], v[12:15]
	v_mfma_f32_16x16x32_f16 v[28:31], v[8:11], v[218:221], v[170:173]
	v_mfma_f32_16x16x32_f16 v[170:173], v[8:11], v[222:225], v[174:177]
	v_mfma_f32_16x16x32_f16 v[162:165], v[8:11], v[226:229], v[162:165]
	v_mfma_f32_16x16x32_f16 v[174:177], v[88:91], v[214:217], v[178:181]
	v_mfma_f32_16x16x32_f16 v[178:181], v[88:91], v[218:221], v[182:185]
	v_mfma_f32_16x16x32_f16 v[182:185], v[88:91], v[222:225], v[186:189]
	v_mfma_f32_16x16x32_f16 v[154:157], v[88:91], v[226:229], v[154:157]
	s_setprio 0
	ds_read_b128 v[8:11], v130 offset:45056
	ds_read_b128 v[186:189], v130 offset:47104
	v_cvt_pk_f16_f32 v35, v34, v35
	v_cvt_pk_f16_f32 v34, v32, v33
	ds_write_b64 v100, v[34:35] offset:28672
	s_add_u32 s80, s22, 0xe0800
	s_addc_u32 s81, s90, 0
	global_load_dwordx4 v[88:91], v201, s[80:81] nt
	s_setprio 1
	s_waitcnt lgkmcnt(1)
	v_mfma_f32_16x16x32_f16 v[16:19], v[8:11], v[214:217], v[16:19]
	v_mfma_f32_16x16x32_f16 v[32:35], v[8:11], v[218:221], v[242:245]
	v_mfma_f32_16x16x32_f16 v[158:161], v[8:11], v[222:225], v[158:161]
	v_mfma_f32_16x16x32_f16 v[166:169], v[8:11], v[226:229], v[166:169]
	v_mfma_f32_16x16x32_f16 v[190:193], v[186:189], v[214:217], v[190:193]
	v_mfma_f32_16x16x32_f16 v[202:205], v[186:189], v[218:221], v[202:205]
	v_mfma_f32_16x16x32_f16 v[206:209], v[186:189], v[222:225], v[206:209]
	v_mfma_f32_16x16x32_f16 v[186:189], v[186:189], v[226:229], v[210:213]
	s_setprio 0
	s_waitcnt vmcnt(4)
	s_waitcnt lgkmcnt(0)
	s_barrier
	s_nop 0
	ds_read_b128 v[210:213], v131
	ds_read_b128 v[214:217], v131 offset:2048
	ds_read_b128 v[218:221], v131 offset:4096
	ds_read_b128 v[222:225], v131 offset:6144
	ds_read_b128 v[8:11], v129
	ds_read_b128 v[226:229], v129 offset:2048
	s_add_u32 s80, s22, 0x900
	v_lshl_add_u64 v[92:93], s[40:41], 0, v[196:197]
	s_addc_u32 s81, s90, 0
	s_mov_b32 m0, s0
	v_cvt_pk_f16_f32 v7, v6, v7
	global_load_lds_dwordx4 v[92:93], off
	v_cvt_pk_f16_f32 v6, v4, v5
	ds_write_b64 v100, v[6:7] offset:32768
	global_load_dwordx4 v[4:7], v201, s[80:81] nt
	s_setprio 1
	s_waitcnt lgkmcnt(1)
	v_mfma_f32_16x16x32_f16 v[20:23], v[8:11], v[210:213], v[20:23]
	v_mfma_f32_16x16x32_f16 v[104:107], v[8:11], v[218:221], v[104:107]
	v_mfma_f32_16x16x32_f16 v[108:111], v[226:229], v[210:213], v[108:111]
	v_mfma_f32_16x16x32_f16 v[112:115], v[226:229], v[214:217], v[112:115]
	v_mfma_f32_16x16x32_f16 v[116:119], v[226:229], v[218:221], v[116:119]
	v_mfma_f32_16x16x32_f16 v[230:233], v[8:11], v[214:217], v[230:233]
	v_mfma_f32_16x16x32_f16 v[234:237], v[8:11], v[222:225], v[234:237]
	v_mfma_f32_16x16x32_f16 v[226:229], v[226:229], v[222:225], v[238:241]
	s_setprio 0
	s_nop 1
	ds_read_b128 v[238:241], v129 offset:4096
	ds_read_b128 v[242:245], v129 offset:6144
	s_mov_b32 m0, s72
	v_lshl_add_u64 v[8:9], v[92:93], 0, s[58:59]
	global_load_lds_dwordx4 v[8:9], off
	v_cvt_pk_f16_f32 v9, v42, v43
	v_cvt_pk_f16_f32 v8, v40, v41
	ds_write_b64 v100, v[8:9] offset:36864
	s_add_u32 s80, s22, 0x20900
	s_addc_u32 s81, s90, 0
	global_load_dwordx4 v[8:11], v201, s[80:81] nt
	s_setprio 1
	s_waitcnt lgkmcnt(1)
	v_mfma_f32_16x16x32_f16 v[24:27], v[238:241], v[210:213], v[24:27]
	v_mfma_f32_16x16x32_f16 v[120:123], v[238:241], v[222:225], v[120:123]
	v_mfma_f32_16x16x32_f16 v[124:127], v[242:245], v[210:213], v[124:127]
	v_mfma_f32_16x16x32_f16 v[146:149], v[242:245], v[214:217], v[146:149]
	v_mfma_f32_16x16x32_f16 v[134:137], v[242:245], v[222:225], v[134:137]
	v_mfma_f32_16x16x32_f16 v[138:141], v[238:241], v[214:217], v[138:141]
	v_mfma_f32_16x16x32_f16 v[142:145], v[238:241], v[218:221], v[142:145]
	v_mfma_f32_16x16x32_f16 v[150:153], v[242:245], v[218:221], v[150:153]
	s_setprio 0
	ds_read_b128 v[238:241], v129 offset:8192
	ds_read_b128 v[242:245], v129 offset:10240
	s_mov_b32 m0, s71
	v_lshl_add_u64 v[40:41], v[92:93], 0, s[60:61]
	global_load_lds_dwordx4 v[40:41], off
	v_cvt_pk_f16_f32 v41, v46, v47
	v_cvt_pk_f16_f32 v40, v44, v45
	ds_write_b64 v100, v[40:41] offset:40960
	s_add_u32 s80, s22, 0x40900
	s_addc_u32 s81, s90, 0
	global_load_dwordx4 v[40:43], v201, s[80:81] nt
	s_setprio 1
	s_waitcnt lgkmcnt(1)
	v_mfma_f32_16x16x32_f16 v[12:15], v[238:241], v[210:213], v[12:15]
	v_mfma_f32_16x16x32_f16 v[28:31], v[238:241], v[214:217], v[28:31]
	v_mfma_f32_16x16x32_f16 v[170:173], v[238:241], v[218:221], v[170:173]
	v_mfma_f32_16x16x32_f16 v[162:165], v[238:241], v[222:225], v[162:165]
	v_mfma_f32_16x16x32_f16 v[174:177], v[242:245], v[210:213], v[174:177]
	v_mfma_f32_16x16x32_f16 v[178:181], v[242:245], v[214:217], v[178:181]
	v_mfma_f32_16x16x32_f16 v[182:185], v[242:245], v[218:221], v[182:185]
	v_mfma_f32_16x16x32_f16 v[154:157], v[242:245], v[222:225], v[154:157]
	s_setprio 0
	ds_read_b128 v[238:241], v129 offset:12288
	ds_read_b128 v[242:245], v129 offset:14336
	s_mov_b32 m0, s70
	v_lshl_add_u64 v[44:45], v[92:93], 0, s[62:63]
	global_load_lds_dwordx4 v[44:45], off
	v_cvt_pk_f16_f32 v45, v50, v51
	v_cvt_pk_f16_f32 v44, v48, v49
	ds_write_b64 v100, v[44:45] offset:45056
	s_add_u32 s70, s22, 0x60900
	s_addc_u32 s71, s90, 0
	global_load_dwordx4 v[44:47], v201, s[70:71] nt
	s_setprio 1
	s_waitcnt lgkmcnt(1)
	v_mfma_f32_16x16x32_f16 v[16:19], v[238:241], v[210:213], v[16:19]
	v_mfma_f32_16x16x32_f16 v[32:35], v[238:241], v[214:217], v[32:35]
	v_mfma_f32_16x16x32_f16 v[158:161], v[238:241], v[218:221], v[158:161]
	v_mfma_f32_16x16x32_f16 v[166:169], v[238:241], v[222:225], v[166:169]
	v_mfma_f32_16x16x32_f16 v[190:193], v[242:245], v[210:213], v[190:193]
	v_mfma_f32_16x16x32_f16 v[202:205], v[242:245], v[214:217], v[202:205]
	v_mfma_f32_16x16x32_f16 v[206:209], v[242:245], v[218:221], v[206:209]
	v_mfma_f32_16x16x32_f16 v[186:189], v[242:245], v[222:225], v[186:189]
	s_setprio 0
	ds_read_b128 v[210:213], v128
	ds_read_b128 v[214:217], v128 offset:2048
	ds_read_b128 v[218:221], v128 offset:4096
	ds_read_b128 v[222:225], v128 offset:6144
	ds_read_b128 v[238:241], v130
	ds_read_b128 v[242:245], v130 offset:2048
	v_cvt_pk_f16_f32 v49, v54, v55
	v_cvt_pk_f16_f32 v48, v52, v53
	ds_write_b64 v100, v[48:49] offset:49152
	s_add_u32 s70, s22, 0x80900
	s_addc_u32 s71, s90, 0
	global_load_dwordx4 v[48:51], v201, s[70:71] nt
	s_setprio 1
	s_waitcnt lgkmcnt(1)
	v_mfma_f32_16x16x32_f16 v[20:23], v[238:241], v[210:213], v[20:23]
	v_mfma_f32_16x16x32_f16 v[104:107], v[238:241], v[218:221], v[104:107]
	v_mfma_f32_16x16x32_f16 v[108:111], v[242:245], v[210:213], v[108:111]
	v_mfma_f32_16x16x32_f16 v[112:115], v[242:245], v[214:217], v[112:115]
	v_mfma_f32_16x16x32_f16 v[116:119], v[242:245], v[218:221], v[116:119]
	v_mfma_f32_16x16x32_f16 v[230:233], v[238:241], v[214:217], v[230:233]
	v_mfma_f32_16x16x32_f16 v[234:237], v[238:241], v[222:225], v[234:237]
	v_mfma_f32_16x16x32_f16 v[226:229], v[242:245], v[222:225], v[226:229]
	s_setprio 0
	ds_read_b128 v[238:241], v130 offset:4096
	ds_read_b128 v[242:245], v130 offset:6144
	v_cvt_pk_f16_f32 v53, v58, v59
	v_cvt_pk_f16_f32 v52, v56, v57
	ds_write_b64 v100, v[52:53] offset:53248
	s_add_u32 s70, s22, 0xa0900
	s_addc_u32 s71, s90, 0
	global_load_dwordx4 v[52:55], v201, s[70:71] nt
	s_setprio 1
	s_waitcnt lgkmcnt(1)
	v_mfma_f32_16x16x32_f16 v[24:27], v[238:241], v[210:213], v[24:27]
	v_mfma_f32_16x16x32_f16 v[120:123], v[238:241], v[222:225], v[120:123]
	v_mfma_f32_16x16x32_f16 v[124:127], v[242:245], v[210:213], v[124:127]
	v_mfma_f32_16x16x32_f16 v[146:149], v[242:245], v[214:217], v[146:149]
	v_mfma_f32_16x16x32_f16 v[134:137], v[242:245], v[222:225], v[134:137]
	v_mfma_f32_16x16x32_f16 v[138:141], v[238:241], v[214:217], v[138:141]
	v_mfma_f32_16x16x32_f16 v[142:145], v[238:241], v[218:221], v[142:145]
	v_mfma_f32_16x16x32_f16 v[150:153], v[242:245], v[218:221], v[150:153]
	s_setprio 0
	ds_read_b128 v[238:241], v130 offset:8192
	ds_read_b128 v[242:245], v130 offset:10240
	v_cvt_pk_f16_f32 v57, v62, v63
	v_cvt_pk_f16_f32 v56, v60, v61
	ds_write_b64 v100, v[56:57] offset:57344
	s_add_u32 s70, s22, 0xc0900
	s_addc_u32 s71, s90, 0
	global_load_dwordx4 v[56:59], v201, s[70:71] nt
	s_setprio 1
	s_waitcnt lgkmcnt(1)
	v_mfma_f32_16x16x32_f16 v[28:31], v[238:241], v[214:217], v[28:31]
	v_mfma_f32_16x16x32_f16 v[246:249], v[238:241], v[210:213], v[12:15]
	v_mfma_f32_16x16x32_f16 v[170:173], v[238:241], v[218:221], v[170:173]
	v_mfma_f32_16x16x32_f16 v[162:165], v[238:241], v[222:225], v[162:165]
	v_mfma_f32_16x16x32_f16 v[174:177], v[242:245], v[210:213], v[174:177]
	v_mfma_f32_16x16x32_f16 v[178:181], v[242:245], v[214:217], v[178:181]
	v_mfma_f32_16x16x32_f16 v[182:185], v[242:245], v[218:221], v[182:185]
	v_mfma_f32_16x16x32_f16 v[154:157], v[242:245], v[222:225], v[154:157]
	s_setprio 0
	ds_read_b128 v[12:15], v130 offset:12288
	ds_read_b128 v[238:241], v130 offset:14336
	v_cvt_pk_f16_f32 v39, v38, v39
	v_cvt_pk_f16_f32 v38, v36, v37
	ds_write_b64 v100, v[38:39] offset:61440
	s_add_u32 s70, s22, 0xe0900
	s_addc_u32 s71, s90, 0
	global_load_dwordx4 v[60:63], v201, s[70:71] nt
	s_setprio 1
	s_waitcnt lgkmcnt(1)
	v_mfma_f32_16x16x32_f16 v[36:39], v[12:15], v[210:213], v[16:19]
	v_mfma_f32_16x16x32_f16 v[32:35], v[12:15], v[214:217], v[32:35]
	v_mfma_f32_16x16x32_f16 v[158:161], v[12:15], v[218:221], v[158:161]
	v_mfma_f32_16x16x32_f16 v[166:169], v[12:15], v[222:225], v[166:169]
	v_mfma_f32_16x16x32_f16 v[190:193], v[238:241], v[210:213], v[190:193]
	v_mfma_f32_16x16x32_f16 v[202:205], v[238:241], v[214:217], v[202:205]
	v_mfma_f32_16x16x32_f16 v[206:209], v[238:241], v[218:221], v[206:209]
	v_mfma_f32_16x16x32_f16 v[186:189], v[238:241], v[222:225], v[186:189]
	s_setprio 0
	s_waitcnt vmcnt(4)
	s_waitcnt lgkmcnt(0)
	s_barrier
	ds_read_b128 v[210:213], v131 offset:32768
	ds_read_b128 v[214:217], v131 offset:34816
	ds_read_b128 v[218:221], v131 offset:36864
	ds_read_b128 v[222:225], v131 offset:38912
	ds_read_b128 v[12:15], v129 offset:32768
	ds_read_b128 v[16:19], v129 offset:34816
	s_add_u32 s70, s22, 0xa00
	v_lshl_add_u64 v[92:93], s[42:43], 0, v[196:197]
	s_addc_u32 s71, s90, 0
	s_mov_b32 m0, s1
	v_cvt_pk_f16_f32 v3, v2, v3
	global_load_lds_dwordx4 v[92:93], off
	v_cvt_pk_f16_f32 v2, v0, v1
	ds_write_b64 v100, v[2:3]
	global_load_dwordx4 v[0:3], v201, s[70:71] nt
	s_setprio 1
	s_waitcnt lgkmcnt(1)
	v_mfma_f32_16x16x32_f16 v[104:107], v[12:15], v[218:221], v[104:107]
	v_mfma_f32_16x16x32_f16 v[108:111], v[16:19], v[210:213], v[108:111]
	v_mfma_f32_16x16x32_f16 v[112:115], v[16:19], v[214:217], v[112:115]
	v_mfma_f32_16x16x32_f16 v[116:119], v[16:19], v[218:221], v[116:119]
	v_mfma_f32_16x16x32_f16 v[238:241], v[12:15], v[210:213], v[20:23]
	v_mfma_f32_16x16x32_f16 v[230:233], v[12:15], v[214:217], v[230:233]
	v_mfma_f32_16x16x32_f16 v[234:237], v[12:15], v[222:225], v[234:237]
	v_mfma_f32_16x16x32_f16 v[226:229], v[16:19], v[222:225], v[226:229]
	s_setprio 0
	ds_read_b128 v[16:19], v129 offset:36864
	ds_read_b128 v[20:23], v129 offset:38912
	s_mov_b32 m0, s92
	v_lshl_add_u64 v[12:13], v[92:93], 0, s[58:59]
	global_load_lds_dwordx4 v[12:13], off
	v_cvt_pk_f16_f32 v13, v66, v67
	v_cvt_pk_f16_f32 v12, v64, v65
	ds_write_b64 v100, v[12:13] offset:4096
	s_add_u32 s0, s22, 0x20a00
	s_addc_u32 s1, s90, 0
	global_load_dwordx4 v[12:15], v201, s[0:1] nt
	s_setprio 1
	s_waitcnt lgkmcnt(1)
	v_mfma_f32_16x16x32_f16 v[64:67], v[16:19], v[210:213], v[24:27]
	v_mfma_f32_16x16x32_f16 v[120:123], v[16:19], v[222:225], v[120:123]
	v_mfma_f32_16x16x32_f16 v[124:127], v[20:23], v[210:213], v[124:127]
	v_mfma_f32_16x16x32_f16 v[146:149], v[20:23], v[214:217], v[146:149]
	v_mfma_f32_16x16x32_f16 v[134:137], v[20:23], v[222:225], v[134:137]
	v_mfma_f32_16x16x32_f16 v[138:141], v[16:19], v[214:217], v[138:141]
	v_mfma_f32_16x16x32_f16 v[142:145], v[16:19], v[218:221], v[142:145]
	v_mfma_f32_16x16x32_f16 v[150:153], v[20:23], v[218:221], v[150:153]
	s_setprio 0
	ds_read_b128 v[20:23], v129 offset:40960
	ds_read_b128 v[24:27], v129 offset:43008
	s_mov_b32 m0, s91
	v_lshl_add_u64 v[16:17], v[92:93], 0, s[60:61]
	global_load_lds_dwordx4 v[16:17], off
	v_cvt_pk_f16_f32 v17, v70, v71
	v_cvt_pk_f16_f32 v16, v68, v69
	ds_write_b64 v100, v[16:17] offset:8192
	s_add_u32 s0, s22, 0x40a00
	s_addc_u32 s1, s90, 0
	global_load_dwordx4 v[16:19], v201, s[0:1] nt
	s_setprio 1
	s_waitcnt lgkmcnt(1)
	v_mfma_f32_16x16x32_f16 v[68:71], v[20:23], v[210:213], v[246:249]
	v_mfma_f32_16x16x32_f16 v[242:245], v[20:23], v[214:217], v[28:31]
	v_mfma_f32_16x16x32_f16 v[170:173], v[20:23], v[218:221], v[170:173]
	v_mfma_f32_16x16x32_f16 v[162:165], v[20:23], v[222:225], v[162:165]
	v_mfma_f32_16x16x32_f16 v[174:177], v[24:27], v[210:213], v[174:177]
	v_mfma_f32_16x16x32_f16 v[178:181], v[24:27], v[214:217], v[178:181]
	v_mfma_f32_16x16x32_f16 v[182:185], v[24:27], v[218:221], v[182:185]
	v_mfma_f32_16x16x32_f16 v[154:157], v[24:27], v[222:225], v[154:157]
	s_setprio 0
	ds_read_b128 v[24:27], v129 offset:45056
	ds_read_b128 v[28:31], v129 offset:47104
	s_mov_b32 m0, s73
	v_lshl_add_u64 v[20:21], v[92:93], 0, s[62:63]
	global_load_lds_dwordx4 v[20:21], off
	v_cvt_pk_f16_f32 v21, v74, v75
	v_cvt_pk_f16_f32 v20, v72, v73
	ds_write_b64 v100, v[20:21] offset:12288
	s_add_u32 s0, s22, 0x60a00
	s_addc_u32 s1, s90, 0
	global_load_dwordx4 v[20:23], v201, s[0:1] nt
	s_setprio 1
	s_waitcnt lgkmcnt(1)
	v_mfma_f32_16x16x32_f16 v[72:75], v[24:27], v[210:213], v[36:39]
	v_mfma_f32_16x16x32_f16 v[246:249], v[24:27], v[214:217], v[32:35]
	v_mfma_f32_16x16x32_f16 v[158:161], v[24:27], v[218:221], v[158:161]
	v_mfma_f32_16x16x32_f16 v[166:169], v[24:27], v[222:225], v[166:169]
	v_mfma_f32_16x16x32_f16 v[190:193], v[28:31], v[210:213], v[190:193]
	v_mfma_f32_16x16x32_f16 v[202:205], v[28:31], v[214:217], v[202:205]
	v_mfma_f32_16x16x32_f16 v[206:209], v[28:31], v[218:221], v[206:209]
	v_mfma_f32_16x16x32_f16 v[186:189], v[28:31], v[222:225], v[186:189]
	s_setprio 0
	ds_read_b128 v[210:213], v128 offset:32768
	ds_read_b128 v[214:217], v128 offset:34816
	ds_read_b128 v[218:221], v128 offset:36864
	ds_read_b128 v[222:225], v128 offset:38912
	ds_read_b128 v[28:31], v130 offset:32768
	ds_read_b128 v[32:35], v130 offset:34816
	v_cvt_pk_f16_f32 v25, v78, v79
	v_cvt_pk_f16_f32 v24, v76, v77
	ds_write_b64 v100, v[24:25] offset:16384
	s_add_u32 s0, s22, 0x80a00
	s_addc_u32 s1, s90, 0
	global_load_dwordx4 v[24:27], v201, s[0:1] nt
	s_setprio 1
	s_waitcnt lgkmcnt(1)
	v_mfma_f32_16x16x32_f16 v[76:79], v[28:31], v[210:213], v[238:241]
	v_mfma_f32_16x16x32_f16 v[104:107], v[28:31], v[218:221], v[104:107]
	v_mfma_f32_16x16x32_f16 v[108:111], v[32:35], v[210:213], v[108:111]
	v_mfma_f32_16x16x32_f16 v[112:115], v[32:35], v[214:217], v[112:115]
	v_mfma_f32_16x16x32_f16 v[116:119], v[32:35], v[218:221], v[116:119]
	v_mfma_f32_16x16x32_f16 v[230:233], v[28:31], v[214:217], v[230:233]
	v_mfma_f32_16x16x32_f16 v[234:237], v[28:31], v[222:225], v[234:237]
	v_mfma_f32_16x16x32_f16 v[226:229], v[32:35], v[222:225], v[226:229]
	s_setprio 0
	ds_read_b128 v[32:35], v130 offset:36864
	ds_read_b128 v[36:39], v130 offset:38912
	v_cvt_pk_f16_f32 v29, v82, v83
	v_cvt_pk_f16_f32 v28, v80, v81
	ds_write_b64 v100, v[28:29] offset:20480
	s_add_u32 s0, s22, 0xa0a00
	s_addc_u32 s1, s90, 0
	global_load_dwordx4 v[28:31], v201, s[0:1] nt
	s_setprio 1
	s_waitcnt lgkmcnt(1)
	v_mfma_f32_16x16x32_f16 v[80:83], v[32:35], v[210:213], v[64:67]
	v_mfma_f32_16x16x32_f16 v[120:123], v[32:35], v[222:225], v[120:123]
	v_mfma_f32_16x16x32_f16 v[124:127], v[36:39], v[210:213], v[124:127]
	v_mfma_f32_16x16x32_f16 v[146:149], v[36:39], v[214:217], v[146:149]
	v_mfma_f32_16x16x32_f16 v[134:137], v[36:39], v[222:225], v[134:137]
	v_mfma_f32_16x16x32_f16 v[138:141], v[32:35], v[214:217], v[138:141]
	v_mfma_f32_16x16x32_f16 v[142:145], v[32:35], v[218:221], v[142:145]
	v_mfma_f32_16x16x32_f16 v[150:153], v[36:39], v[218:221], v[150:153]
	s_setprio 0
	ds_read_b128 v[36:39], v130 offset:40960
	ds_read_b128 v[64:67], v130 offset:43008
	v_cvt_pk_f16_f32 v33, v86, v87
	v_cvt_pk_f16_f32 v32, v84, v85
	ds_write_b64 v100, v[32:33] offset:24576
	s_add_u32 s0, s22, 0xc0a00
	s_addc_u32 s1, s90, 0
	global_load_dwordx4 v[32:35], v201, s[0:1] nt
	s_setprio 1
	s_waitcnt lgkmcnt(1)
	v_mfma_f32_16x16x32_f16 v[68:71], v[36:39], v[210:213], v[68:71]
	v_mfma_f32_16x16x32_f16 v[84:87], v[36:39], v[214:217], v[242:245]
	v_mfma_f32_16x16x32_f16 v[170:173], v[36:39], v[218:221], v[170:173]
	v_mfma_f32_16x16x32_f16 v[162:165], v[36:39], v[222:225], v[162:165]
	v_mfma_f32_16x16x32_f16 v[174:177], v[64:67], v[210:213], v[174:177]
	v_mfma_f32_16x16x32_f16 v[178:181], v[64:67], v[214:217], v[178:181]
	v_mfma_f32_16x16x32_f16 v[182:185], v[64:67], v[218:221], v[182:185]
	v_mfma_f32_16x16x32_f16 v[154:157], v[64:67], v[222:225], v[154:157]
	s_setprio 0
	ds_read_b128 v[64:67], v130 offset:45056
	ds_read_b128 v[238:241], v130 offset:47104
	v_cvt_pk_f16_f32 v37, v90, v91
	v_cvt_pk_f16_f32 v36, v88, v89
	ds_write_b64 v100, v[36:37] offset:28672
	s_add_u32 s0, s22, 0xe0a00
	s_addc_u32 s1, s90, 0
	global_load_dwordx4 v[36:39], v201, s[0:1] nt
	s_setprio 1
	s_waitcnt lgkmcnt(1)
	v_mfma_f32_16x16x32_f16 v[72:75], v[64:67], v[210:213], v[72:75]
	v_mfma_f32_16x16x32_f16 v[88:91], v[64:67], v[214:217], v[246:249]
	v_mfma_f32_16x16x32_f16 v[158:161], v[64:67], v[218:221], v[158:161]
	v_mfma_f32_16x16x32_f16 v[166:169], v[64:67], v[222:225], v[166:169]
	v_mfma_f32_16x16x32_f16 v[190:193], v[238:241], v[210:213], v[190:193]
	v_mfma_f32_16x16x32_f16 v[202:205], v[238:241], v[214:217], v[202:205]
	v_mfma_f32_16x16x32_f16 v[206:209], v[238:241], v[218:221], v[206:209]
	v_mfma_f32_16x16x32_f16 v[186:189], v[238:241], v[222:225], v[186:189]
	s_setprio 0
	s_waitcnt vmcnt(4)
	s_waitcnt lgkmcnt(0)
	s_barrier
	ds_read_b128 v[210:213], v131
	ds_read_b128 v[214:217], v131 offset:2048
	ds_read_b128 v[218:221], v131 offset:4096
	ds_read_b128 v[222:225], v131 offset:6144
	ds_read_b128 v[64:67], v129
	ds_read_b128 v[238:241], v129 offset:2048
	s_add_u32 s70, s22, 0xb00
	v_lshl_add_u64 v[92:93], s[44:45], 0, v[196:197]
	s_addc_u32 s71, s90, 0
	v_readfirstlane_b32 s0, v95
	s_mov_b32 m0, s0
	v_cvt_pk_f16_f32 v7, v6, v7
	global_load_lds_dwordx4 v[92:93], off
	v_cvt_pk_f16_f32 v6, v4, v5
	ds_write_b64 v100, v[6:7] offset:32768
	global_load_dwordx4 v[4:7], v201, s[70:71] nt
	s_setprio 1
	s_waitcnt lgkmcnt(1)
	v_mfma_f32_16x16x32_f16 v[76:79], v[64:67], v[210:213], v[76:79]
	v_mfma_f32_16x16x32_f16 v[104:107], v[64:67], v[218:221], v[104:107]
	v_mfma_f32_16x16x32_f16 v[108:111], v[238:241], v[210:213], v[108:111]
	v_mfma_f32_16x16x32_f16 v[112:115], v[238:241], v[214:217], v[112:115]
	v_mfma_f32_16x16x32_f16 v[116:119], v[238:241], v[218:221], v[116:119]
	v_mfma_f32_16x16x32_f16 v[230:233], v[64:67], v[214:217], v[230:233]
	v_mfma_f32_16x16x32_f16 v[234:237], v[64:67], v[222:225], v[234:237]
	v_mfma_f32_16x16x32_f16 v[226:229], v[238:241], v[222:225], v[226:229]
	s_setprio 0
	ds_read_b128 v[238:241], v129 offset:4096
	ds_read_b128 v[242:245], v129 offset:6144
	v_readfirstlane_b32 s72, v96
	v_lshl_add_u64 v[64:65], v[92:93], 0, s[58:59]
	s_mov_b32 m0, s72
	v_cvt_pk_f16_f32 v11, v10, v11
	global_load_lds_dwordx4 v[64:65], off
	v_cvt_pk_f16_f32 v10, v8, v9
	ds_write_b64 v100, v[10:11] offset:36864
	s_add_u32 s70, s22, 0x20b00
	s_addc_u32 s71, s90, 0
	global_load_dwordx4 v[64:67], v201, s[70:71] nt
	s_setprio 1
	s_waitcnt lgkmcnt(1)
	v_mfma_f32_16x16x32_f16 v[8:11], v[238:241], v[210:213], v[80:83]
	v_mfma_f32_16x16x32_f16 v[80:83], v[238:241], v[214:217], v[138:141]
	v_mfma_f32_16x16x32_f16 v[138:141], v[238:241], v[218:221], v[142:145]
	v_mfma_f32_16x16x32_f16 v[120:123], v[238:241], v[222:225], v[120:123]
	v_mfma_f32_16x16x32_f16 v[124:127], v[242:245], v[210:213], v[124:127]
	v_mfma_f32_16x16x32_f16 v[142:145], v[242:245], v[214:217], v[146:149]
	v_mfma_f32_16x16x32_f16 v[146:149], v[242:245], v[218:221], v[150:153]
	v_mfma_f32_16x16x32_f16 v[134:137], v[242:245], v[222:225], v[134:137]
	s_setprio 0
	s_nop 0
	ds_read_b128 v[150:153], v129 offset:8192
	ds_read_b128 v[238:241], v129 offset:10240
	v_readfirstlane_b32 s71, v97
	v_lshl_add_u64 v[198:199], v[92:93], 0, s[60:61]
	s_mov_b32 m0, s71
	v_cvt_pk_f16_f32 v43, v42, v43
	global_load_lds_dwordx4 v[198:199], off
	v_cvt_pk_f16_f32 v42, v40, v41
	ds_write_b64 v100, v[42:43] offset:40960
	s_add_u32 s80, s22, 0x40b00
	s_addc_u32 s81, s90, 0
	global_load_dwordx4 v[40:43], v201, s[80:81] nt
	s_setprio 1
	s_waitcnt lgkmcnt(1)
	v_mfma_f32_16x16x32_f16 v[68:71], v[150:153], v[210:213], v[68:71]
	v_mfma_f32_16x16x32_f16 v[84:87], v[150:153], v[214:217], v[84:87]
	v_mfma_f32_16x16x32_f16 v[170:173], v[150:153], v[218:221], v[170:173]
	v_mfma_f32_16x16x32_f16 v[150:153], v[150:153], v[222:225], v[162:165]
	v_mfma_f32_16x16x32_f16 v[162:165], v[238:241], v[210:213], v[174:177]
	v_mfma_f32_16x16x32_f16 v[174:177], v[238:241], v[214:217], v[178:181]
	v_mfma_f32_16x16x32_f16 v[178:181], v[238:241], v[218:221], v[182:185]
	v_mfma_f32_16x16x32_f16 v[154:157], v[238:241], v[222:225], v[154:157]
	s_setprio 0
	s_nop 0
	ds_read_b128 v[182:185], v129 offset:12288
	ds_read_b128 v[238:241], v129 offset:14336
	v_readfirstlane_b32 s70, v98
	v_lshl_add_u64 v[92:93], v[92:93], 0, s[62:63]
	s_mov_b32 m0, s70
	v_cvt_pk_f16_f32 v47, v46, v47
	global_load_lds_dwordx4 v[92:93], off
	v_cvt_pk_f16_f32 v46, v44, v45
	ds_write_b64 v100, v[46:47] offset:45056
	s_add_u32 s80, s22, 0x60b00
	s_addc_u32 s81, s90, 0
	global_load_dwordx4 v[44:47], v201, s[80:81] nt
	s_setprio 1
	s_waitcnt lgkmcnt(1)
	v_mfma_f32_16x16x32_f16 v[72:75], v[182:185], v[210:213], v[72:75]
	v_mfma_f32_16x16x32_f16 v[88:91], v[182:185], v[214:217], v[88:91]
	v_mfma_f32_16x16x32_f16 v[158:161], v[182:185], v[218:221], v[158:161]
	v_mfma_f32_16x16x32_f16 v[166:169], v[182:185], v[222:225], v[166:169]
	v_mfma_f32_16x16x32_f16 v[182:185], v[238:241], v[210:213], v[190:193]
	v_mfma_f32_16x16x32_f16 v[190:193], v[238:241], v[214:217], v[202:205]
	v_mfma_f32_16x16x32_f16 v[202:205], v[238:241], v[218:221], v[206:209]
	v_mfma_f32_16x16x32_f16 v[186:189], v[238:241], v[222:225], v[186:189]
	s_setprio 0
	s_nop 0
	ds_read_b128 v[206:209], v128
	ds_read_b128 v[210:213], v128 offset:2048
	ds_read_b128 v[214:217], v128 offset:4096
	ds_read_b128 v[218:221], v128 offset:6144
	ds_read_b128 v[222:225], v130
	ds_read_b128 v[238:241], v130 offset:2048
	v_cvt_pk_f16_f32 v51, v50, v51
	v_cvt_pk_f16_f32 v50, v48, v49
	ds_write_b64 v100, v[50:51] offset:49152
	s_add_u32 s80, s22, 0x80b00
	s_addc_u32 s81, s90, 0
	global_load_dwordx4 v[48:51], v201, s[80:81] nt
	s_setprio 1
	s_waitcnt lgkmcnt(1)
	v_mfma_f32_16x16x32_f16 v[76:79], v[222:225], v[206:209], v[76:79]
	v_mfma_f32_16x16x32_f16 v[104:107], v[222:225], v[214:217], v[104:107]
	v_mfma_f32_16x16x32_f16 v[108:111], v[238:241], v[206:209], v[108:111]
	v_mfma_f32_16x16x32_f16 v[112:115], v[238:241], v[210:213], v[112:115]
	v_mfma_f32_16x16x32_f16 v[116:119], v[238:241], v[214:217], v[116:119]
	v_mfma_f32_16x16x32_f16 v[230:233], v[222:225], v[210:213], v[230:233]
	v_mfma_f32_16x16x32_f16 v[222:225], v[222:225], v[218:221], v[234:237]
	v_mfma_f32_16x16x32_f16 v[226:229], v[238:241], v[218:221], v[226:229]
	s_setprio 0
	s_nop 0
	ds_read_b128 v[234:237], v130 offset:4096
	ds_read_b128 v[238:241], v130 offset:6144
	v_cvt_pk_f16_f32 v55, v54, v55
	v_cvt_pk_f16_f32 v54, v52, v53
	ds_write_b64 v100, v[54:55] offset:53248
	s_add_u32 s80, s22, 0xa0b00
	s_addc_u32 s81, s90, 0
	global_load_dwordx4 v[52:55], v201, s[80:81] nt
	s_setprio 1
	s_waitcnt lgkmcnt(1)
	v_mfma_f32_16x16x32_f16 v[80:83], v[234:237], v[210:213], v[80:83]
	v_mfma_f32_16x16x32_f16 v[120:123], v[234:237], v[218:221], v[120:123]
	v_mfma_f32_16x16x32_f16 v[124:127], v[238:241], v[206:209], v[124:127]
	v_mfma_f32_16x16x32_f16 v[146:149], v[238:241], v[214:217], v[146:149]
	v_mfma_f32_16x16x32_f16 v[134:137], v[238:241], v[218:221], v[134:137]
	v_mfma_f32_16x16x32_f16 v[242:245], v[234:237], v[206:209], v[8:11]
	v_mfma_f32_16x16x32_f16 v[138:141], v[234:237], v[214:217], v[138:141]
	v_mfma_f32_16x16x32_f16 v[142:145], v[238:241], v[210:213], v[142:145]
	s_setprio 0
	ds_read_b128 v[8:11], v130 offset:8192
	ds_read_b128 v[234:237], v130 offset:10240
	v_cvt_pk_f16_f32 v59, v58, v59
	v_cvt_pk_f16_f32 v58, v56, v57
	ds_write_b64 v100, v[58:59] offset:57344
	s_add_u32 s80, s22, 0xc0b00
	s_addc_u32 s81, s90, 0
	global_load_dwordx4 v[56:59], v201, s[80:81] nt
	s_setprio 1
	s_waitcnt lgkmcnt(1)
	v_mfma_f32_16x16x32_f16 v[84:87], v[8:11], v[210:213], v[84:87]
	v_mfma_f32_16x16x32_f16 v[238:241], v[8:11], v[206:209], v[68:71]
	v_mfma_f32_16x16x32_f16 v[170:173], v[8:11], v[214:217], v[170:173]
	v_mfma_f32_16x16x32_f16 v[150:153], v[8:11], v[218:221], v[150:153]
	v_mfma_f32_16x16x32_f16 v[162:165], v[234:237], v[206:209], v[162:165]
	v_mfma_f32_16x16x32_f16 v[174:177], v[234:237], v[210:213], v[174:177]
	v_mfma_f32_16x16x32_f16 v[178:181], v[234:237], v[214:217], v[178:181]
	v_mfma_f32_16x16x32_f16 v[154:157], v[234:237], v[218:221], v[154:157]
	s_setprio 0
	ds_read_b128 v[8:11], v130 offset:12288
	ds_read_b128 v[68:71], v130 offset:14336
	v_cvt_pk_f16_f32 v63, v62, v63
	v_cvt_pk_f16_f32 v62, v60, v61
	ds_write_b64 v100, v[62:63] offset:61440
	s_add_u32 s80, s22, 0xe0b00
	s_addc_u32 s81, s90, 0
	global_load_dwordx4 v[60:63], v201, s[80:81] nt
	s_setprio 1
	s_waitcnt lgkmcnt(1)
	v_mfma_f32_16x16x32_f16 v[88:91], v[8:11], v[210:213], v[88:91]
	v_mfma_f32_16x16x32_f16 v[234:237], v[8:11], v[206:209], v[72:75]
	v_mfma_f32_16x16x32_f16 v[158:161], v[8:11], v[214:217], v[158:161]
	v_mfma_f32_16x16x32_f16 v[166:169], v[8:11], v[218:221], v[166:169]
	v_mfma_f32_16x16x32_f16 v[182:185], v[68:71], v[206:209], v[182:185]
	v_mfma_f32_16x16x32_f16 v[190:193], v[68:71], v[210:213], v[190:193]
	v_mfma_f32_16x16x32_f16 v[202:205], v[68:71], v[214:217], v[202:205]
	v_mfma_f32_16x16x32_f16 v[186:189], v[68:71], v[218:221], v[186:189]
	s_setprio 0
	s_waitcnt vmcnt(4)
	s_waitcnt lgkmcnt(0)
	s_barrier
	ds_read_b128 v[206:209], v131 offset:32768
	ds_read_b128 v[210:213], v131 offset:34816
	ds_read_b128 v[214:217], v131 offset:36864
	ds_read_b128 v[218:221], v131 offset:38912
	ds_read_b128 v[68:71], v129 offset:32768
	ds_read_b128 v[72:75], v129 offset:34816
	s_add_u32 s80, s22, 0xc00
	v_lshl_add_u64 v[92:93], s[46:47], 0, v[196:197]
	s_addc_u32 s81, s90, 0
	v_readfirstlane_b32 s1, v94
	s_mov_b32 m0, s1
	v_cvt_pk_f16_f32 v3, v2, v3
	global_load_lds_dwordx4 v[92:93], off
	v_cvt_pk_f16_f32 v2, v0, v1
	ds_write_b64 v100, v[2:3]
	global_load_dwordx4 v[8:11], v201, s[80:81] nt
	s_setprio 1
	s_waitcnt lgkmcnt(1)
	v_mfma_f32_16x16x32_f16 v[0:3], v[68:71], v[206:209], v[76:79]
	v_mfma_f32_16x16x32_f16 v[104:107], v[68:71], v[214:217], v[104:107]
	v_mfma_f32_16x16x32_f16 v[108:111], v[72:75], v[206:209], v[108:111]
	v_mfma_f32_16x16x32_f16 v[112:115], v[72:75], v[210:213], v[112:115]
	v_mfma_f32_16x16x32_f16 v[116:119], v[72:75], v[214:217], v[116:119]
	v_mfma_f32_16x16x32_f16 v[230:233], v[68:71], v[210:213], v[230:233]
	v_mfma_f32_16x16x32_f16 v[222:225], v[68:71], v[218:221], v[222:225]
	v_mfma_f32_16x16x32_f16 v[226:229], v[72:75], v[218:221], v[226:229]
	s_setprio 0
	ds_read_b128 v[72:75], v129 offset:36864
	ds_read_b128 v[76:79], v129 offset:38912
	v_readfirstlane_b32 s92, v99
	v_lshl_add_u64 v[68:69], v[92:93], 0, s[58:59]
	s_mov_b32 m0, s92
	v_cvt_pk_f16_f32 v15, v14, v15
	global_load_lds_dwordx4 v[68:69], off
	v_cvt_pk_f16_f32 v14, v12, v13
	ds_write_b64 v100, v[14:15] offset:4096
	s_add_u32 s80, s22, 0x20c00
	s_addc_u32 s81, s90, 0
	global_load_dwordx4 v[68:71], v201, s[80:81] nt
	s_setprio 1
	s_waitcnt lgkmcnt(1)
	v_mfma_f32_16x16x32_f16 v[12:15], v[72:75], v[206:209], v[242:245]
	v_mfma_f32_16x16x32_f16 v[120:123], v[72:75], v[218:221], v[120:123]
	v_mfma_f32_16x16x32_f16 v[124:127], v[76:79], v[206:209], v[124:127]
	v_mfma_f32_16x16x32_f16 v[146:149], v[76:79], v[214:217], v[146:149]
	v_mfma_f32_16x16x32_f16 v[134:137], v[76:79], v[218:221], v[134:137]
	v_mfma_f32_16x16x32_f16 v[242:245], v[72:75], v[210:213], v[80:83]
	v_mfma_f32_16x16x32_f16 v[138:141], v[72:75], v[214:217], v[138:141]
	v_mfma_f32_16x16x32_f16 v[142:145], v[76:79], v[210:213], v[142:145]
	s_setprio 0
	ds_read_b128 v[76:79], v129 offset:40960
	ds_read_b128 v[80:83], v129 offset:43008
	v_readfirstlane_b32 s91, v101
	v_lshl_add_u64 v[72:73], v[92:93], 0, s[60:61]
	s_mov_b32 m0, s91
	v_cvt_pk_f16_f32 v19, v18, v19
	global_load_lds_dwordx4 v[72:73], off
	v_cvt_pk_f16_f32 v18, v16, v17
	ds_write_b64 v100, v[18:19] offset:8192
	s_add_u32 s80, s22, 0x40c00
	s_addc_u32 s81, s90, 0
	global_load_dwordx4 v[72:75], v201, s[80:81] nt
	s_setprio 1
	s_waitcnt lgkmcnt(1)
	v_mfma_f32_16x16x32_f16 v[16:19], v[76:79], v[206:209], v[238:241]
	v_mfma_f32_16x16x32_f16 v[238:241], v[76:79], v[210:213], v[84:87]
	v_mfma_f32_16x16x32_f16 v[170:173], v[76:79], v[214:217], v[170:173]
	v_mfma_f32_16x16x32_f16 v[150:153], v[76:79], v[218:221], v[150:153]
	v_mfma_f32_16x16x32_f16 v[162:165], v[80:83], v[206:209], v[162:165]
	v_mfma_f32_16x16x32_f16 v[174:177], v[80:83], v[210:213], v[174:177]
	v_mfma_f32_16x16x32_f16 v[178:181], v[80:83], v[214:217], v[178:181]
	v_mfma_f32_16x16x32_f16 v[154:157], v[80:83], v[218:221], v[154:157]
	s_setprio 0
	ds_read_b128 v[80:83], v129 offset:45056
	ds_read_b128 v[84:87], v129 offset:47104
	v_readfirstlane_b32 s73, v102
	v_lshl_add_u64 v[76:77], v[92:93], 0, s[62:63]
	s_mov_b32 m0, s73
	v_cvt_pk_f16_f32 v23, v22, v23
	global_load_lds_dwordx4 v[76:77], off
	v_cvt_pk_f16_f32 v22, v20, v21
	ds_write_b64 v100, v[22:23] offset:12288
	s_add_u32 s80, s22, 0x60c00
	s_addc_u32 s81, s90, 0
	global_load_dwordx4 v[76:79], v201, s[80:81] nt
	s_setprio 1
	s_waitcnt lgkmcnt(1)
	v_mfma_f32_16x16x32_f16 v[20:23], v[80:83], v[206:209], v[234:237]
	v_mfma_f32_16x16x32_f16 v[234:237], v[80:83], v[210:213], v[88:91]
	v_mfma_f32_16x16x32_f16 v[158:161], v[80:83], v[214:217], v[158:161]
	v_mfma_f32_16x16x32_f16 v[166:169], v[80:83], v[218:221], v[166:169]
	v_mfma_f32_16x16x32_f16 v[182:185], v[84:87], v[206:209], v[182:185]
	v_mfma_f32_16x16x32_f16 v[190:193], v[84:87], v[210:213], v[190:193]
	v_mfma_f32_16x16x32_f16 v[202:205], v[84:87], v[214:217], v[202:205]
	v_mfma_f32_16x16x32_f16 v[186:189], v[84:87], v[218:221], v[186:189]
	s_setprio 0
	ds_read_b128 v[206:209], v128 offset:32768
	ds_read_b128 v[210:213], v128 offset:34816
	ds_read_b128 v[214:217], v128 offset:36864
	ds_read_b128 v[218:221], v128 offset:38912
	ds_read_b128 v[84:87], v130 offset:32768
	ds_read_b128 v[88:91], v130 offset:34816
	v_cvt_pk_f16_f32 v27, v26, v27
	v_cvt_pk_f16_f32 v26, v24, v25
	ds_write_b64 v100, v[26:27] offset:16384
	s_add_u32 s80, s22, 0x80c00
	s_addc_u32 s81, s90, 0
	global_load_dwordx4 v[80:83], v201, s[80:81] nt
	s_setprio 1
	s_waitcnt lgkmcnt(1)
	v_mfma_f32_16x16x32_f16 v[24:27], v[84:87], v[206:209], v[0:3]
	v_mfma_f32_16x16x32_f16 v[104:107], v[84:87], v[214:217], v[104:107]
	v_mfma_f32_16x16x32_f16 v[108:111], v[88:91], v[206:209], v[108:111]
	v_mfma_f32_16x16x32_f16 v[112:115], v[88:91], v[210:213], v[112:115]
	v_mfma_f32_16x16x32_f16 v[116:119], v[88:91], v[214:217], v[116:119]
	v_mfma_f32_16x16x32_f16 v[230:233], v[84:87], v[210:213], v[230:233]
	v_mfma_f32_16x16x32_f16 v[222:225], v[84:87], v[218:221], v[222:225]
	v_mfma_f32_16x16x32_f16 v[226:229], v[88:91], v[218:221], v[226:229]
	s_setprio 0
	ds_read_b128 v[0:3], v130 offset:36864
	ds_read_b128 v[88:91], v130 offset:38912
	v_cvt_pk_f16_f32 v31, v30, v31
	v_cvt_pk_f16_f32 v30, v28, v29
	ds_write_b64 v100, v[30:31] offset:20480
	s_add_u32 s80, s22, 0xa0c00
	s_addc_u32 s81, s90, 0
	global_load_dwordx4 v[84:87], v201, s[80:81] nt
	s_setprio 1
	s_waitcnt lgkmcnt(1)
	v_mfma_f32_16x16x32_f16 v[12:15], v[0:3], v[206:209], v[12:15]
	v_mfma_f32_16x16x32_f16 v[28:31], v[0:3], v[210:213], v[242:245]
	v_mfma_f32_16x16x32_f16 v[120:123], v[0:3], v[218:221], v[120:123]
	v_mfma_f32_16x16x32_f16 v[124:127], v[88:91], v[206:209], v[124:127]
	v_mfma_f32_16x16x32_f16 v[146:149], v[88:91], v[214:217], v[146:149]
	v_mfma_f32_16x16x32_f16 v[134:137], v[88:91], v[218:221], v[134:137]
	v_mfma_f32_16x16x32_f16 v[138:141], v[0:3], v[214:217], v[138:141]
	v_mfma_f32_16x16x32_f16 v[142:145], v[88:91], v[210:213], v[142:145]
	s_setprio 0
	ds_read_b128 v[0:3], v130 offset:40960
	ds_read_b128 v[242:245], v130 offset:43008
	v_cvt_pk_f16_f32 v35, v34, v35
	v_cvt_pk_f16_f32 v34, v32, v33
	ds_write_b64 v100, v[34:35] offset:24576
	s_add_u32 s80, s22, 0xc0c00
	s_addc_u32 s81, s90, 0
	global_load_dwordx4 v[88:91], v201, s[80:81] nt
	s_setprio 1
	s_waitcnt lgkmcnt(1)
	v_mfma_f32_16x16x32_f16 v[16:19], v[0:3], v[206:209], v[16:19]
	v_mfma_f32_16x16x32_f16 v[32:35], v[0:3], v[210:213], v[238:241]
	v_mfma_f32_16x16x32_f16 v[170:173], v[0:3], v[214:217], v[170:173]
	v_mfma_f32_16x16x32_f16 v[150:153], v[0:3], v[218:221], v[150:153]
	v_mfma_f32_16x16x32_f16 v[162:165], v[242:245], v[206:209], v[162:165]
	v_mfma_f32_16x16x32_f16 v[174:177], v[242:245], v[210:213], v[174:177]
	v_mfma_f32_16x16x32_f16 v[178:181], v[242:245], v[214:217], v[178:181]
	v_mfma_f32_16x16x32_f16 v[154:157], v[242:245], v[218:221], v[154:157]
	s_setprio 0
	ds_read_b128 v[0:3], v130 offset:45056
	ds_read_b128 v[238:241], v130 offset:47104
	v_cvt_pk_f16_f32 v39, v38, v39
	v_cvt_pk_f16_f32 v38, v36, v37
	ds_write_b64 v100, v[38:39] offset:28672
	s_add_u32 s80, s22, 0xe0c00
	s_addc_u32 s81, s90, 0
	global_load_dwordx4 v[36:39], v201, s[80:81] nt
	s_setprio 1
	s_waitcnt lgkmcnt(1)
	v_mfma_f32_16x16x32_f16 v[20:23], v[0:3], v[206:209], v[20:23]
	v_mfma_f32_16x16x32_f16 v[234:237], v[0:3], v[210:213], v[234:237]
	v_mfma_f32_16x16x32_f16 v[158:161], v[0:3], v[214:217], v[158:161]
	v_mfma_f32_16x16x32_f16 v[166:169], v[0:3], v[218:221], v[166:169]
	v_mfma_f32_16x16x32_f16 v[182:185], v[238:241], v[206:209], v[182:185]
	v_mfma_f32_16x16x32_f16 v[190:193], v[238:241], v[210:213], v[190:193]
	v_mfma_f32_16x16x32_f16 v[202:205], v[238:241], v[214:217], v[202:205]
	v_mfma_f32_16x16x32_f16 v[186:189], v[238:241], v[218:221], v[186:189]
	s_setprio 0
	s_waitcnt vmcnt(4)
	s_waitcnt lgkmcnt(0)
	s_barrier
	ds_read_b128 v[206:209], v131
	ds_read_b128 v[210:213], v131 offset:2048
	ds_read_b128 v[214:217], v131 offset:4096
	ds_read_b128 v[218:221], v131 offset:6144
	ds_read_b128 v[238:241], v129
	ds_read_b128 v[242:245], v129 offset:2048
	s_add_u32 s80, s22, 0xd00
	v_lshl_add_u64 v[92:93], s[48:49], 0, v[196:197]
	s_addc_u32 s81, s90, 0
	s_mov_b32 m0, s0
	v_cvt_pk_f16_f32 v1, v6, v7
	global_load_lds_dwordx4 v[92:93], off
	v_cvt_pk_f16_f32 v0, v4, v5
	ds_write_b64 v100, v[0:1] offset:32768
	global_load_dwordx4 v[0:3], v201, s[80:81] nt
	s_setprio 1
	s_waitcnt lgkmcnt(1)
	v_mfma_f32_16x16x32_f16 v[24:27], v[238:241], v[206:209], v[24:27]
	v_mfma_f32_16x16x32_f16 v[104:107], v[238:241], v[214:217], v[104:107]
	v_mfma_f32_16x16x32_f16 v[108:111], v[242:245], v[206:209], v[108:111]
	v_mfma_f32_16x16x32_f16 v[112:115], v[242:245], v[210:213], v[112:115]
	v_mfma_f32_16x16x32_f16 v[116:119], v[242:245], v[214:217], v[116:119]
	v_mfma_f32_16x16x32_f16 v[230:233], v[238:241], v[210:213], v[230:233]
	v_mfma_f32_16x16x32_f16 v[222:225], v[238:241], v[218:221], v[222:225]
	v_mfma_f32_16x16x32_f16 v[226:229], v[242:245], v[218:221], v[226:229]
	s_setprio 0
	ds_read_b128 v[238:241], v129 offset:4096
	ds_read_b128 v[242:245], v129 offset:6144
	s_mov_b32 m0, s72
	v_lshl_add_u64 v[4:5], v[92:93], 0, s[58:59]
	global_load_lds_dwordx4 v[4:5], off
	v_cvt_pk_f16_f32 v5, v66, v67
	v_cvt_pk_f16_f32 v4, v64, v65
	ds_write_b64 v100, v[4:5] offset:36864
	s_add_u32 s80, s22, 0x20d00
	s_addc_u32 s81, s90, 0
	global_load_dwordx4 v[4:7], v201, s[80:81] nt
	s_setprio 1
	s_waitcnt lgkmcnt(1)
	v_mfma_f32_16x16x32_f16 v[64:67], v[238:241], v[206:209], v[12:15]
	v_mfma_f32_16x16x32_f16 v[28:31], v[238:241], v[210:213], v[28:31]
	v_mfma_f32_16x16x32_f16 v[120:123], v[238:241], v[218:221], v[120:123]
	v_mfma_f32_16x16x32_f16 v[124:127], v[242:245], v[206:209], v[124:127]
	v_mfma_f32_16x16x32_f16 v[146:149], v[242:245], v[214:217], v[146:149]
	v_mfma_f32_16x16x32_f16 v[134:137], v[242:245], v[218:221], v[134:137]
	v_mfma_f32_16x16x32_f16 v[138:141], v[238:241], v[214:217], v[138:141]
	v_mfma_f32_16x16x32_f16 v[142:145], v[242:245], v[210:213], v[142:145]
	s_setprio 0
	ds_read_b128 v[238:241], v129 offset:8192
	ds_read_b128 v[242:245], v129 offset:10240
	s_mov_b32 m0, s71
	v_lshl_add_u64 v[12:13], v[92:93], 0, s[60:61]
	global_load_lds_dwordx4 v[12:13], off
	v_cvt_pk_f16_f32 v13, v42, v43
	v_cvt_pk_f16_f32 v12, v40, v41
	ds_write_b64 v100, v[12:13] offset:40960
	s_add_u32 s80, s22, 0x40d00
	s_addc_u32 s81, s90, 0
	global_load_dwordx4 v[12:15], v201, s[80:81] nt
	s_setprio 1
	s_waitcnt lgkmcnt(1)
	v_mfma_f32_16x16x32_f16 v[40:43], v[238:241], v[206:209], v[16:19]
	v_mfma_f32_16x16x32_f16 v[32:35], v[238:241], v[210:213], v[32:35]
	v_mfma_f32_16x16x32_f16 v[170:173], v[238:241], v[214:217], v[170:173]
	v_mfma_f32_16x16x32_f16 v[150:153], v[238:241], v[218:221], v[150:153]
	v_mfma_f32_16x16x32_f16 v[162:165], v[242:245], v[206:209], v[162:165]
	v_mfma_f32_16x16x32_f16 v[174:177], v[242:245], v[210:213], v[174:177]
	v_mfma_f32_16x16x32_f16 v[178:181], v[242:245], v[214:217], v[178:181]
	v_mfma_f32_16x16x32_f16 v[154:157], v[242:245], v[218:221], v[154:157]
	s_setprio 0
	ds_read_b128 v[238:241], v129 offset:12288
	ds_read_b128 v[242:245], v129 offset:14336
	s_mov_b32 m0, s70
	v_lshl_add_u64 v[16:17], v[92:93], 0, s[62:63]
	global_load_lds_dwordx4 v[16:17], off
	v_cvt_pk_f16_f32 v17, v46, v47
	v_cvt_pk_f16_f32 v16, v44, v45
	ds_write_b64 v100, v[16:17] offset:45056
	s_add_u32 s70, s22, 0x60d00
	s_addc_u32 s71, s90, 0
	global_load_dwordx4 v[16:19], v201, s[70:71] nt
	s_setprio 1
	s_waitcnt lgkmcnt(1)
	v_mfma_f32_16x16x32_f16 v[44:47], v[238:241], v[206:209], v[20:23]
	v_mfma_f32_16x16x32_f16 v[234:237], v[238:241], v[210:213], v[234:237]
	v_mfma_f32_16x16x32_f16 v[158:161], v[238:241], v[214:217], v[158:161]
	v_mfma_f32_16x16x32_f16 v[166:169], v[238:241], v[218:221], v[166:169]
	v_mfma_f32_16x16x32_f16 v[182:185], v[242:245], v[206:209], v[182:185]
	v_mfma_f32_16x16x32_f16 v[190:193], v[242:245], v[210:213], v[190:193]
	v_mfma_f32_16x16x32_f16 v[202:205], v[242:245], v[214:217], v[202:205]
	v_mfma_f32_16x16x32_f16 v[186:189], v[242:245], v[218:221], v[186:189]
	s_setprio 0
	ds_read_b128 v[206:209], v128
	ds_read_b128 v[210:213], v128 offset:2048
	ds_read_b128 v[214:217], v128 offset:4096
	ds_read_b128 v[218:221], v128 offset:6144
	ds_read_b128 v[238:241], v130
	ds_read_b128 v[242:245], v130 offset:2048
	v_cvt_pk_f16_f32 v21, v50, v51
	v_cvt_pk_f16_f32 v20, v48, v49
	ds_write_b64 v100, v[20:21] offset:49152
	s_add_u32 s70, s22, 0x80d00
	s_addc_u32 s71, s90, 0
	global_load_dwordx4 v[20:23], v201, s[70:71] nt
	s_setprio 1
	s_waitcnt lgkmcnt(1)
	v_mfma_f32_16x16x32_f16 v[48:51], v[238:241], v[206:209], v[24:27]
	v_mfma_f32_16x16x32_f16 v[104:107], v[238:241], v[214:217], v[104:107]
	v_mfma_f32_16x16x32_f16 v[108:111], v[242:245], v[206:209], v[108:111]
	v_mfma_f32_16x16x32_f16 v[112:115], v[242:245], v[210:213], v[112:115]
	v_mfma_f32_16x16x32_f16 v[116:119], v[242:245], v[214:217], v[116:119]
	v_mfma_f32_16x16x32_f16 v[230:233], v[238:241], v[210:213], v[230:233]
	v_mfma_f32_16x16x32_f16 v[222:225], v[238:241], v[218:221], v[222:225]
	v_mfma_f32_16x16x32_f16 v[226:229], v[242:245], v[218:221], v[226:229]
	s_setprio 0
	ds_read_b128 v[238:241], v130 offset:4096
	ds_read_b128 v[242:245], v130 offset:6144
	v_cvt_pk_f16_f32 v25, v54, v55
	v_cvt_pk_f16_f32 v24, v52, v53
	ds_write_b64 v100, v[24:25] offset:53248
	s_add_u32 s70, s22, 0xa0d00
	s_addc_u32 s71, s90, 0
	global_load_dwordx4 v[24:27], v201, s[70:71] nt
	s_setprio 1
	s_waitcnt lgkmcnt(1)
	v_mfma_f32_16x16x32_f16 v[52:55], v[238:241], v[206:209], v[64:67]
	v_mfma_f32_16x16x32_f16 v[64:67], v[238:241], v[210:213], v[28:31]
	v_mfma_f32_16x16x32_f16 v[120:123], v[238:241], v[218:221], v[120:123]
	v_mfma_f32_16x16x32_f16 v[124:127], v[242:245], v[206:209], v[124:127]
	v_mfma_f32_16x16x32_f16 v[146:149], v[242:245], v[214:217], v[146:149]
	v_mfma_f32_16x16x32_f16 v[134:137], v[242:245], v[218:221], v[134:137]
	v_mfma_f32_16x16x32_f16 v[138:141], v[238:241], v[214:217], v[138:141]
	v_mfma_f32_16x16x32_f16 v[142:145], v[242:245], v[210:213], v[142:145]
	s_setprio 0
	ds_read_b128 v[238:241], v130 offset:8192
	ds_read_b128 v[242:245], v130 offset:10240
	v_cvt_pk_f16_f32 v29, v58, v59
	v_cvt_pk_f16_f32 v28, v56, v57
	ds_write_b64 v100, v[28:29] offset:57344
	s_add_u32 s70, s22, 0xc0d00
	s_addc_u32 s71, s90, 0
	global_load_dwordx4 v[28:31], v201, s[70:71] nt
	s_setprio 1
	s_waitcnt lgkmcnt(1)
	v_mfma_f32_16x16x32_f16 v[56:59], v[238:241], v[206:209], v[40:43]
	v_mfma_f32_16x16x32_f16 v[246:249], v[238:241], v[210:213], v[32:35]
	v_mfma_f32_16x16x32_f16 v[170:173], v[238:241], v[214:217], v[170:173]
	v_mfma_f32_16x16x32_f16 v[150:153], v[238:241], v[218:221], v[150:153]
	v_mfma_f32_16x16x32_f16 v[162:165], v[242:245], v[206:209], v[162:165]
	v_mfma_f32_16x16x32_f16 v[174:177], v[242:245], v[210:213], v[174:177]
	v_mfma_f32_16x16x32_f16 v[178:181], v[242:245], v[214:217], v[178:181]
	v_mfma_f32_16x16x32_f16 v[154:157], v[242:245], v[218:221], v[154:157]
	s_setprio 0
	ds_read_b128 v[40:43], v130 offset:12288
	ds_read_b128 v[238:241], v130 offset:14336
	v_cvt_pk_f16_f32 v33, v62, v63
	v_cvt_pk_f16_f32 v32, v60, v61
	ds_write_b64 v100, v[32:33] offset:61440
	s_add_u32 s70, s22, 0xe0d00
	s_addc_u32 s71, s90, 0
	global_load_dwordx4 v[32:35], v201, s[70:71] nt
	s_setprio 1
	s_waitcnt lgkmcnt(1)
	v_mfma_f32_16x16x32_f16 v[60:63], v[40:43], v[206:209], v[44:47]
	v_mfma_f32_16x16x32_f16 v[234:237], v[40:43], v[210:213], v[234:237]
	v_mfma_f32_16x16x32_f16 v[158:161], v[40:43], v[214:217], v[158:161]
	v_mfma_f32_16x16x32_f16 v[166:169], v[40:43], v[218:221], v[166:169]
	v_mfma_f32_16x16x32_f16 v[182:185], v[238:241], v[206:209], v[182:185]
	v_mfma_f32_16x16x32_f16 v[190:193], v[238:241], v[210:213], v[190:193]
	v_mfma_f32_16x16x32_f16 v[202:205], v[238:241], v[214:217], v[202:205]
	v_mfma_f32_16x16x32_f16 v[186:189], v[238:241], v[218:221], v[186:189]
	s_setprio 0
	s_waitcnt vmcnt(4)
	s_waitcnt lgkmcnt(0)
	s_barrier
	ds_read_b128 v[206:209], v131 offset:32768
	ds_read_b128 v[210:213], v131 offset:34816
	ds_read_b128 v[214:217], v131 offset:36864
	ds_read_b128 v[218:221], v131 offset:38912
	ds_read_b128 v[40:43], v129 offset:32768
	ds_read_b128 v[44:47], v129 offset:34816
	s_add_u32 s70, s22, 0xe00
	v_lshl_add_u64 v[92:93], s[50:51], 0, v[196:197]
	s_addc_u32 s71, s90, 0
	s_mov_b32 m0, s1
	v_cvt_pk_f16_f32 v11, v10, v11
	global_load_lds_dwordx4 v[92:93], off
	v_cvt_pk_f16_f32 v10, v8, v9
	ds_write_b64 v100, v[10:11]
	global_load_dwordx4 v[8:11], v201, s[70:71] nt
	s_setprio 1
	s_waitcnt lgkmcnt(1)
	v_mfma_f32_16x16x32_f16 v[104:107], v[40:43], v[214:217], v[104:107]
	v_mfma_f32_16x16x32_f16 v[108:111], v[44:47], v[206:209], v[108:111]
	v_mfma_f32_16x16x32_f16 v[112:115], v[44:47], v[210:213], v[112:115]
	v_mfma_f32_16x16x32_f16 v[116:119], v[44:47], v[214:217], v[116:119]
	v_mfma_f32_16x16x32_f16 v[238:241], v[40:43], v[206:209], v[48:51]
	v_mfma_f32_16x16x32_f16 v[230:233], v[40:43], v[210:213], v[230:233]
	v_mfma_f32_16x16x32_f16 v[222:225], v[40:43], v[218:221], v[222:225]
	v_mfma_f32_16x16x32_f16 v[226:229], v[44:47], v[218:221], v[226:229]
	s_setprio 0
	ds_read_b128 v[44:47], v129 offset:36864
	ds_read_b128 v[48:51], v129 offset:38912
	s_mov_b32 m0, s92
	v_lshl_add_u64 v[40:41], v[92:93], 0, s[58:59]
	global_load_lds_dwordx4 v[40:41], off
	v_cvt_pk_f16_f32 v41, v70, v71
	v_cvt_pk_f16_f32 v40, v68, v69
	ds_write_b64 v100, v[40:41] offset:4096
	s_add_u32 s0, s22, 0x20e00
	s_addc_u32 s1, s90, 0
	global_load_dwordx4 v[40:43], v201, s[0:1] nt
	s_setprio 1
	s_waitcnt lgkmcnt(1)
	v_mfma_f32_16x16x32_f16 v[68:71], v[44:47], v[206:209], v[52:55]
	v_mfma_f32_16x16x32_f16 v[64:67], v[44:47], v[210:213], v[64:67]
	v_mfma_f32_16x16x32_f16 v[120:123], v[44:47], v[218:221], v[120:123]
	v_mfma_f32_16x16x32_f16 v[124:127], v[48:51], v[206:209], v[124:127]
	v_mfma_f32_16x16x32_f16 v[146:149], v[48:51], v[214:217], v[146:149]
	v_mfma_f32_16x16x32_f16 v[134:137], v[48:51], v[218:221], v[134:137]
	v_mfma_f32_16x16x32_f16 v[138:141], v[44:47], v[214:217], v[138:141]
	v_mfma_f32_16x16x32_f16 v[142:145], v[48:51], v[210:213], v[142:145]
	s_setprio 0
	ds_read_b128 v[48:51], v129 offset:40960
	ds_read_b128 v[52:55], v129 offset:43008
	s_mov_b32 m0, s91
	v_lshl_add_u64 v[44:45], v[92:93], 0, s[60:61]
	global_load_lds_dwordx4 v[44:45], off
	v_cvt_pk_f16_f32 v45, v74, v75
	v_cvt_pk_f16_f32 v44, v72, v73
	ds_write_b64 v100, v[44:45] offset:8192
	s_add_u32 s0, s22, 0x40e00
	s_addc_u32 s1, s90, 0
	global_load_dwordx4 v[44:47], v201, s[0:1] nt
	s_setprio 1
	s_waitcnt lgkmcnt(1)
	v_mfma_f32_16x16x32_f16 v[72:75], v[48:51], v[206:209], v[56:59]
	v_mfma_f32_16x16x32_f16 v[242:245], v[48:51], v[210:213], v[246:249]
	v_mfma_f32_16x16x32_f16 v[170:173], v[48:51], v[214:217], v[170:173]
	v_mfma_f32_16x16x32_f16 v[150:153], v[48:51], v[218:221], v[150:153]
	v_mfma_f32_16x16x32_f16 v[162:165], v[52:55], v[206:209], v[162:165]
	v_mfma_f32_16x16x32_f16 v[174:177], v[52:55], v[210:213], v[174:177]
	v_mfma_f32_16x16x32_f16 v[178:181], v[52:55], v[214:217], v[178:181]
	v_mfma_f32_16x16x32_f16 v[154:157], v[52:55], v[218:221], v[154:157]
	s_setprio 0
	ds_read_b128 v[52:55], v129 offset:45056
	ds_read_b128 v[56:59], v129 offset:47104
	s_mov_b32 m0, s73
	v_lshl_add_u64 v[48:49], v[92:93], 0, s[62:63]
	global_load_lds_dwordx4 v[48:49], off
	v_cvt_pk_f16_f32 v49, v78, v79
	v_cvt_pk_f16_f32 v48, v76, v77
	ds_write_b64 v100, v[48:49] offset:12288
	s_add_u32 s0, s22, 0x60e00
	s_addc_u32 s1, s90, 0
	global_load_dwordx4 v[48:51], v201, s[0:1] nt
	s_setprio 1
	s_waitcnt lgkmcnt(1)
	v_mfma_f32_16x16x32_f16 v[76:79], v[52:55], v[206:209], v[60:63]
	v_mfma_f32_16x16x32_f16 v[234:237], v[52:55], v[210:213], v[234:237]
	v_mfma_f32_16x16x32_f16 v[158:161], v[52:55], v[214:217], v[158:161]
	v_mfma_f32_16x16x32_f16 v[166:169], v[52:55], v[218:221], v[166:169]
	v_mfma_f32_16x16x32_f16 v[182:185], v[56:59], v[206:209], v[182:185]
	v_mfma_f32_16x16x32_f16 v[190:193], v[56:59], v[210:213], v[190:193]
	v_mfma_f32_16x16x32_f16 v[202:205], v[56:59], v[214:217], v[202:205]
	v_mfma_f32_16x16x32_f16 v[186:189], v[56:59], v[218:221], v[186:189]
	s_setprio 0
	ds_read_b128 v[206:209], v128 offset:32768
	ds_read_b128 v[210:213], v128 offset:34816
	ds_read_b128 v[214:217], v128 offset:36864
	ds_read_b128 v[218:221], v128 offset:38912
	ds_read_b128 v[56:59], v130 offset:32768
	ds_read_b128 v[60:63], v130 offset:34816
	v_cvt_pk_f16_f32 v53, v82, v83
	v_cvt_pk_f16_f32 v52, v80, v81
	ds_write_b64 v100, v[52:53] offset:16384
	s_add_u32 s0, s22, 0x80e00
	s_addc_u32 s1, s90, 0
	global_load_dwordx4 v[52:55], v201, s[0:1] nt
	s_setprio 1
	s_waitcnt lgkmcnt(1)
	v_mfma_f32_16x16x32_f16 v[80:83], v[56:59], v[206:209], v[238:241]
	v_mfma_f32_16x16x32_f16 v[104:107], v[56:59], v[214:217], v[104:107]
	v_mfma_f32_16x16x32_f16 v[108:111], v[60:63], v[206:209], v[108:111]
	v_mfma_f32_16x16x32_f16 v[112:115], v[60:63], v[210:213], v[112:115]
	v_mfma_f32_16x16x32_f16 v[116:119], v[60:63], v[214:217], v[116:119]
	v_mfma_f32_16x16x32_f16 v[230:233], v[56:59], v[210:213], v[230:233]
	v_mfma_f32_16x16x32_f16 v[222:225], v[56:59], v[218:221], v[222:225]
	v_mfma_f32_16x16x32_f16 v[226:229], v[60:63], v[218:221], v[226:229]
	s_setprio 0
	ds_read_b128 v[60:63], v130 offset:36864
	ds_read_b128 v[238:241], v130 offset:38912
	v_cvt_pk_f16_f32 v57, v86, v87
	v_cvt_pk_f16_f32 v56, v84, v85
	ds_write_b64 v100, v[56:57] offset:20480
	s_add_u32 s0, s22, 0xa0e00
	s_addc_u32 s1, s90, 0
	global_load_dwordx4 v[56:59], v201, s[0:1] nt
	s_setprio 1
	s_waitcnt lgkmcnt(1)
	v_mfma_f32_16x16x32_f16 v[68:71], v[60:63], v[206:209], v[68:71]
	v_mfma_f32_16x16x32_f16 v[64:67], v[60:63], v[210:213], v[64:67]
	v_mfma_f32_16x16x32_f16 v[84:87], v[60:63], v[214:217], v[138:141]
	v_mfma_f32_16x16x32_f16 v[120:123], v[60:63], v[218:221], v[120:123]
	v_mfma_f32_16x16x32_f16 v[124:127], v[238:241], v[206:209], v[124:127]
	v_mfma_f32_16x16x32_f16 v[134:137], v[238:241], v[218:221], v[134:137]
	v_mfma_f32_16x16x32_f16 v[138:141], v[238:241], v[210:213], v[142:145]
	v_mfma_f32_16x16x32_f16 v[142:145], v[238:241], v[214:217], v[146:149]
	s_setprio 0
	s_nop 1
	ds_read_b128 v[146:149], v130 offset:40960
	ds_read_b128 v[238:241], v130 offset:43008
	v_cvt_pk_f16_f32 v61, v90, v91
	v_cvt_pk_f16_f32 v60, v88, v89
	ds_write_b64 v100, v[60:61] offset:24576
	s_add_u32 s0, s22, 0xc0e00
	s_addc_u32 s1, s90, 0
	global_load_dwordx4 v[60:63], v201, s[0:1] nt
	s_setprio 1
	s_waitcnt lgkmcnt(1)
	v_mfma_f32_16x16x32_f16 v[72:75], v[146:149], v[206:209], v[72:75]
	v_mfma_f32_16x16x32_f16 v[88:91], v[146:149], v[210:213], v[242:245]
	v_mfma_f32_16x16x32_f16 v[170:173], v[146:149], v[214:217], v[170:173]
	v_mfma_f32_16x16x32_f16 v[146:149], v[146:149], v[218:221], v[150:153]
	v_mfma_f32_16x16x32_f16 v[150:153], v[238:241], v[206:209], v[162:165]
	v_mfma_f32_16x16x32_f16 v[162:165], v[238:241], v[210:213], v[174:177]
	v_mfma_f32_16x16x32_f16 v[174:177], v[238:241], v[214:217], v[178:181]
	v_mfma_f32_16x16x32_f16 v[154:157], v[238:241], v[218:221], v[154:157]
	s_setprio 0
	s_nop 0
	ds_read_b128 v[178:181], v130 offset:45056
	ds_read_b128 v[238:241], v130 offset:47104
	v_cvt_pk_f16_f32 v39, v38, v39
	v_cvt_pk_f16_f32 v38, v36, v37
	ds_write_b64 v100, v[38:39] offset:28672
	s_add_u32 s0, s22, 0xe0e00
	s_addc_u32 s1, s90, 0
	global_load_dwordx4 v[36:39], v201, s[0:1] nt
	s_setprio 1
	s_waitcnt lgkmcnt(1)
	v_mfma_f32_16x16x32_f16 v[76:79], v[178:181], v[206:209], v[76:79]
	v_mfma_f32_16x16x32_f16 v[234:237], v[178:181], v[210:213], v[234:237]
	v_mfma_f32_16x16x32_f16 v[158:161], v[178:181], v[214:217], v[158:161]
	v_mfma_f32_16x16x32_f16 v[166:169], v[178:181], v[218:221], v[166:169]
	v_mfma_f32_16x16x32_f16 v[178:181], v[238:241], v[206:209], v[182:185]
	v_mfma_f32_16x16x32_f16 v[182:185], v[238:241], v[210:213], v[190:193]
	v_mfma_f32_16x16x32_f16 v[190:193], v[238:241], v[214:217], v[202:205]
	v_mfma_f32_16x16x32_f16 v[186:189], v[238:241], v[218:221], v[186:189]
	s_setprio 0
	s_waitcnt vmcnt(4)
	s_waitcnt lgkmcnt(0)
	s_barrier
	ds_read_b128 v[202:205], v131
	ds_read_b128 v[206:209], v131 offset:2048
	ds_read_b128 v[210:213], v131 offset:4096
	ds_read_b128 v[214:217], v131 offset:6144
	ds_read_b128 v[218:221], v129
	ds_read_b128 v[238:241], v129 offset:2048
	s_add_u32 s70, s22, 0xf00
	v_lshl_add_u64 v[92:93], s[52:53], 0, v[196:197]
	s_addc_u32 s71, s90, 0
	v_readfirstlane_b32 s0, v95
	s_mov_b32 m0, s0
	v_cvt_pk_f16_f32 v3, v2, v3
	global_load_lds_dwordx4 v[92:93], off
	v_cvt_pk_f16_f32 v2, v0, v1
	ds_write_b64 v100, v[2:3] offset:32768
	global_load_dwordx4 v[0:3], v201, s[70:71] nt
	s_setprio 1
	s_waitcnt lgkmcnt(1)
	v_mfma_f32_16x16x32_f16 v[80:83], v[218:221], v[202:205], v[80:83]
	v_mfma_f32_16x16x32_f16 v[104:107], v[218:221], v[210:213], v[104:107]
	v_mfma_f32_16x16x32_f16 v[108:111], v[238:241], v[202:205], v[108:111]
	v_mfma_f32_16x16x32_f16 v[112:115], v[238:241], v[206:209], v[112:115]
	v_mfma_f32_16x16x32_f16 v[116:119], v[238:241], v[210:213], v[116:119]
	v_mfma_f32_16x16x32_f16 v[230:233], v[218:221], v[206:209], v[230:233]
	v_mfma_f32_16x16x32_f16 v[218:221], v[218:221], v[214:217], v[222:225]
	v_mfma_f32_16x16x32_f16 v[222:225], v[238:241], v[214:217], v[226:229]
	s_setprio 0
	s_nop 1
	ds_read_b128 v[226:229], v129 offset:4096
	ds_read_b128 v[238:241], v129 offset:6144
	v_readfirstlane_b32 s1, v96
	v_lshl_add_u64 v[198:199], v[92:93], 0, s[58:59]
	s_mov_b32 m0, s1
	v_cvt_pk_f16_f32 v7, v6, v7
	global_load_lds_dwordx4 v[198:199], off
	v_cvt_pk_f16_f32 v6, v4, v5
	ds_write_b64 v100, v[6:7] offset:36864
	s_add_u32 s70, s22, 0x20f00
	s_addc_u32 s71, s90, 0
	global_load_dwordx4 v[4:7], v201, s[70:71] nt
	s_setprio 1
	s_waitcnt lgkmcnt(1)
	v_mfma_f32_16x16x32_f16 v[68:71], v[226:229], v[202:205], v[68:71]
	v_mfma_f32_16x16x32_f16 v[64:67], v[226:229], v[206:209], v[64:67]
	v_mfma_f32_16x16x32_f16 v[84:87], v[226:229], v[210:213], v[84:87]
	v_mfma_f32_16x16x32_f16 v[120:123], v[226:229], v[214:217], v[120:123]
	v_mfma_f32_16x16x32_f16 v[124:127], v[238:241], v[202:205], v[124:127]
	v_mfma_f32_16x16x32_f16 v[134:137], v[238:241], v[214:217], v[134:137]
	v_mfma_f32_16x16x32_f16 v[138:141], v[238:241], v[206:209], v[138:141]
	v_mfma_f32_16x16x32_f16 v[142:145], v[238:241], v[210:213], v[142:145]
	s_setprio 0
	ds_read_b128 v[226:229], v129 offset:8192
	ds_read_b128 v[238:241], v129 offset:10240
	v_readfirstlane_b32 s70, v97
	v_lshl_add_u64 v[198:199], v[92:93], 0, s[60:61]
	s_mov_b32 m0, s70
	v_cvt_pk_f16_f32 v15, v14, v15
	global_load_lds_dwordx4 v[198:199], off
	v_cvt_pk_f16_f32 v14, v12, v13
	ds_write_b64 v100, v[14:15] offset:40960
	s_add_u32 s72, s22, 0x40f00
	s_addc_u32 s73, s90, 0
	global_load_dwordx4 v[12:15], v201, s[72:73] nt
	s_setprio 1
	s_waitcnt lgkmcnt(1)
	v_mfma_f32_16x16x32_f16 v[72:75], v[226:229], v[202:205], v[72:75]
	v_mfma_f32_16x16x32_f16 v[88:91], v[226:229], v[206:209], v[88:91]
	v_mfma_f32_16x16x32_f16 v[146:149], v[226:229], v[214:217], v[146:149]
	v_mfma_f32_16x16x32_f16 v[170:173], v[226:229], v[210:213], v[170:173]
	v_mfma_f32_16x16x32_f16 v[150:153], v[238:241], v[202:205], v[150:153]
	v_mfma_f32_16x16x32_f16 v[162:165], v[238:241], v[206:209], v[162:165]
	v_mfma_f32_16x16x32_f16 v[174:177], v[238:241], v[210:213], v[174:177]
	v_mfma_f32_16x16x32_f16 v[154:157], v[238:241], v[214:217], v[154:157]
	s_setprio 0
	ds_read_b128 v[226:229], v129 offset:12288
	ds_read_b128 v[238:241], v129 offset:14336
	v_readfirstlane_b32 s71, v98
	v_lshl_add_u64 v[92:93], v[92:93], 0, s[62:63]
	s_mov_b32 m0, s71
	v_cvt_pk_f16_f32 v19, v18, v19
	global_load_lds_dwordx4 v[92:93], off
	v_cvt_pk_f16_f32 v18, v16, v17
	ds_write_b64 v100, v[18:19] offset:45056
	s_add_u32 s72, s22, 0x60f00
	s_addc_u32 s73, s90, 0
	global_load_dwordx4 v[16:19], v201, s[72:73] nt
	s_setprio 1
	s_waitcnt lgkmcnt(1)
	v_mfma_f32_16x16x32_f16 v[76:79], v[226:229], v[202:205], v[76:79]
	v_mfma_f32_16x16x32_f16 v[234:237], v[226:229], v[206:209], v[234:237]
	v_mfma_f32_16x16x32_f16 v[158:161], v[226:229], v[210:213], v[158:161]
	v_mfma_f32_16x16x32_f16 v[166:169], v[226:229], v[214:217], v[166:169]
	v_mfma_f32_16x16x32_f16 v[178:181], v[238:241], v[202:205], v[178:181]
	v_mfma_f32_16x16x32_f16 v[182:185], v[238:241], v[206:209], v[182:185]
	v_mfma_f32_16x16x32_f16 v[190:193], v[238:241], v[210:213], v[190:193]
	v_mfma_f32_16x16x32_f16 v[186:189], v[238:241], v[214:217], v[186:189]
	s_setprio 0
	ds_read_b128 v[202:205], v128
	ds_read_b128 v[206:209], v128 offset:2048
	ds_read_b128 v[210:213], v128 offset:4096
	ds_read_b128 v[214:217], v128 offset:6144
	ds_read_b128 v[226:229], v130
	ds_read_b128 v[238:241], v130 offset:2048
	v_cvt_pk_f16_f32 v23, v22, v23
	v_cvt_pk_f16_f32 v22, v20, v21
	ds_write_b64 v100, v[22:23] offset:49152
	s_add_u32 s72, s22, 0x80f00
	s_addc_u32 s73, s90, 0
	global_load_dwordx4 v[20:23], v201, s[72:73] nt
	s_setprio 1
	s_waitcnt lgkmcnt(1)
	v_mfma_f32_16x16x32_f16 v[80:83], v[226:229], v[202:205], v[80:83]
	v_mfma_f32_16x16x32_f16 v[104:107], v[226:229], v[210:213], v[104:107]
	v_mfma_f32_16x16x32_f16 v[108:111], v[238:241], v[202:205], v[108:111]
	v_mfma_f32_16x16x32_f16 v[112:115], v[238:241], v[206:209], v[112:115]
	v_mfma_f32_16x16x32_f16 v[116:119], v[238:241], v[210:213], v[116:119]
	v_mfma_f32_16x16x32_f16 v[230:233], v[226:229], v[206:209], v[230:233]
	v_mfma_f32_16x16x32_f16 v[218:221], v[226:229], v[214:217], v[218:221]
	v_mfma_f32_16x16x32_f16 v[222:225], v[238:241], v[214:217], v[222:225]
	s_setprio 0
	ds_read_b128 v[226:229], v130 offset:4096
	ds_read_b128 v[238:241], v130 offset:6144
	v_cvt_pk_f16_f32 v27, v26, v27
	v_cvt_pk_f16_f32 v26, v24, v25
	ds_write_b64 v100, v[26:27] offset:53248
	s_add_u32 s72, s22, 0xa0f00
	s_addc_u32 s73, s90, 0
	global_load_dwordx4 v[24:27], v201, s[72:73] nt
	s_setprio 1
	s_waitcnt lgkmcnt(1)
	v_mfma_f32_16x16x32_f16 v[68:71], v[226:229], v[202:205], v[68:71]
	v_mfma_f32_16x16x32_f16 v[64:67], v[226:229], v[206:209], v[64:67]
	v_mfma_f32_16x16x32_f16 v[84:87], v[226:229], v[210:213], v[84:87]
	v_mfma_f32_16x16x32_f16 v[120:123], v[226:229], v[214:217], v[120:123]
	v_mfma_f32_16x16x32_f16 v[124:127], v[238:241], v[202:205], v[124:127]
	v_mfma_f32_16x16x32_f16 v[134:137], v[238:241], v[214:217], v[134:137]
	v_mfma_f32_16x16x32_f16 v[138:141], v[238:241], v[206:209], v[138:141]
	v_mfma_f32_16x16x32_f16 v[142:145], v[238:241], v[210:213], v[142:145]
	s_setprio 0
	ds_read_b128 v[226:229], v130 offset:8192
	ds_read_b128 v[238:241], v130 offset:10240
	v_cvt_pk_f16_f32 v31, v30, v31
	v_cvt_pk_f16_f32 v30, v28, v29
	ds_write_b64 v100, v[30:31] offset:57344
	s_add_u32 s72, s22, 0xc0f00
	s_addc_u32 s73, s90, 0
	global_load_dwordx4 v[28:31], v201, s[72:73] nt
	s_setprio 1
	s_waitcnt lgkmcnt(1)
	v_mfma_f32_16x16x32_f16 v[72:75], v[226:229], v[202:205], v[72:75]
	v_mfma_f32_16x16x32_f16 v[88:91], v[226:229], v[206:209], v[88:91]
	v_mfma_f32_16x16x32_f16 v[146:149], v[226:229], v[214:217], v[146:149]
	v_mfma_f32_16x16x32_f16 v[170:173], v[226:229], v[210:213], v[170:173]
	v_mfma_f32_16x16x32_f16 v[150:153], v[238:241], v[202:205], v[150:153]
	v_mfma_f32_16x16x32_f16 v[162:165], v[238:241], v[206:209], v[162:165]
	v_mfma_f32_16x16x32_f16 v[174:177], v[238:241], v[210:213], v[174:177]
	v_mfma_f32_16x16x32_f16 v[154:157], v[238:241], v[214:217], v[154:157]
	s_setprio 0
	ds_read_b128 v[226:229], v130 offset:12288
	ds_read_b128 v[238:241], v130 offset:14336
	v_cvt_pk_f16_f32 v35, v34, v35
	v_cvt_pk_f16_f32 v34, v32, v33
	ds_write_b64 v100, v[34:35] offset:61440
	s_add_u32 s72, s22, 0xe0f00
	s_addc_u32 s73, s90, 0
	global_load_dwordx4 v[32:35], v201, s[72:73] nt
	s_setprio 1
	s_waitcnt lgkmcnt(1)
	v_mfma_f32_16x16x32_f16 v[76:79], v[226:229], v[202:205], v[76:79]
	v_mfma_f32_16x16x32_f16 v[234:237], v[226:229], v[206:209], v[234:237]
	v_mfma_f32_16x16x32_f16 v[158:161], v[226:229], v[210:213], v[158:161]
	v_mfma_f32_16x16x32_f16 v[166:169], v[226:229], v[214:217], v[166:169]
	v_mfma_f32_16x16x32_f16 v[178:181], v[238:241], v[202:205], v[178:181]
	v_mfma_f32_16x16x32_f16 v[182:185], v[238:241], v[206:209], v[182:185]
	v_mfma_f32_16x16x32_f16 v[190:193], v[238:241], v[210:213], v[190:193]
	v_mfma_f32_16x16x32_f16 v[186:189], v[238:241], v[214:217], v[186:189]
	s_setprio 0
	s_waitcnt vmcnt(4)
	s_waitcnt lgkmcnt(0)
	s_barrier
	ds_read_b128 v[202:205], v131 offset:32768
	ds_read_b128 v[206:209], v131 offset:34816
	ds_read_b128 v[210:213], v131 offset:36864
	ds_read_b128 v[214:217], v131 offset:38912
	ds_read_b128 v[226:229], v129 offset:32768
	ds_read_b128 v[238:241], v129 offset:34816
	v_lshl_add_u64 v[198:199], s[54:55], 0, v[196:197]
	v_readfirstlane_b32 s64, v94
	s_mov_b32 m0, s64
	v_cvt_pk_f16_f32 v11, v10, v11
	global_load_lds_dwordx4 v[198:199], off
	v_cvt_pk_f16_f32 v10, v8, v9
	ds_write_b64 v100, v[10:11]
	s_setprio 1
	s_waitcnt lgkmcnt(1)
	v_mfma_f32_16x16x32_f16 v[8:11], v[226:229], v[202:205], v[80:83]
	v_mfma_f32_16x16x32_f16 v[80:83], v[226:229], v[206:209], v[230:233]
	v_mfma_f32_16x16x32_f16 v[92:95], v[226:229], v[210:213], v[104:107]
	v_mfma_f32_16x16x32_f16 v[104:107], v[226:229], v[214:217], v[218:221]
	v_mfma_f32_16x16x32_f16 v[108:111], v[238:241], v[202:205], v[108:111]
	v_mfma_f32_16x16x32_f16 v[112:115], v[238:241], v[206:209], v[112:115]
	v_mfma_f32_16x16x32_f16 v[116:119], v[238:241], v[210:213], v[116:119]
	v_mfma_f32_16x16x32_f16 v[218:221], v[238:241], v[214:217], v[222:225]
	s_setprio 0
	s_nop 1
	ds_read_b128 v[222:225], v129 offset:36864
	ds_read_b128 v[226:229], v129 offset:38912
	v_readfirstlane_b32 s64, v99
	v_lshl_add_u64 v[96:97], v[198:199], 0, s[58:59]
	s_mov_b32 m0, s64
	v_cvt_pk_f16_f32 v43, v42, v43
	global_load_lds_dwordx4 v[96:97], off
	v_cvt_pk_f16_f32 v42, v40, v41
	ds_write_b64 v100, v[42:43] offset:4096
	s_setprio 1
	s_waitcnt lgkmcnt(1)
	v_mfma_f32_16x16x32_f16 v[40:43], v[222:225], v[202:205], v[68:71]
	v_mfma_f32_16x16x32_f16 v[64:67], v[222:225], v[206:209], v[64:67]
	v_mfma_f32_16x16x32_f16 v[68:71], v[222:225], v[210:213], v[84:87]
	v_mfma_f32_16x16x32_f16 v[84:87], v[222:225], v[214:217], v[120:123]
	v_mfma_f32_16x16x32_f16 v[96:99], v[226:229], v[202:205], v[124:127]
	v_mfma_f32_16x16x32_f16 v[120:123], v[226:229], v[206:209], v[138:141]
	v_mfma_f32_16x16x32_f16 v[124:127], v[226:229], v[210:213], v[142:145]
	v_mfma_f32_16x16x32_f16 v[134:137], v[226:229], v[214:217], v[134:137]
	s_setprio 0
	ds_read_b128 v[138:141], v129 offset:40960
	ds_read_b128 v[142:145], v129 offset:43008
	v_readfirstlane_b32 s64, v101
	v_lshl_add_u64 v[222:223], v[198:199], 0, s[60:61]
	s_mov_b32 m0, s64
	v_cvt_pk_f16_f32 v47, v46, v47
	global_load_lds_dwordx4 v[222:223], off
	v_cvt_pk_f16_f32 v46, v44, v45
	ds_write_b64 v100, v[46:47] offset:8192
	s_setprio 1
	s_waitcnt lgkmcnt(1)
	v_mfma_f32_16x16x32_f16 v[44:47], v[138:141], v[202:205], v[72:75]
	v_mfma_f32_16x16x32_f16 v[72:75], v[138:141], v[206:209], v[88:91]
	v_mfma_f32_16x16x32_f16 v[88:91], v[138:141], v[210:213], v[170:173]
	v_mfma_f32_16x16x32_f16 v[138:141], v[138:141], v[214:217], v[146:149]
	v_mfma_f32_16x16x32_f16 v[146:149], v[142:145], v[202:205], v[150:153]
	v_mfma_f32_16x16x32_f16 v[150:153], v[142:145], v[206:209], v[162:165]
	v_mfma_f32_16x16x32_f16 v[162:165], v[142:145], v[210:213], v[174:177]
	v_mfma_f32_16x16x32_f16 v[142:145], v[142:145], v[214:217], v[154:157]
	s_setprio 0
	s_nop 1
	ds_read_b128 v[154:157], v129 offset:45056
	ds_read_b128 v[170:173], v129 offset:47104
	v_readfirstlane_b32 s64, v102
	v_lshl_add_u64 v[174:175], v[198:199], 0, s[62:63]
	s_mov_b32 m0, s64
	v_cvt_pk_f16_f32 v51, v50, v51
	global_load_lds_dwordx4 v[174:175], off
	v_cvt_pk_f16_f32 v50, v48, v49
	ds_write_b64 v100, v[50:51] offset:12288
	s_setprio 1
	s_waitcnt lgkmcnt(1)
	v_mfma_f32_16x16x32_f16 v[48:51], v[154:157], v[202:205], v[76:79]
	v_mfma_f32_16x16x32_f16 v[76:79], v[154:157], v[206:209], v[234:237]
	v_mfma_f32_16x16x32_f16 v[158:161], v[154:157], v[210:213], v[158:161]
	v_mfma_f32_16x16x32_f16 v[154:157], v[154:157], v[214:217], v[166:169]
	v_mfma_f32_16x16x32_f16 v[166:169], v[170:173], v[202:205], v[178:181]
	v_mfma_f32_16x16x32_f16 v[174:177], v[170:173], v[206:209], v[182:185]
	v_mfma_f32_16x16x32_f16 v[178:181], v[170:173], v[210:213], v[190:193]
	v_mfma_f32_16x16x32_f16 v[170:173], v[170:173], v[214:217], v[186:189]
	s_setprio 0
	ds_read_b128 v[182:185], v128 offset:32768
	s_nop 0
	ds_read_b128 v[186:189], v128 offset:34816
	ds_read_b128 v[190:193], v128 offset:36864
	ds_read_b128 v[202:205], v128 offset:38912
	ds_read_b128 v[206:209], v130 offset:32768
	ds_read_b128 v[210:213], v130 offset:34816
	v_cvt_pk_f16_f32 v55, v54, v55
	v_cvt_pk_f16_f32 v54, v52, v53
	ds_write_b64 v100, v[54:55] offset:16384
	s_setprio 1
	s_waitcnt lgkmcnt(1)
	v_mfma_f32_16x16x32_f16 v[8:11], v[206:209], v[182:185], v[8:11]
	v_mfma_f32_16x16x32_f16 v[52:55], v[206:209], v[186:189], v[80:83]
	v_mfma_f32_16x16x32_f16 v[80:83], v[206:209], v[190:193], v[92:95]
	v_mfma_f32_16x16x32_f16 v[92:95], v[206:209], v[202:205], v[104:107]
	v_mfma_f32_16x16x32_f16 v[102:105], v[210:213], v[182:185], v[108:111]
	v_mfma_f32_16x16x32_f16 v[106:109], v[210:213], v[186:189], v[112:115]
	v_mfma_f32_16x16x32_f16 v[110:113], v[210:213], v[190:193], v[116:119]
	v_mfma_f32_16x16x32_f16 v[114:117], v[210:213], v[202:205], v[218:221]
	s_setprio 0
	ds_read_b128 v[206:209], v130 offset:36864
	ds_read_b128 v[210:213], v130 offset:38912
	v_cvt_pk_f16_f32 v59, v58, v59
	v_cvt_pk_f16_f32 v58, v56, v57
	ds_write_b64 v100, v[58:59] offset:20480
	s_setprio 1
	s_waitcnt lgkmcnt(1)
	v_mfma_f32_16x16x32_f16 v[40:43], v[206:209], v[182:185], v[40:43]
	v_mfma_f32_16x16x32_f16 v[56:59], v[206:209], v[186:189], v[64:67]
	v_mfma_f32_16x16x32_f16 v[64:67], v[206:209], v[190:193], v[68:71]
	v_mfma_f32_16x16x32_f16 v[68:71], v[206:209], v[202:205], v[84:87]
	v_mfma_f32_16x16x32_f16 v[84:87], v[210:213], v[182:185], v[96:99]
	v_mfma_f32_16x16x32_f16 v[96:99], v[210:213], v[186:189], v[120:123]
	v_mfma_f32_16x16x32_f16 v[118:121], v[210:213], v[190:193], v[124:127]
	v_mfma_f32_16x16x32_f16 v[122:125], v[210:213], v[202:205], v[134:137]
	s_setprio 0
	s_nop 1
	ds_read_b128 v[134:137], v130 offset:40960
	ds_read_b128 v[206:209], v130 offset:43008
	v_cvt_pk_f16_f32 v63, v62, v63
	v_cvt_pk_f16_f32 v62, v60, v61
	ds_write_b64 v100, v[62:63] offset:24576
	s_setprio 1
	s_waitcnt lgkmcnt(1)
	v_mfma_f32_16x16x32_f16 v[44:47], v[134:137], v[182:185], v[44:47]
	v_mfma_f32_16x16x32_f16 v[60:63], v[134:137], v[186:189], v[72:75]
	v_mfma_f32_16x16x32_f16 v[72:75], v[134:137], v[190:193], v[88:91]
	v_mfma_f32_16x16x32_f16 v[88:91], v[134:137], v[202:205], v[138:141]
	v_mfma_f32_16x16x32_f16 v[134:137], v[206:209], v[182:185], v[146:149]
	v_mfma_f32_16x16x32_f16 v[146:149], v[206:209], v[190:193], v[162:165]
	v_mfma_f32_16x16x32_f16 v[138:141], v[206:209], v[186:189], v[150:153]
	v_mfma_f32_16x16x32_f16 v[142:145], v[206:209], v[202:205], v[142:145]
	s_setprio 0
	s_nop 0
	ds_read_b128 v[150:153], v130 offset:45056
	ds_read_b128 v[162:165], v130 offset:47104
	v_cvt_pk_f16_f32 v39, v38, v39
	v_cvt_pk_f16_f32 v38, v36, v37
	ds_write_b64 v100, v[38:39] offset:28672
	s_setprio 1
	s_waitcnt lgkmcnt(1)
	v_mfma_f32_16x16x32_f16 v[36:39], v[150:153], v[182:185], v[48:51]
	v_mfma_f32_16x16x32_f16 v[48:51], v[150:153], v[186:189], v[76:79]
	v_mfma_f32_16x16x32_f16 v[76:79], v[150:153], v[190:193], v[158:161]
	v_mfma_f32_16x16x32_f16 v[150:153], v[150:153], v[202:205], v[154:157]
	v_mfma_f32_16x16x32_f16 v[154:157], v[162:165], v[182:185], v[166:169]
	v_mfma_f32_16x16x32_f16 v[158:161], v[162:165], v[186:189], v[174:177]
	v_mfma_f32_16x16x32_f16 v[166:169], v[162:165], v[190:193], v[178:181]
	v_mfma_f32_16x16x32_f16 v[162:165], v[162:165], v[202:205], v[170:173]
	s_setprio 0
	s_waitcnt vmcnt(0)
	s_waitcnt lgkmcnt(0)
	s_barrier
	s_nop 0
	ds_read_b128 v[170:173], v131
	ds_read_b128 v[174:177], v131 offset:2048
	ds_read_b128 v[178:181], v131 offset:4096
	ds_read_b128 v[182:185], v131 offset:6144
	ds_read_b128 v[186:189], v129
	ds_read_b128 v[190:193], v129 offset:2048
	v_lshl_add_u64 v[126:127], s[56:57], 0, v[196:197]
	s_mov_b32 m0, s0
	v_cvt_pk_f16_f32 v3, v2, v3
	global_load_lds_dwordx4 v[126:127], off
	v_cvt_pk_f16_f32 v2, v0, v1
	ds_write_b64 v100, v[2:3] offset:32768
	s_setprio 1
	s_waitcnt lgkmcnt(1)
	v_mfma_f32_16x16x32_f16 v[0:3], v[186:189], v[170:173], v[8:11]
	v_mfma_f32_16x16x32_f16 v[8:11], v[186:189], v[174:177], v[52:55]
	v_mfma_f32_16x16x32_f16 v[52:55], v[186:189], v[178:181], v[80:83]
	v_mfma_f32_16x16x32_f16 v[80:83], v[186:189], v[182:185], v[92:95]
	v_mfma_f32_16x16x32_f16 v[92:95], v[190:193], v[170:173], v[102:105]
	v_mfma_f32_16x16x32_f16 v[102:105], v[190:193], v[174:177], v[106:109]
	v_mfma_f32_16x16x32_f16 v[106:109], v[190:193], v[178:181], v[110:113]
	v_mfma_f32_16x16x32_f16 v[110:113], v[190:193], v[182:185], v[114:117]
	s_setprio 0
	s_nop 1
	ds_read_b128 v[114:117], v129 offset:4096
	ds_read_b128 v[186:189], v129 offset:6144
	s_mov_b32 m0, s1
	v_lshl_add_u64 v[190:191], v[126:127], 0, s[58:59]
	global_load_lds_dwordx4 v[190:191], off
	v_cvt_pk_f16_f32 v7, v6, v7
	v_cvt_pk_f16_f32 v6, v4, v5
	ds_write_b64 v100, v[6:7] offset:36864
	s_setprio 1
	s_waitcnt lgkmcnt(1)
	v_mfma_f32_16x16x32_f16 v[190:193], v[114:117], v[170:173], v[40:43]
	v_mfma_f32_16x16x32_f16 v[56:59], v[114:117], v[174:177], v[56:59]
	v_mfma_f32_16x16x32_f16 v[64:67], v[114:117], v[178:181], v[64:67]
	v_mfma_f32_16x16x32_f16 v[68:71], v[114:117], v[182:185], v[68:71]
	v_mfma_f32_16x16x32_f16 v[84:87], v[186:189], v[170:173], v[84:87]
	v_mfma_f32_16x16x32_f16 v[96:99], v[186:189], v[174:177], v[96:99]
	v_mfma_f32_16x16x32_f16 v[114:117], v[186:189], v[178:181], v[118:121]
	v_mfma_f32_16x16x32_f16 v[118:121], v[186:189], v[182:185], v[122:125]
	s_setprio 0
	ds_read_b128 v[4:7], v129 offset:8192
	ds_read_b128 v[40:43], v129 offset:10240
	s_mov_b32 m0, s70
	v_lshl_add_u64 v[122:123], v[126:127], 0, s[60:61]
	global_load_lds_dwordx4 v[122:123], off
	v_cvt_pk_f16_f32 v15, v14, v15
	v_cvt_pk_f16_f32 v14, v12, v13
	ds_write_b64 v100, v[14:15] offset:40960
	s_setprio 1
	s_waitcnt lgkmcnt(1)
	v_mfma_f32_16x16x32_f16 v[122:125], v[4:7], v[170:173], v[44:47]
	v_mfma_f32_16x16x32_f16 v[88:91], v[4:7], v[182:185], v[88:91]
	v_mfma_f32_16x16x32_f16 v[134:137], v[40:43], v[170:173], v[134:137]
	v_mfma_f32_16x16x32_f16 v[146:149], v[40:43], v[178:181], v[146:149]
	v_mfma_f32_16x16x32_f16 v[186:189], v[4:7], v[174:177], v[60:63]
	v_mfma_f32_16x16x32_f16 v[202:205], v[4:7], v[178:181], v[72:75]
	v_mfma_f32_16x16x32_f16 v[138:141], v[40:43], v[174:177], v[138:141]
	v_mfma_f32_16x16x32_f16 v[142:145], v[40:43], v[182:185], v[142:145]
	s_setprio 0
	ds_read_b128 v[4:7], v129 offset:12288
	ds_read_b128 v[12:15], v129 offset:14336
	s_mov_b32 m0, s71
	v_lshl_add_u64 v[40:41], v[126:127], 0, s[62:63]
	global_load_lds_dwordx4 v[40:41], off
	v_cvt_pk_f16_f32 v19, v18, v19
	v_cvt_pk_f16_f32 v18, v16, v17
	ds_write_b64 v100, v[18:19] offset:45056
	s_setprio 1
	s_waitcnt lgkmcnt(1)
	v_mfma_f32_16x16x32_f16 v[206:209], v[4:7], v[170:173], v[36:39]
	v_mfma_f32_16x16x32_f16 v[210:213], v[4:7], v[174:177], v[48:51]
	v_mfma_f32_16x16x32_f16 v[214:217], v[4:7], v[178:181], v[76:79]
	v_mfma_f32_16x16x32_f16 v[150:153], v[4:7], v[182:185], v[150:153]
	v_mfma_f32_16x16x32_f16 v[154:157], v[12:15], v[170:173], v[154:157]
	v_mfma_f32_16x16x32_f16 v[158:161], v[12:15], v[174:177], v[158:161]
	v_mfma_f32_16x16x32_f16 v[166:169], v[12:15], v[178:181], v[166:169]
	v_mfma_f32_16x16x32_f16 v[162:165], v[12:15], v[182:185], v[162:165]
	s_setprio 0
	ds_read_b128 v[170:173], v128
	ds_read_b128 v[174:177], v128 offset:2048
	ds_read_b128 v[178:181], v128 offset:4096
	ds_read_b128 v[182:185], v128 offset:6144
	ds_read_b128 v[12:15], v130
	ds_read_b128 v[40:43], v130 offset:2048
	v_cvt_pk_f16_f32 v5, v22, v23
	v_cvt_pk_f16_f32 v4, v20, v21
	ds_write_b64 v100, v[4:5] offset:49152
	s_setprio 1
	s_waitcnt lgkmcnt(1)
	v_mfma_f32_16x16x32_f16 v[0:3], v[12:15], v[170:173], v[0:3]
	v_mfma_f32_16x16x32_f16 v[4:7], v[12:15], v[174:177], v[8:11]
	v_mfma_f32_16x16x32_f16 v[8:11], v[12:15], v[178:181], v[52:55]
	v_mfma_f32_16x16x32_f16 v[12:15], v[12:15], v[182:185], v[80:83]
	v_mfma_f32_16x16x32_f16 v[16:19], v[40:43], v[170:173], v[92:95]
	v_mfma_f32_16x16x32_f16 v[20:23], v[40:43], v[174:177], v[102:105]
	v_mfma_f32_16x16x32_f16 v[36:39], v[40:43], v[178:181], v[106:109]
	v_mfma_f32_16x16x32_f16 v[40:43], v[40:43], v[182:185], v[110:113]
	s_setprio 0
	ds_read_b128 v[52:55], v130 offset:4096
	ds_read_b128 v[72:75], v130 offset:6144
	v_cvt_pk_f16_f32 v27, v26, v27
	v_cvt_pk_f16_f32 v26, v24, v25
	ds_write_b64 v100, v[26:27] offset:53248
	s_setprio 1
	s_waitcnt lgkmcnt(1)
	v_mfma_f32_16x16x32_f16 v[24:27], v[52:55], v[170:173], v[190:193]
	v_mfma_f32_16x16x32_f16 v[44:47], v[52:55], v[174:177], v[56:59]
	v_mfma_f32_16x16x32_f16 v[48:51], v[52:55], v[178:181], v[64:67]
	v_mfma_f32_16x16x32_f16 v[52:55], v[52:55], v[182:185], v[68:71]
	v_mfma_f32_16x16x32_f16 v[56:59], v[72:75], v[170:173], v[84:87]
	v_mfma_f32_16x16x32_f16 v[60:63], v[72:75], v[174:177], v[96:99]
	v_mfma_f32_16x16x32_f16 v[64:67], v[72:75], v[178:181], v[114:117]
	v_mfma_f32_16x16x32_f16 v[68:71], v[72:75], v[182:185], v[118:121]
	s_setprio 0
	ds_read_b128 v[80:83], v130 offset:8192
	ds_read_b128 v[96:99], v130 offset:10240
	v_cvt_pk_f16_f32 v31, v30, v31
	v_cvt_pk_f16_f32 v30, v28, v29
	ds_write_b64 v100, v[30:31] offset:57344
	s_setprio 1
	s_waitcnt lgkmcnt(1)
	v_mfma_f32_16x16x32_f16 v[28:31], v[80:83], v[170:173], v[122:125]
	v_mfma_f32_16x16x32_f16 v[72:75], v[80:83], v[174:177], v[186:189]
	v_mfma_f32_16x16x32_f16 v[76:79], v[80:83], v[178:181], v[202:205]
	v_mfma_f32_16x16x32_f16 v[80:83], v[80:83], v[182:185], v[88:91]
	v_mfma_f32_16x16x32_f16 v[84:87], v[96:99], v[170:173], v[134:137]
	v_mfma_f32_16x16x32_f16 v[88:91], v[96:99], v[174:177], v[138:141]
	v_mfma_f32_16x16x32_f16 v[92:95], v[96:99], v[178:181], v[146:149]
	v_mfma_f32_16x16x32_f16 v[96:99], v[96:99], v[182:185], v[142:145]
	s_setprio 0
	ds_read_b128 v[108:111], v130 offset:12288
	ds_read_b128 v[124:127], v130 offset:14336
	v_cvt_pk_f16_f32 v35, v34, v35
	v_cvt_pk_f16_f32 v34, v32, v33
	ds_write_b64 v100, v[34:35] offset:61440
	s_setprio 1
	s_waitcnt lgkmcnt(1)
	v_mfma_f32_16x16x32_f16 v[32:35], v[108:111], v[170:173], v[206:209]
	v_mfma_f32_16x16x32_f16 v[100:103], v[108:111], v[174:177], v[210:213]
	v_mfma_f32_16x16x32_f16 v[104:107], v[108:111], v[178:181], v[214:217]
	v_mfma_f32_16x16x32_f16 v[108:111], v[108:111], v[182:185], v[150:153]
	v_mfma_f32_16x16x32_f16 v[112:115], v[124:127], v[170:173], v[154:157]
	v_mfma_f32_16x16x32_f16 v[116:119], v[124:127], v[174:177], v[158:161]
	v_mfma_f32_16x16x32_f16 v[120:123], v[124:127], v[178:181], v[166:169]
	v_mfma_f32_16x16x32_f16 v[124:127], v[124:127], v[182:185], v[162:165]
	s_setprio 0
	s_waitcnt vmcnt(0)
	s_waitcnt lgkmcnt(0)
	s_barrier
	ds_read_b128 v[134:137], v131 offset:32768
	ds_read_b128 v[138:141], v131 offset:34816
	ds_read_b128 v[142:145], v131 offset:36864
	ds_read_b128 v[148:151], v131 offset:38912
	ds_read_b128 v[152:155], v129 offset:32768
	ds_read_b128 v[156:159], v129 offset:34816
	s_setprio 1
	s_waitcnt lgkmcnt(0)
	v_mfma_f32_16x16x32_f16 v[0:3], v[152:155], v[134:137], v[0:3]
	v_mfma_f32_16x16x32_f16 v[4:7], v[152:155], v[138:141], v[4:7]
	v_mfma_f32_16x16x32_f16 v[8:11], v[152:155], v[142:145], v[8:11]
	v_mfma_f32_16x16x32_f16 v[12:15], v[152:155], v[148:151], v[12:15]
	v_mfma_f32_16x16x32_f16 v[16:19], v[156:159], v[134:137], v[16:19]
	v_mfma_f32_16x16x32_f16 v[20:23], v[156:159], v[138:141], v[20:23]
	v_mfma_f32_16x16x32_f16 v[36:39], v[156:159], v[142:145], v[36:39]
	v_mfma_f32_16x16x32_f16 v[40:43], v[156:159], v[148:151], v[40:43]
	s_setprio 0
	ds_read_b128 v[152:155], v129 offset:36864
	ds_read_b128 v[156:159], v129 offset:38912
	v_and_b32_e32 v250, 0x7ffffc00, v194
	v_lshl_add_u64 v[252:253], s[10:11], 0, v[196:197]
	v_readfirstlane_b32 s32, v250
	s_nop 0
	s_mov_b32 m0, s32
	s_nop 0
	global_load_lds_dwordx4 v[252:253], off
	v_mov_b32_e32 v146, 0
	v_and_b32_e32 v251, 0xfffffff, v132
	v_cmp_gt_u32_e32 vcc, s82, v251
	v_mov_b32_e32 v132, 0
	v_mov_b32_e32 v133, 0
	s_and_saveexec_b64 s[0:1], vcc
	s_cbranch_execz .LBB1_7
	s_and_b32 s64, s78, 0x7ffffc00
	s_or_b32 s64, s64, s33
	v_or_b32_e32 v132, s64, v251
	v_mov_b32_e32 v133, v195
	v_lshl_add_u64 v[132:133], v[132:133], 2, s[12:13]
	global_load_dword v133, v[132:133], off
	v_or_b32_e32 v132, s33, v251
	v_lshlrev_b32_e32 v132, 2, v132
	global_load_dword v146, v132, s[16:17]
	s_nop 0
	global_load_dword v132, v132, s[14:15]

.LBB1_20:
	s_or_b64 exec, exec, s[0:1]
	v_add_f32_e32 v67, v194, v154
	v_add_f32_e32 v67, v67, v106
	v_add_f32_e32 v67, v67, v66
	v_mov_b32_e32 v69, v195
	v_cmp_eq_u32_e32 vcc, 0, v204
	v_add_f32_dpp v67, v67, v67 quad_perm:[1,0,3,2] row_mask:0xf bank_mask:0xf bound_ctrl:1
	s_nop 1
	v_add_f32_dpp v67, v67, v67 quad_perm:[2,3,0,1] row_mask:0xf bank_mask:0xf bound_ctrl:1
	s_nop 1
	v_add_f32_dpp v68, v67, v67 row_half_mirror row_mask:0xf bank_mask:0xf bound_ctrl:1
	v_lshl_or_b32 v67, v208, 2, v207
	v_mul_lo_u32 v67, v67, s85
	v_mov_b32_dpp v69, v68 row_mirror row_mask:0xf bank_mask:0xf
	s_and_saveexec_b64 s[0:1], vcc
	v_add_f32_e32 v68, v68, v69
	ds_write_b32 v67, v68 offset:37376
	s_or_b64 exec, exec, s[0:1]
	v_lshl_add_u32 v68, v1, 12, v200
	v_and_b32_e32 v69, 51, v0
	v_lshl_or_b32 v70, v69, 2, v68
	v_and_b32_e32 v69, 48, v0
	v_lshl_add_u32 v67, v69, 2, v67
	v_lshlrev_b32_e32 v69, 4, v0
	v_and_b32_e32 v69, 48, v69
	v_and_b32_e32 v71, 12, v0
	v_add3_u32 v67, v67, v69, v71
	v_cvt_f32_f16_e32 v69, v50
	v_cvt_f32_f16_sdwa v50, v50 dst_sel:DWORD dst_unused:UNUSED_PAD src0_sel:WORD_1
	v_lshl_or_b32 v68, v204, 6, v68
	s_and_b64 s[0:1], exec, s[72:73]
	v_mul_f32_e32 v69, v194, v69
	v_mul_f32_e32 v50, v194, v50
	v_fma_mix_f32 v50, v154, v54, v50 op_sel:[0,1,0] op_sel_hi:[0,1,0]
	v_fma_mix_f32 v50, v106, v58, v50 op_sel:[0,1,0] op_sel_hi:[0,1,0]
	v_fma_mix_f32 v69, v154, v54, v69 op_sel_hi:[0,1,0]
	v_fma_mix_f32 v54, v66, v62, v50 op_sel:[0,1,0] op_sel_hi:[0,1,0]
	v_bitop3_b32 v50, v0, 4, 12 bitop3:0x6c
	v_lshl_or_b32 v50, v50, 2, v70
	ds_write_b32 v50, v54 offset:256
	v_cvt_f32_f16_e32 v54, v51
	v_cvt_f32_f16_sdwa v51, v51 dst_sel:DWORD dst_unused:UNUSED_PAD src0_sel:WORD_1
	v_fma_mix_f32 v69, v106, v58, v69 op_sel_hi:[0,1,0]
	v_fma_mix_f32 v72, v66, v62, v69 op_sel_hi:[0,1,0]
	v_mul_f32_e32 v54, v194, v54
	v_mul_f32_e32 v51, v194, v51
	v_fma_mix_f32 v51, v154, v55, v51 op_sel:[0,1,0] op_sel_hi:[0,1,0]
	v_fma_mix_f32 v51, v106, v59, v51 op_sel:[0,1,0] op_sel_hi:[0,1,0]
	v_fma_mix_f32 v54, v154, v55, v54 op_sel_hi:[0,1,0]
	v_fma_mix_f32 v55, v66, v63, v51 op_sel:[0,1,0] op_sel_hi:[0,1,0]
	v_bitop3_b32 v51, v0, 12, v0 bitop3:0xc
	v_lshl_or_b32 v51, v51, 2, v70
	ds_write_b32 v51, v55 offset:768
	v_cvt_f32_f16_e32 v55, v52
	v_cvt_f32_f16_sdwa v52, v52 dst_sel:DWORD dst_unused:UNUSED_PAD src0_sel:WORD_1
	v_fma_mix_f32 v54, v106, v59, v54 op_sel_hi:[0,1,0]
	v_fma_mix_f32 v58, v66, v63, v54 op_sel_hi:[0,1,0]
	v_bitop3_b32 v54, v0, 8, 12 bitop3:0x6c
	v_mul_f32_e32 v52, v194, v52
	v_fma_mix_f32 v52, v154, v56, v52 op_sel:[0,1,0] op_sel_hi:[0,1,0]
	v_fma_mix_f32 v52, v106, v60, v52 op_sel:[0,1,0] op_sel_hi:[0,1,0]
	v_fma_mix_f32 v52, v66, v64, v52 op_sel:[0,1,0] op_sel_hi:[0,1,0]
	ds_write_b32 v50, v52 offset:1280
	v_cvt_f32_f16_e32 v52, v53
	v_lshl_or_b32 v54, v54, 2, v70
	v_lshl_or_b32 v69, v71, 2, v70
	v_mul_f32_e32 v55, v194, v55
	v_mul_f32_e32 v52, v194, v52
	v_fma_mix_f32 v52, v154, v57, v52 op_sel_hi:[0,1,0]
	v_fma_mix_f32 v52, v106, v61, v52 op_sel_hi:[0,1,0]
	v_fma_mix_f32 v52, v66, v65, v52 op_sel_hi:[0,1,0]
	ds_write_b32 v54, v52 offset:1536
	v_cvt_f32_f16_sdwa v52, v53 dst_sel:DWORD dst_unused:UNUSED_PAD src0_sel:WORD_1
	v_fma_mix_f32 v55, v154, v56, v55 op_sel_hi:[0,1,0]
	v_fma_mix_f32 v55, v106, v60, v55 op_sel_hi:[0,1,0]
	v_fma_mix_f32 v55, v66, v64, v55 op_sel_hi:[0,1,0]
	v_mul_f32_e32 v52, v194, v52
	v_fma_mix_f32 v52, v154, v57, v52 op_sel:[0,1,0] op_sel_hi:[0,1,0]
	v_fma_mix_f32 v52, v106, v61, v52 op_sel:[0,1,0] op_sel_hi:[0,1,0]
	v_fma_mix_f32 v52, v66, v65, v52 op_sel:[0,1,0] op_sel_hi:[0,1,0]
	ds_write_b32 v51, v52 offset:1792
	v_cvt_f32_f16_e32 v52, v34
	v_cvt_f32_f16_sdwa v34, v34 dst_sel:DWORD dst_unused:UNUSED_PAD src0_sel:WORD_1
	ds_write_b32 v69, v72
	ds_write_b32 v54, v58 offset:512
	v_mul_f32_e32 v52, v194, v52
	v_mul_f32_e32 v34, v194, v34
	v_fma_mix_f32 v34, v154, v38, v34 op_sel:[0,1,0] op_sel_hi:[0,1,0]
	v_fma_mix_f32 v34, v106, v42, v34 op_sel:[0,1,0] op_sel_hi:[0,1,0]
	v_fma_mix_f32 v34, v66, v46, v34 op_sel:[0,1,0] op_sel_hi:[0,1,0]
	ds_write_b32 v50, v34 offset:2304
	v_cvt_f32_f16_e32 v34, v35
	v_fma_mix_f32 v52, v154, v38, v52 op_sel_hi:[0,1,0]
	v_fma_mix_f32 v52, v106, v42, v52 op_sel_hi:[0,1,0]
	v_fma_mix_f32 v52, v66, v46, v52 op_sel_hi:[0,1,0]
	v_mul_f32_e32 v34, v194, v34
	v_fma_mix_f32 v34, v154, v39, v34 op_sel_hi:[0,1,0]
	v_fma_mix_f32 v34, v106, v43, v34 op_sel_hi:[0,1,0]
	v_fma_mix_f32 v34, v66, v47, v34 op_sel_hi:[0,1,0]
	ds_write_b32 v54, v34 offset:2560
	v_cvt_f32_f16_sdwa v34, v35 dst_sel:DWORD dst_unused:UNUSED_PAD src0_sel:WORD_1
	ds_write_b32 v69, v55 offset:1024
	ds_write_b32 v69, v52 offset:2048
	s_cselect_b32 s0, 0, 8
	v_mul_f32_e32 v34, v194, v34
	v_fma_mix_f32 v34, v154, v39, v34 op_sel:[0,1,0] op_sel_hi:[0,1,0]
	v_fma_mix_f32 v34, v106, v43, v34 op_sel:[0,1,0] op_sel_hi:[0,1,0]
	v_fma_mix_f32 v34, v66, v47, v34 op_sel:[0,1,0] op_sel_hi:[0,1,0]
	ds_write_b32 v51, v34 offset:2816
	v_cvt_f32_f16_e32 v34, v36
	s_add_i32 s22, s0, s89
	s_lshl_b64 s[0:1], s[22:23], 20
	s_add_u32 s0, s6, s0
	v_mul_f32_e32 v34, v194, v34
	v_fma_mix_f32 v34, v154, v40, v34 op_sel_hi:[0,1,0]
	v_fma_mix_f32 v34, v106, v44, v34 op_sel_hi:[0,1,0]
	v_fma_mix_f32 v34, v66, v48, v34 op_sel_hi:[0,1,0]
	ds_write_b32 v69, v34 offset:3072
	v_cvt_f32_f16_sdwa v34, v36 dst_sel:DWORD dst_unused:UNUSED_PAD src0_sel:WORD_1
	s_addc_u32 s1, s7, s1
	s_mov_b64 s[72:73], s[0:1]
	v_mul_f32_e32 v34, v194, v34
	v_fma_mix_f32 v34, v154, v40, v34 op_sel:[0,1,0] op_sel_hi:[0,1,0]
	v_fma_mix_f32 v34, v106, v44, v34 op_sel:[0,1,0] op_sel_hi:[0,1,0]
	v_fma_mix_f32 v34, v66, v48, v34 op_sel:[0,1,0] op_sel_hi:[0,1,0]
	ds_write_b32 v50, v34 offset:3328
	v_cvt_f32_f16_e32 v34, v37
	v_mul_f32_e32 v34, v194, v34
	v_fma_mix_f32 v34, v154, v41, v34 op_sel_hi:[0,1,0]
	v_fma_mix_f32 v34, v106, v45, v34 op_sel_hi:[0,1,0]
	v_fma_mix_f32 v34, v66, v49, v34 op_sel_hi:[0,1,0]
	ds_write_b32 v54, v34 offset:3584
	v_cvt_f32_f16_sdwa v34, v37 dst_sel:DWORD dst_unused:UNUSED_PAD src0_sel:WORD_1
	v_mul_f32_e32 v34, v194, v34
	v_fma_mix_f32 v34, v154, v41, v34 op_sel:[0,1,0] op_sel_hi:[0,1,0]
	v_fma_mix_f32 v34, v106, v45, v34 op_sel:[0,1,0] op_sel_hi:[0,1,0]
	v_fma_mix_f32 v34, v66, v49, v34 op_sel:[0,1,0] op_sel_hi:[0,1,0]
	ds_write_b32 v51, v34 offset:3840
	ds_read_b128 v[34:37], v68
	ds_read_b128 v[38:41], v68 offset:16
	ds_read_b128 v[42:45], v68 offset:32
	ds_read_b128 v[46:49], v68 offset:48
	s_waitcnt lgkmcnt(2)
	v_pk_add_f32 v[36:37], v[36:37], v[40:41]
	v_pk_add_f32 v[34:35], v[34:35], v[38:39]
	s_waitcnt lgkmcnt(0)
	v_pk_add_f32 v[38:39], v[44:45], v[48:49]
	v_pk_add_f32 v[40:41], v[42:43], v[46:47]
	v_pk_add_f32 v[36:37], v[36:37], v[38:39]
	v_pk_add_f32 v[34:35], v[34:35], v[40:41]
	s_nop 0
	v_add_f32_e32 v34, v34, v35
	v_add_f32_e32 v35, v36, v37
	v_add_f32_e32 v34, v34, v35
	ds_write_b32 v67, v34 offset:36864
	v_cvt_f32_f16_e32 v34, v2
	v_cvt_f32_f16_sdwa v2, v2 dst_sel:DWORD dst_unused:UNUSED_PAD src0_sel:WORD_1
	v_mul_f32_e32 v34, v194, v34
	v_mul_f32_e32 v2, v194, v2
	v_fma_mix_f32 v2, v154, v6, v2 op_sel:[0,1,0] op_sel_hi:[0,1,0]
	v_fma_mix_f32 v2, v106, v14, v2 op_sel:[0,1,0] op_sel_hi:[0,1,0]
	v_fma_mix_f32 v2, v66, v30, v2 op_sel:[0,1,0] op_sel_hi:[0,1,0]
	ds_write_b32 v50, v2 offset:256
	v_cvt_f32_f16_e32 v2, v3
	v_fma_mix_f32 v34, v154, v6, v34 op_sel_hi:[0,1,0]
	v_fma_mix_f32 v34, v106, v14, v34 op_sel_hi:[0,1,0]
	v_fma_mix_f32 v34, v66, v30, v34 op_sel_hi:[0,1,0]
	v_mul_f32_e32 v2, v194, v2
	v_fma_mix_f32 v2, v154, v7, v2 op_sel_hi:[0,1,0]
	v_fma_mix_f32 v2, v106, v15, v2 op_sel_hi:[0,1,0]
	v_fma_mix_f32 v2, v66, v31, v2 op_sel_hi:[0,1,0]
	ds_write_b32 v54, v2 offset:512
	v_cvt_f32_f16_sdwa v2, v3 dst_sel:DWORD dst_unused:UNUSED_PAD src0_sel:WORD_1
	ds_write_b32 v69, v34
	v_mul_f32_e32 v2, v194, v2
	v_fma_mix_f32 v2, v154, v7, v2 op_sel:[0,1,0] op_sel_hi:[0,1,0]
	v_fma_mix_f32 v2, v106, v15, v2 op_sel:[0,1,0] op_sel_hi:[0,1,0]
	v_fma_mix_f32 v2, v66, v31, v2 op_sel:[0,1,0] op_sel_hi:[0,1,0]
	ds_write_b32 v51, v2 offset:768
	v_cvt_f32_f16_e32 v2, v4
	v_mul_f32_e32 v2, v194, v2
	v_fma_mix_f32 v2, v154, v8, v2 op_sel_hi:[0,1,0]
	v_fma_mix_f32 v2, v106, v16, v2 op_sel_hi:[0,1,0]
	v_fma_mix_f32 v2, v66, v32, v2 op_sel_hi:[0,1,0]
	ds_write_b32 v69, v2 offset:1024
	v_cvt_f32_f16_sdwa v2, v4 dst_sel:DWORD dst_unused:UNUSED_PAD src0_sel:WORD_1
	v_mul_f32_e32 v2, v194, v2
	v_fma_mix_f32 v2, v154, v8, v2 op_sel:[0,1,0] op_sel_hi:[0,1,0]
	v_fma_mix_f32 v2, v106, v16, v2 op_sel:[0,1,0] op_sel_hi:[0,1,0]
	v_fma_mix_f32 v2, v66, v32, v2 op_sel:[0,1,0] op_sel_hi:[0,1,0]
	ds_write_b32 v50, v2 offset:1280
	v_cvt_f32_f16_e32 v2, v5
	v_mul_f32_e32 v2, v194, v2
	v_fma_mix_f32 v2, v154, v9, v2 op_sel_hi:[0,1,0]
	v_fma_mix_f32 v2, v106, v17, v2 op_sel_hi:[0,1,0]
	v_fma_mix_f32 v2, v66, v33, v2 op_sel_hi:[0,1,0]
	ds_write_b32 v54, v2 offset:1536
	v_cvt_f32_f16_sdwa v2, v5 dst_sel:DWORD dst_unused:UNUSED_PAD src0_sel:WORD_1
	v_mul_f32_e32 v2, v194, v2
	v_fma_mix_f32 v2, v154, v9, v2 op_sel:[0,1,0] op_sel_hi:[0,1,0]
	v_fma_mix_f32 v2, v106, v17, v2 op_sel:[0,1,0] op_sel_hi:[0,1,0]
	v_fma_mix_f32 v2, v66, v33, v2 op_sel:[0,1,0] op_sel_hi:[0,1,0]
	ds_write_b32 v51, v2 offset:1792
	v_cvt_f32_f16_e32 v2, v10
	v_mul_f32_e32 v2, v194, v2
	v_fma_mix_f32 v2, v154, v18, v2 op_sel_hi:[0,1,0]
	v_fma_mix_f32 v2, v106, v22, v2 op_sel_hi:[0,1,0]
	v_fma_mix_f32 v2, v66, v26, v2 op_sel_hi:[0,1,0]
	ds_write_b32 v69, v2 offset:2048
	v_cvt_f32_f16_sdwa v2, v10 dst_sel:DWORD dst_unused:UNUSED_PAD src0_sel:WORD_1
	v_mul_f32_e32 v2, v194, v2
	v_fma_mix_f32 v2, v154, v18, v2 op_sel:[0,1,0] op_sel_hi:[0,1,0]
	v_fma_mix_f32 v2, v106, v22, v2 op_sel:[0,1,0] op_sel_hi:[0,1,0]
	v_fma_mix_f32 v2, v66, v26, v2 op_sel:[0,1,0] op_sel_hi:[0,1,0]
	ds_write_b32 v50, v2 offset:2304
	v_cvt_f32_f16_e32 v2, v11
	v_mul_f32_e32 v2, v194, v2
	v_fma_mix_f32 v2, v154, v19, v2 op_sel_hi:[0,1,0]
	v_fma_mix_f32 v2, v106, v23, v2 op_sel_hi:[0,1,0]
	v_fma_mix_f32 v2, v66, v27, v2 op_sel_hi:[0,1,0]
	ds_write_b32 v54, v2 offset:2560
	v_cvt_f32_f16_sdwa v2, v11 dst_sel:DWORD dst_unused:UNUSED_PAD src0_sel:WORD_1
	v_mul_f32_e32 v2, v194, v2
	v_fma_mix_f32 v2, v154, v19, v2 op_sel:[0,1,0] op_sel_hi:[0,1,0]
	v_fma_mix_f32 v2, v106, v23, v2 op_sel:[0,1,0] op_sel_hi:[0,1,0]
	v_fma_mix_f32 v2, v66, v27, v2 op_sel:[0,1,0] op_sel_hi:[0,1,0]
	ds_write_b32 v51, v2 offset:2816
	v_cvt_f32_f16_e32 v2, v12
	v_mul_f32_e32 v2, v194, v2
	v_fma_mix_f32 v2, v154, v20, v2 op_sel_hi:[0,1,0]
	v_fma_mix_f32 v2, v106, v24, v2 op_sel_hi:[0,1,0]
	v_fma_mix_f32 v2, v66, v28, v2 op_sel_hi:[0,1,0]
	ds_write_b32 v69, v2 offset:3072
	v_cvt_f32_f16_sdwa v2, v12 dst_sel:DWORD dst_unused:UNUSED_PAD src0_sel:WORD_1
	v_mul_f32_e32 v2, v194, v2
	v_fma_mix_f32 v2, v154, v20, v2 op_sel:[0,1,0] op_sel_hi:[0,1,0]
	v_fma_mix_f32 v2, v106, v24, v2 op_sel:[0,1,0] op_sel_hi:[0,1,0]
	v_fma_mix_f32 v2, v66, v28, v2 op_sel:[0,1,0] op_sel_hi:[0,1,0]
	ds_write_b32 v50, v2 offset:3328
	v_cvt_f32_f16_e32 v2, v13
	v_mul_f32_e32 v2, v194, v2
	v_fma_mix_f32 v2, v154, v21, v2 op_sel_hi:[0,1,0]
	v_fma_mix_f32 v2, v106, v25, v2 op_sel_hi:[0,1,0]
	v_fma_mix_f32 v2, v66, v29, v2 op_sel_hi:[0,1,0]
	ds_write_b32 v54, v2 offset:3584
	v_cvt_f32_f16_sdwa v2, v13 dst_sel:DWORD dst_unused:UNUSED_PAD src0_sel:WORD_1
	v_mul_f32_e32 v2, v194, v2
	v_fma_mix_f32 v2, v154, v21, v2 op_sel:[0,1,0] op_sel_hi:[0,1,0]
	v_fma_mix_f32 v2, v106, v25, v2 op_sel:[0,1,0] op_sel_hi:[0,1,0]
	v_fma_mix_f32 v2, v66, v29, v2 op_sel:[0,1,0] op_sel_hi:[0,1,0]
	ds_write_b32 v51, v2 offset:3840
	ds_read_b128 v[2:5], v68
	ds_read_b128 v[6:9], v68 offset:16
	ds_read_b128 v[10:13], v68 offset:32
	ds_read_b128 v[14:17], v68 offset:48
	s_waitcnt lgkmcnt(2)
	v_pk_add_f32 v[4:5], v[4:5], v[8:9]
	v_pk_add_f32 v[2:3], v[2:3], v[6:7]
	s_waitcnt lgkmcnt(0)
	v_pk_add_f32 v[6:7], v[12:13], v[16:17]
	v_pk_add_f32 v[8:9], v[10:11], v[14:15]
	v_pk_add_f32 v[4:5], v[4:5], v[6:7]
	v_pk_add_f32 v[2:3], v[2:3], v[8:9]
	s_nop 0
	v_add_f32_e32 v2, v2, v3
	v_add_f32_e32 v3, v4, v5
	v_add_f32_e32 v2, v2, v3
	ds_write_b32 v67, v2 offset:37120
	s_waitcnt vmcnt(0)
	s_add_u32 s80, s72, 0x20000
	s_addc_u32 s81, s73, 0
	s_add_u32 s90, s72, 0x40000
	s_addc_u32 s91, s73, 0
	s_add_u32 s92, s72, 0x60000
	s_addc_u32 s93, s73, 0
	s_add_u32 s94, s72, 0x80000
	s_addc_u32 s95, s73, 0
	s_add_u32 s96, s72, 0xa0000
	s_addc_u32 s97, s73, 0
	s_add_u32 s98, s72, 0xc0000
	s_addc_u32 s99, s73, 0
	s_add_u32 s64, s72, 0xe0000
	s_addc_u32 s65, s73, 0
	s_add_u32 s0, s0, 0x100
	s_addc_u32 s1, s1, 0
	v_mov_b64_e32 v[62:63], v[216:217]
	v_mov_b64_e32 v[64:65], v[218:219]
	v_mov_b64_e32 v[58:59], v[220:221]
	v_mov_b64_e32 v[60:61], v[222:223]
	v_mov_b64_e32 v[54:55], v[224:225]
	v_mov_b64_e32 v[56:57], v[226:227]
	v_mov_b64_e32 v[50:51], v[228:229]
	v_mov_b64_e32 v[52:53], v[230:231]
	v_mov_b64_e32 v[46:47], v[232:233]
	v_mov_b64_e32 v[48:49], v[234:235]
	v_mov_b64_e32 v[42:43], v[236:237]
	v_mov_b64_e32 v[44:45], v[238:239]
	v_mov_b64_e32 v[38:39], v[240:241]
	v_mov_b64_e32 v[40:41], v[242:243]
	v_mov_b64_e32 v[34:35], v[244:245]
	v_mov_b64_e32 v[36:37], v[246:247]
	s_add_u32 s64, s0, 0x20000
	s_addc_u32 s65, s1, 0
	s_add_u32 s72, s0, 0x40000
	s_addc_u32 s73, s1, 0
	s_add_u32 s80, s0, 0x60000
	s_addc_u32 s81, s1, 0
	s_add_u32 s90, s0, 0x80000
	s_addc_u32 s91, s1, 0
	s_add_u32 s92, s0, 0xa0000
	s_addc_u32 s93, s1, 0
	s_add_u32 s94, s0, 0xc0000
	s_addc_u32 s95, s1, 0
	s_add_u32 s96, s0, 0xe0000
	s_addc_u32 s97, s1, 0
	v_mov_b64_e32 v[30:31], v[156:157]
	v_mov_b64_e32 v[32:33], v[158:159]
	v_mov_b64_e32 v[26:27], v[168:169]
	v_mov_b64_e32 v[28:29], v[170:171]
	v_mov_b64_e32 v[22:23], v[180:181]
	v_mov_b64_e32 v[24:25], v[182:183]
	v_mov_b64_e32 v[18:19], v[184:185]
	v_mov_b64_e32 v[20:21], v[186:187]
	v_mov_b64_e32 v[14:15], v[188:189]
	v_mov_b64_e32 v[16:17], v[190:191]
	v_mov_b64_e32 v[10:11], v[136:137]
	v_mov_b64_e32 v[12:13], v[138:139]
	v_mov_b64_e32 v[6:7], v[148:149]
	v_mov_b64_e32 v[8:9], v[150:151]
	v_mov_b64_e32 v[2:3], v[160:161]
	v_mov_b64_e32 v[4:5], v[162:163]
	s_andn2_b64 vcc, exec, s[70:71]
	s_waitcnt lgkmcnt(0)
	s_barrier
.LBB1_24:
	v_cmp_gt_i32_e32 vcc, s86, v0
	s_and_saveexec_b64 s[0:1], vcc
	s_cbranch_execz .LBB1_1
	s_mov_b32 s22, 0xfe03f81
	v_mul_hi_i32 v1, v0, s22
	v_lshrrev_b32_e32 v66, 31, v1
	v_ashrrev_i32_e32 v1, 3, v1
	v_add_u32_e32 v1, v1, v66
	v_lshl_add_u32 v66, v1, 7, v1
	v_sub_u32_e32 v66, v0, v66
	v_mul_lo_u32 v67, v1, s88
	v_lshl_add_u32 v67, v66, 2, v67
	v_add_u32_e32 v68, 0x9000, v67
	ds_read2_b32 v[68:69], v68 offset1:132
	v_add_u32_e32 v67, 0x9400, v67
	ds_read2_b32 v[70:71], v67 offset0:8 offset1:140
	v_add_u32_e32 v1, s77, v1
	v_lshl_or_b32 v1, v1, 3, s74
	s_waitcnt lgkmcnt(0)
	v_add_f32_e32 v67, v68, v69
	v_mov_b64_e32 v[68:69], s[20:21]
	v_add_f32_e32 v67, v67, v70
	v_add_f32_e32 v70, v67, v71
	v_ashrrev_i32_e32 v67, 31, v66
	v_mad_i64_i32 v[68:69], s[64:65], v1, s85, v[68:69]
	v_lshl_add_u64 v[66:67], v[66:67], 2, v[68:69]
	global_store_dword v[66:67], v70, off
	s_branch .LBB1_1
